# GEMM epilogues: lane^8 exchange by DPP row_ror:8 instead of ds_bpermute (counted lgkmcnt waits re-derived)
# speedup vs baseline: 1.0183x; 1.0110x over previous
; __device__ __forceinline__ float sigm(float x) { return __builtin_amdgcn_rcpf(1.0f + __builtin_amdgcn_exp2f(-1.4426950408889634f * x)); }
; __device__ __forceinline__ u32x4 pack8(const f32x4& v0, const f32x4& v1) { u32x4 w; w.x = cvt_pk_bf16(v0[0], v0[1]); w.y = cvt_pk_bf16(v0[2], v0[3]); w.z = cvt_pk_bf16(v1[0], v1[1]); w.w = cvt_pk_bf16(v1[2], v1[3]); return w; }
; __device__ __forceinline__ u32x4 xor8_16B(u32x4 v) { u32x4 r; r.x = (unsigned)__shfl_xor((int)v.x, 8); r.y = (unsigned)__shfl_xor((int)v.y, 8); r.z = (unsigned)__shfl_xor((int)v.z, 8); r.w = (unsigned)__shfl_xor((int)v.w, 8); return r; }
; __device__ __forceinline__ u32x4 bperm_16B(int src_byte, u32x4 v) { u32x4 r; r.x = (unsigned)__builtin_amdgcn_ds_bpermute(src_byte, (int)v.x); r.y = (unsigned)__builtin_amdgcn_ds_bpermute(src_byte, (int)v.y); r.z = (unsigned)__builtin_amdgcn_ds_bpermute(src_byte, (int)v.z); r.w = (unsigned)__builtin_amdgcn_ds_bpermute(src_byte, (int)v.w); return r; }
; __device__ __forceinline__ void store_rows_bf16(bf16_t* O, size_t ldc, int r0, int c0, int fr, int fq, u32x4 w0, u32x4 w1) {
;     const bool h = fr & 8; const u32x4 recv = xor8_16B(h ? w0 : w1);
;     const u32x4 d1 = h ? recv : w0, d2 = h ? w1 : recv;
;     const int lane = fr + 16 * fq, src = ((lane >> 3) + 8 * ((lane >> 2) & 1) + 16 * (lane & 3)) * 4;
;     const u32x4 e1 = bperm_16B(src, d1), e2 = bperm_16B(src, d2);
;     bf16_t* p = O + (size_t)(r0 + (lane >> 3)) * ldc + c0 + 8 * (lane & 7);
;     *(u32x4*)p = e1; *(u32x4*)(p + 8 * ldc) = e2;
;     __device__ __forceinline__ void operator()(const f32x4 (&acc)[2][2][4][2], const Unit& u, int wr, int wc, int fr, int fq) const {
;     ...
;                 for (int bj = 0; bj < 2; ++bj) { f32x4 v0 = acc[ai][bj][m][0], v1 = acc[ai][bj][m][1];
;                     if (mode == 1) { _Pragma("unroll") for (int i = 0; i < 4; ++i) { v0[i] = sigm(v0[i]); v1[i] = sigm(v1[i]); } }
;                     else { v0 = v0 * sc; v1 = v1 * sc; }
;                     w[bj] = pack8(v0, v1); }
;                 store_rows_bf16(base, (size_t)ldc, u.pm * BM + wr * 64 + ai * HALF + m * 16, colt + wc * 64, fr, fq, w[0], w[1]); }
.LBB0_231:
	v_and_b32_e32 v19, 64, v209
	v_xor_b32_e32 v14, 8, v209
	v_add_u32_e32 v19, 64, v19
	v_cmp_lt_i32_e32 vcc, v14, v19
	v_cvt_pk_bf16_f32 v6, v6, v7
	v_cvt_pk_bf16_f32 v7, v8, v9
	v_cvt_pk_bf16_f32 v8, v10, v11
	v_cvt_pk_bf16_f32 v9, v12, v13
	s_add_i32 s52, s20, s42
	s_nop 0
	v_cndmask_b32_e32 v14, v209, v14, vcc
	v_cndmask_b32_e64 v10, v18, v9, s[4:5]
	v_cndmask_b32_e64 v11, v17, v8, s[4:5]
	v_cndmask_b32_e64 v12, v16, v7, s[4:5]
	v_cndmask_b32_e64 v13, v15, v6, s[4:5]
	v_lshlrev_b32_e32 v14, 2, v14
	v_mov_b32_dpp v10, v10 row_ror:8 row_mask:0xf bank_mask:0xf
	v_mov_b32_dpp v11, v11 row_ror:8 row_mask:0xf bank_mask:0xf
	v_mov_b32_dpp v12, v12 row_ror:8 row_mask:0xf bank_mask:0xf
	v_mov_b32_dpp v13, v13 row_ror:8 row_mask:0xf bank_mask:0xf
	s_ashr_i32 s53, s52, 31
	s_lshl_b64 s[52:53], s[52:53], 1
	s_add_u32 s50, s50, s52
	s_addc_u32 s51, s51, s53
	s_lshl_b32 s20, s81, 8
	s_waitcnt lgkmcnt(0)
	v_cndmask_b32_e64 v18, v10, v18, s[4:5]
	v_cndmask_b32_e64 v17, v11, v17, s[4:5]
	v_cndmask_b32_e64 v16, v12, v16, s[4:5]
	v_cndmask_b32_e64 v15, v13, v15, s[4:5]
	v_cndmask_b32_e64 v19, v9, v10, s[4:5]
	v_cndmask_b32_e64 v20, v8, v11, s[4:5]
	v_cndmask_b32_e64 v11, v7, v12, s[4:5]
	v_cndmask_b32_e64 v10, v6, v13, s[4:5]
	ds_bpermute_b32 v6, v198, v15
	ds_bpermute_b32 v7, v198, v16
	ds_bpermute_b32 v8, v198, v17
	ds_bpermute_b32 v9, v198, v18
	v_add_u32_e32 v15, s20, v199
	ds_bpermute_b32 v10, v198, v10
	ds_bpermute_b32 v11, v198, v11
	ds_bpermute_b32 v12, v198, v20
	ds_bpermute_b32 v13, v198, v19
	v_ashrrev_i32_e32 v16, 31, v15
	v_mul_lo_u32 v18, s48, v16
	v_mul_lo_u32 v19, s49, v15
	v_mad_u64_u32 v[16:17], s[52:53], s48, v15, 0
	v_lshl_add_u64 v[4:5], s[50:51], 0, v[170:171]
	v_add3_u32 v17, v17, v18, v19
	s_lshl_b64 s[50:51], s[48:49], 4
	v_lshl_add_u64 v[16:17], v[16:17], 1, v[4:5]
	s_waitcnt lgkmcnt(0)
	global_store_dwordx4 v[16:17], v[6:9], off
	s_and_b64 vcc, exec, s[2:3]
	s_mov_b64 s[52:53], -1
	v_lshl_add_u64 v[6:7], v[16:17], 0, s[50:51]
	global_store_dwordx4 v[6:7], v[10:13], off
	s_cbranch_vccnz .LBB0_233
	s_nop 0
	v_mov_b32_e32 v10, v2
	v_mov_b32_e32 v11, v2
	v_pk_mul_f32 v[8:9], v[144:145], v[10:11]
	v_pk_mul_f32 v[6:7], v[142:143], v[2:3]
	v_pk_mul_f32 v[12:13], v[140:141], v[10:11]
	v_pk_mul_f32 v[10:11], v[138:139], v[2:3]
	s_mov_b64 s[52:53], 0

; __device__ __forceinline__ float sigm(float x) { return __builtin_amdgcn_rcpf(1.0f + __builtin_amdgcn_exp2f(-1.4426950408889634f * x)); }
; __device__ __forceinline__ u32x4 pack8(const f32x4& v0, const f32x4& v1) { u32x4 w; w.x = cvt_pk_bf16(v0[0], v0[1]); w.y = cvt_pk_bf16(v0[2], v0[3]); w.z = cvt_pk_bf16(v1[0], v1[1]); w.w = cvt_pk_bf16(v1[2], v1[3]); return w; }
; __device__ __forceinline__ u32x4 xor8_16B(u32x4 v) { u32x4 r; r.x = (unsigned)__shfl_xor((int)v.x, 8); r.y = (unsigned)__shfl_xor((int)v.y, 8); r.z = (unsigned)__shfl_xor((int)v.z, 8); r.w = (unsigned)__shfl_xor((int)v.w, 8); return r; }
; __device__ __forceinline__ u32x4 bperm_16B(int src_byte, u32x4 v) { u32x4 r; r.x = (unsigned)__builtin_amdgcn_ds_bpermute(src_byte, (int)v.x); r.y = (unsigned)__builtin_amdgcn_ds_bpermute(src_byte, (int)v.y); r.z = (unsigned)__builtin_amdgcn_ds_bpermute(src_byte, (int)v.z); r.w = (unsigned)__builtin_amdgcn_ds_bpermute(src_byte, (int)v.w); return r; }
; __device__ __forceinline__ void store_rows_bf16(bf16_t* O, size_t ldc, int r0, int c0, int fr, int fq, u32x4 w0, u32x4 w1) {
;     const bool h = fr & 8; const u32x4 recv = xor8_16B(h ? w0 : w1);
;     const u32x4 d1 = h ? recv : w0, d2 = h ? w1 : recv;
;     const int lane = fr + 16 * fq, src = ((lane >> 3) + 8 * ((lane >> 2) & 1) + 16 * (lane & 3)) * 4;
;     const u32x4 e1 = bperm_16B(src, d1), e2 = bperm_16B(src, d2);
;     bf16_t* p = O + (size_t)(r0 + (lane >> 3)) * ldc + c0 + 8 * (lane & 7);
;     *(u32x4*)p = e1; *(u32x4*)(p + 8 * ldc) = e2;
;     __device__ __forceinline__ void operator()(const f32x4 (&acc)[2][2][4][2], const Unit& u, int wr, int wc, int fr, int fq) const {
;     ...
;                 for (int bj = 0; bj < 2; ++bj) { f32x4 v0 = acc[ai][bj][m][0], v1 = acc[ai][bj][m][1];
;                     if (mode == 1) { _Pragma("unroll") for (int i = 0; i < 4; ++i) { v0[i] = sigm(v0[i]); v1[i] = sigm(v1[i]); } }
;                     else { v0 = v0 * sc; v1 = v1 * sc; }
;                     w[bj] = pack8(v0, v1); }
;                 store_rows_bf16(base, (size_t)ldc, u.pm * BM + wr * 64 + ai * HALF + m * 16, colt + wc * 64, fr, fq, w[0], w[1]); }
.LBB0_239:
	v_cvt_pk_bf16_f32 v6, v6, v7
	v_cvt_pk_bf16_f32 v7, v8, v9
	v_cvt_pk_bf16_f32 v8, v10, v11
	v_cvt_pk_bf16_f32 v9, v12, v13
	s_and_b64 vcc, exec, s[2:3]
	v_cndmask_b32_e64 v10, v19, v9, s[4:5]
	v_cndmask_b32_e64 v11, v18, v8, s[4:5]
	v_cndmask_b32_e64 v12, v17, v7, s[4:5]
	v_cndmask_b32_e64 v13, v16, v6, s[4:5]
	v_mov_b32_dpp v10, v10 row_ror:8 row_mask:0xf bank_mask:0xf
	v_mov_b32_dpp v11, v11 row_ror:8 row_mask:0xf bank_mask:0xf
	v_mov_b32_dpp v12, v12 row_ror:8 row_mask:0xf bank_mask:0xf
	v_mov_b32_dpp v13, v13 row_ror:8 row_mask:0xf bank_mask:0xf
	s_waitcnt lgkmcnt(0)
	v_cndmask_b32_e64 v19, v10, v19, s[4:5]
	v_cndmask_b32_e64 v18, v11, v18, s[4:5]
	v_cndmask_b32_e64 v17, v12, v17, s[4:5]
	v_cndmask_b32_e64 v16, v13, v16, s[4:5]
	v_cndmask_b32_e64 v20, v9, v10, s[4:5]
	v_cndmask_b32_e64 v21, v8, v11, s[4:5]
	v_cndmask_b32_e64 v11, v7, v12, s[4:5]
	v_cndmask_b32_e64 v10, v6, v13, s[4:5]
	ds_bpermute_b32 v6, v198, v16
	ds_bpermute_b32 v7, v198, v17
	ds_bpermute_b32 v8, v198, v18
	ds_bpermute_b32 v9, v198, v19
	v_add_u32_e32 v16, s20, v200
	ds_bpermute_b32 v10, v198, v10
	ds_bpermute_b32 v11, v198, v11
	ds_bpermute_b32 v12, v198, v21
	ds_bpermute_b32 v13, v198, v20
	v_ashrrev_i32_e32 v17, 31, v16
	v_mul_lo_u32 v18, s48, v17
	v_mul_lo_u32 v19, s49, v16
	v_mad_u64_u32 v[16:17], s[52:53], s48, v16, 0
	v_add3_u32 v17, v17, v18, v19
	v_lshl_add_u64 v[16:17], v[16:17], 1, v[4:5]
	s_waitcnt lgkmcnt(0)
	global_store_dwordx4 v[16:17], v[6:9], off
	s_mov_b64 s[52:53], -1
	s_nop 0
	v_lshl_add_u64 v[6:7], v[16:17], 0, s[50:51]
	global_store_dwordx4 v[6:7], v[10:13], off
	s_cbranch_vccnz .LBB0_241
	s_nop 0
	v_mov_b32_e32 v10, v2
	v_mov_b32_e32 v11, v2
	v_pk_mul_f32 v[8:9], v[128:129], v[10:11]
	v_pk_mul_f32 v[6:7], v[126:127], v[2:3]
	v_pk_mul_f32 v[12:13], v[124:125], v[10:11]
	v_pk_mul_f32 v[10:11], v[122:123], v[2:3]
	s_mov_b64 s[52:53], 0

; __device__ __forceinline__ float sigm(float x) { return __builtin_amdgcn_rcpf(1.0f + __builtin_amdgcn_exp2f(-1.4426950408889634f * x)); }
; __device__ __forceinline__ u32x4 pack8(const f32x4& v0, const f32x4& v1) { u32x4 w; w.x = cvt_pk_bf16(v0[0], v0[1]); w.y = cvt_pk_bf16(v0[2], v0[3]); w.z = cvt_pk_bf16(v1[0], v1[1]); w.w = cvt_pk_bf16(v1[2], v1[3]); return w; }
; __device__ __forceinline__ u32x4 xor8_16B(u32x4 v) { u32x4 r; r.x = (unsigned)__shfl_xor((int)v.x, 8); r.y = (unsigned)__shfl_xor((int)v.y, 8); r.z = (unsigned)__shfl_xor((int)v.z, 8); r.w = (unsigned)__shfl_xor((int)v.w, 8); return r; }
; __device__ __forceinline__ u32x4 bperm_16B(int src_byte, u32x4 v) { u32x4 r; r.x = (unsigned)__builtin_amdgcn_ds_bpermute(src_byte, (int)v.x); r.y = (unsigned)__builtin_amdgcn_ds_bpermute(src_byte, (int)v.y); r.z = (unsigned)__builtin_amdgcn_ds_bpermute(src_byte, (int)v.z); r.w = (unsigned)__builtin_amdgcn_ds_bpermute(src_byte, (int)v.w); return r; }
; __device__ __forceinline__ void store_rows_bf16(bf16_t* O, size_t ldc, int r0, int c0, int fr, int fq, u32x4 w0, u32x4 w1) {
;     const bool h = fr & 8; const u32x4 recv = xor8_16B(h ? w0 : w1);
;     const u32x4 d1 = h ? recv : w0, d2 = h ? w1 : recv;
;     const int lane = fr + 16 * fq, src = ((lane >> 3) + 8 * ((lane >> 2) & 1) + 16 * (lane & 3)) * 4;
;     const u32x4 e1 = bperm_16B(src, d1), e2 = bperm_16B(src, d2);
;     bf16_t* p = O + (size_t)(r0 + (lane >> 3)) * ldc + c0 + 8 * (lane & 7);
;     *(u32x4*)p = e1; *(u32x4*)(p + 8 * ldc) = e2;
;     __device__ __forceinline__ void operator()(const f32x4 (&acc)[2][2][4][2], const Unit& u, int wr, int wc, int fr, int fq) const {
;     ...
;                 for (int bj = 0; bj < 2; ++bj) { f32x4 v0 = acc[ai][bj][m][0], v1 = acc[ai][bj][m][1];
;                     if (mode == 1) { _Pragma("unroll") for (int i = 0; i < 4; ++i) { v0[i] = sigm(v0[i]); v1[i] = sigm(v1[i]); } }
;                     else { v0 = v0 * sc; v1 = v1 * sc; }
;                     w[bj] = pack8(v0, v1); }
;                 store_rows_bf16(base, (size_t)ldc, u.pm * BM + wr * 64 + ai * HALF + m * 16, colt + wc * 64, fr, fq, w[0], w[1]); }
.LBB0_247:
	v_cvt_pk_bf16_f32 v6, v6, v7
	v_cvt_pk_bf16_f32 v7, v8, v9
	v_cvt_pk_bf16_f32 v8, v10, v11
	v_cvt_pk_bf16_f32 v9, v12, v13
	s_and_b64 vcc, exec, s[2:3]
	v_cndmask_b32_e64 v10, v19, v9, s[4:5]
	v_cndmask_b32_e64 v11, v18, v8, s[4:5]
	v_cndmask_b32_e64 v12, v17, v7, s[4:5]
	v_cndmask_b32_e64 v13, v16, v6, s[4:5]
	v_mov_b32_dpp v10, v10 row_ror:8 row_mask:0xf bank_mask:0xf
	v_mov_b32_dpp v11, v11 row_ror:8 row_mask:0xf bank_mask:0xf
	v_mov_b32_dpp v12, v12 row_ror:8 row_mask:0xf bank_mask:0xf
	v_mov_b32_dpp v13, v13 row_ror:8 row_mask:0xf bank_mask:0xf
	s_waitcnt lgkmcnt(0)
	v_cndmask_b32_e64 v19, v10, v19, s[4:5]
	v_cndmask_b32_e64 v18, v11, v18, s[4:5]
	v_cndmask_b32_e64 v17, v12, v17, s[4:5]
	v_cndmask_b32_e64 v16, v13, v16, s[4:5]
	v_cndmask_b32_e64 v20, v9, v10, s[4:5]
	v_cndmask_b32_e64 v21, v8, v11, s[4:5]
	v_cndmask_b32_e64 v11, v7, v12, s[4:5]
	v_cndmask_b32_e64 v10, v6, v13, s[4:5]
	ds_bpermute_b32 v6, v198, v16
	ds_bpermute_b32 v7, v198, v17
	ds_bpermute_b32 v8, v198, v18
	ds_bpermute_b32 v9, v198, v19
	v_add_u32_e32 v16, s20, v201
	ds_bpermute_b32 v10, v198, v10
	ds_bpermute_b32 v11, v198, v11
	ds_bpermute_b32 v12, v198, v21
	ds_bpermute_b32 v13, v198, v20
	v_ashrrev_i32_e32 v17, 31, v16
	v_mul_lo_u32 v18, s48, v17
	v_mul_lo_u32 v19, s49, v16
	v_mad_u64_u32 v[16:17], s[52:53], s48, v16, 0
	v_add3_u32 v17, v17, v18, v19
	v_lshl_add_u64 v[16:17], v[16:17], 1, v[4:5]
	s_waitcnt lgkmcnt(0)
	global_store_dwordx4 v[16:17], v[6:9], off
	s_mov_b64 s[52:53], -1
	s_nop 0
	v_lshl_add_u64 v[6:7], v[16:17], 0, s[50:51]
	global_store_dwordx4 v[6:7], v[10:13], off
	s_cbranch_vccnz .LBB0_249
	s_nop 0
	v_mov_b32_e32 v10, v2
	v_mov_b32_e32 v11, v2
	v_pk_mul_f32 v[8:9], v[112:113], v[10:11]
	v_pk_mul_f32 v[6:7], v[110:111], v[2:3]
	v_pk_mul_f32 v[12:13], v[108:109], v[10:11]
	v_pk_mul_f32 v[10:11], v[106:107], v[2:3]
	s_mov_b64 s[52:53], 0

; __device__ __forceinline__ float sigm(float x) { return __builtin_amdgcn_rcpf(1.0f + __builtin_amdgcn_exp2f(-1.4426950408889634f * x)); }
; __device__ __forceinline__ u32x4 pack8(const f32x4& v0, const f32x4& v1) { u32x4 w; w.x = cvt_pk_bf16(v0[0], v0[1]); w.y = cvt_pk_bf16(v0[2], v0[3]); w.z = cvt_pk_bf16(v1[0], v1[1]); w.w = cvt_pk_bf16(v1[2], v1[3]); return w; }
; __device__ __forceinline__ u32x4 xor8_16B(u32x4 v) { u32x4 r; r.x = (unsigned)__shfl_xor((int)v.x, 8); r.y = (unsigned)__shfl_xor((int)v.y, 8); r.z = (unsigned)__shfl_xor((int)v.z, 8); r.w = (unsigned)__shfl_xor((int)v.w, 8); return r; }
; __device__ __forceinline__ u32x4 bperm_16B(int src_byte, u32x4 v) { u32x4 r; r.x = (unsigned)__builtin_amdgcn_ds_bpermute(src_byte, (int)v.x); r.y = (unsigned)__builtin_amdgcn_ds_bpermute(src_byte, (int)v.y); r.z = (unsigned)__builtin_amdgcn_ds_bpermute(src_byte, (int)v.z); r.w = (unsigned)__builtin_amdgcn_ds_bpermute(src_byte, (int)v.w); return r; }
; __device__ __forceinline__ void store_rows_bf16(bf16_t* O, size_t ldc, int r0, int c0, int fr, int fq, u32x4 w0, u32x4 w1) {
;     const bool h = fr & 8; const u32x4 recv = xor8_16B(h ? w0 : w1);
;     const u32x4 d1 = h ? recv : w0, d2 = h ? w1 : recv;
;     const int lane = fr + 16 * fq, src = ((lane >> 3) + 8 * ((lane >> 2) & 1) + 16 * (lane & 3)) * 4;
;     const u32x4 e1 = bperm_16B(src, d1), e2 = bperm_16B(src, d2);
;     bf16_t* p = O + (size_t)(r0 + (lane >> 3)) * ldc + c0 + 8 * (lane & 7);
;     *(u32x4*)p = e1; *(u32x4*)(p + 8 * ldc) = e2;
;     __device__ __forceinline__ void operator()(const f32x4 (&acc)[2][2][4][2], const Unit& u, int wr, int wc, int fr, int fq) const {
;     ...
;                 for (int bj = 0; bj < 2; ++bj) { f32x4 v0 = acc[ai][bj][m][0], v1 = acc[ai][bj][m][1];
;                     if (mode == 1) { _Pragma("unroll") for (int i = 0; i < 4; ++i) { v0[i] = sigm(v0[i]); v1[i] = sigm(v1[i]); } }
;                     else { v0 = v0 * sc; v1 = v1 * sc; }
;                     w[bj] = pack8(v0, v1); }
;                 store_rows_bf16(base, (size_t)ldc, u.pm * BM + wr * 64 + ai * HALF + m * 16, colt + wc * 64, fr, fq, w[0], w[1]); }
.LBB0_255:
	v_cvt_pk_bf16_f32 v6, v6, v7
	v_cvt_pk_bf16_f32 v7, v8, v9
	v_cvt_pk_bf16_f32 v8, v10, v11
	v_cvt_pk_bf16_f32 v9, v12, v13
	s_and_b64 vcc, exec, s[2:3]
	v_cndmask_b32_e64 v10, v19, v9, s[4:5]
	v_cndmask_b32_e64 v11, v18, v8, s[4:5]
	v_cndmask_b32_e64 v12, v17, v7, s[4:5]
	v_cndmask_b32_e64 v13, v16, v6, s[4:5]
	v_mov_b32_dpp v10, v10 row_ror:8 row_mask:0xf bank_mask:0xf
	v_mov_b32_dpp v11, v11 row_ror:8 row_mask:0xf bank_mask:0xf
	v_mov_b32_dpp v12, v12 row_ror:8 row_mask:0xf bank_mask:0xf
	v_mov_b32_dpp v13, v13 row_ror:8 row_mask:0xf bank_mask:0xf
	s_waitcnt lgkmcnt(0)
	v_cndmask_b32_e64 v19, v10, v19, s[4:5]
	v_cndmask_b32_e64 v18, v11, v18, s[4:5]
	v_cndmask_b32_e64 v17, v12, v17, s[4:5]
	v_cndmask_b32_e64 v16, v13, v16, s[4:5]
	v_cndmask_b32_e64 v20, v9, v10, s[4:5]
	v_cndmask_b32_e64 v21, v8, v11, s[4:5]
	v_cndmask_b32_e64 v11, v7, v12, s[4:5]
	v_cndmask_b32_e64 v10, v6, v13, s[4:5]
	ds_bpermute_b32 v6, v198, v16
	ds_bpermute_b32 v7, v198, v17
	ds_bpermute_b32 v8, v198, v18
	ds_bpermute_b32 v9, v198, v19
	v_add_u32_e32 v16, s20, v202
	ds_bpermute_b32 v10, v198, v10
	ds_bpermute_b32 v11, v198, v11
	ds_bpermute_b32 v12, v198, v21
	ds_bpermute_b32 v13, v198, v20
	v_ashrrev_i32_e32 v17, 31, v16
	v_mul_lo_u32 v18, s48, v17
	v_mul_lo_u32 v19, s49, v16
	v_mad_u64_u32 v[16:17], s[52:53], s48, v16, 0
	v_add3_u32 v17, v17, v18, v19
	v_lshl_add_u64 v[16:17], v[16:17], 1, v[4:5]
	s_waitcnt lgkmcnt(0)
	global_store_dwordx4 v[16:17], v[6:9], off
	s_mov_b64 s[52:53], -1
	s_nop 0
	v_lshl_add_u64 v[6:7], v[16:17], 0, s[50:51]
	global_store_dwordx4 v[6:7], v[10:13], off
	s_cbranch_vccnz .LBB0_257
	s_nop 0
	v_mov_b32_e32 v10, v2
	v_mov_b32_e32 v11, v2
	v_pk_mul_f32 v[8:9], v[96:97], v[10:11]
	v_pk_mul_f32 v[6:7], v[94:95], v[2:3]
	v_pk_mul_f32 v[12:13], v[92:93], v[10:11]
	v_pk_mul_f32 v[10:11], v[90:91], v[2:3]
	s_mov_b64 s[52:53], 0

; __device__ __forceinline__ float sigm(float x) { return __builtin_amdgcn_rcpf(1.0f + __builtin_amdgcn_exp2f(-1.4426950408889634f * x)); }
; __device__ __forceinline__ u32x4 pack8(const f32x4& v0, const f32x4& v1) { u32x4 w; w.x = cvt_pk_bf16(v0[0], v0[1]); w.y = cvt_pk_bf16(v0[2], v0[3]); w.z = cvt_pk_bf16(v1[0], v1[1]); w.w = cvt_pk_bf16(v1[2], v1[3]); return w; }
; __device__ __forceinline__ u32x4 xor8_16B(u32x4 v) { u32x4 r; r.x = (unsigned)__shfl_xor((int)v.x, 8); r.y = (unsigned)__shfl_xor((int)v.y, 8); r.z = (unsigned)__shfl_xor((int)v.z, 8); r.w = (unsigned)__shfl_xor((int)v.w, 8); return r; }
; __device__ __forceinline__ u32x4 bperm_16B(int src_byte, u32x4 v) { u32x4 r; r.x = (unsigned)__builtin_amdgcn_ds_bpermute(src_byte, (int)v.x); r.y = (unsigned)__builtin_amdgcn_ds_bpermute(src_byte, (int)v.y); r.z = (unsigned)__builtin_amdgcn_ds_bpermute(src_byte, (int)v.z); r.w = (unsigned)__builtin_amdgcn_ds_bpermute(src_byte, (int)v.w); return r; }
; __device__ __forceinline__ void store_rows_bf16(bf16_t* O, size_t ldc, int r0, int c0, int fr, int fq, u32x4 w0, u32x4 w1) {
;     const bool h = fr & 8; const u32x4 recv = xor8_16B(h ? w0 : w1);
;     const u32x4 d1 = h ? recv : w0, d2 = h ? w1 : recv;
;     const int lane = fr + 16 * fq, src = ((lane >> 3) + 8 * ((lane >> 2) & 1) + 16 * (lane & 3)) * 4;
;     const u32x4 e1 = bperm_16B(src, d1), e2 = bperm_16B(src, d2);
;     bf16_t* p = O + (size_t)(r0 + (lane >> 3)) * ldc + c0 + 8 * (lane & 7);
;     *(u32x4*)p = e1; *(u32x4*)(p + 8 * ldc) = e2;
;     __device__ __forceinline__ void operator()(const f32x4 (&acc)[2][2][4][2], const Unit& u, int wr, int wc, int fr, int fq) const {
;     ...
;                 for (int bj = 0; bj < 2; ++bj) { f32x4 v0 = acc[ai][bj][m][0], v1 = acc[ai][bj][m][1];
;                     if (mode == 1) { _Pragma("unroll") for (int i = 0; i < 4; ++i) { v0[i] = sigm(v0[i]); v1[i] = sigm(v1[i]); } }
;                     else { v0 = v0 * sc; v1 = v1 * sc; }
;                     w[bj] = pack8(v0, v1); }
;                 store_rows_bf16(base, (size_t)ldc, u.pm * BM + wr * 64 + ai * HALF + m * 16, colt + wc * 64, fr, fq, w[0], w[1]); }
.LBB0_263:
	v_cvt_pk_bf16_f32 v6, v6, v7
	v_cvt_pk_bf16_f32 v7, v8, v9
	v_cvt_pk_bf16_f32 v8, v10, v11
	v_cvt_pk_bf16_f32 v9, v12, v13
	s_and_b64 vcc, exec, s[2:3]
	v_cndmask_b32_e64 v10, v19, v9, s[4:5]
	v_cndmask_b32_e64 v11, v18, v8, s[4:5]
	v_cndmask_b32_e64 v12, v17, v7, s[4:5]
	v_cndmask_b32_e64 v13, v16, v6, s[4:5]
	v_mov_b32_dpp v10, v10 row_ror:8 row_mask:0xf bank_mask:0xf
	v_mov_b32_dpp v11, v11 row_ror:8 row_mask:0xf bank_mask:0xf
	v_mov_b32_dpp v12, v12 row_ror:8 row_mask:0xf bank_mask:0xf
	v_mov_b32_dpp v13, v13 row_ror:8 row_mask:0xf bank_mask:0xf
	s_waitcnt lgkmcnt(0)
	v_cndmask_b32_e64 v19, v10, v19, s[4:5]
	v_cndmask_b32_e64 v18, v11, v18, s[4:5]
	v_cndmask_b32_e64 v17, v12, v17, s[4:5]
	v_cndmask_b32_e64 v16, v13, v16, s[4:5]
	v_cndmask_b32_e64 v20, v9, v10, s[4:5]
	v_cndmask_b32_e64 v21, v8, v11, s[4:5]
	v_cndmask_b32_e64 v11, v7, v12, s[4:5]
	v_cndmask_b32_e64 v10, v6, v13, s[4:5]
	ds_bpermute_b32 v6, v198, v16
	ds_bpermute_b32 v7, v198, v17
	ds_bpermute_b32 v8, v198, v18
	ds_bpermute_b32 v9, v198, v19
	v_add_u32_e32 v16, 0x80, v15
	ds_bpermute_b32 v10, v198, v10
	ds_bpermute_b32 v11, v198, v11
	ds_bpermute_b32 v12, v198, v21
	ds_bpermute_b32 v13, v198, v20
	v_ashrrev_i32_e32 v17, 31, v16
	v_mul_lo_u32 v18, s48, v17
	v_mul_lo_u32 v19, s49, v16
	v_mad_u64_u32 v[16:17], s[52:53], s48, v16, 0
	v_add3_u32 v17, v17, v18, v19
	v_lshl_add_u64 v[16:17], v[16:17], 1, v[4:5]
	s_waitcnt lgkmcnt(0)
	global_store_dwordx4 v[16:17], v[6:9], off
	s_mov_b64 s[52:53], -1
	s_nop 0
	v_lshl_add_u64 v[6:7], v[16:17], 0, s[50:51]
	global_store_dwordx4 v[6:7], v[10:13], off
	s_cbranch_vccnz .LBB0_265
	s_nop 0
	v_mov_b32_e32 v10, v2
	v_mov_b32_e32 v11, v2
	v_pk_mul_f32 v[8:9], v[80:81], v[10:11]
	v_pk_mul_f32 v[6:7], v[78:79], v[2:3]
	v_pk_mul_f32 v[12:13], v[76:77], v[10:11]
	v_pk_mul_f32 v[10:11], v[74:75], v[2:3]
	s_mov_b64 s[52:53], 0

; __device__ __forceinline__ float sigm(float x) { return __builtin_amdgcn_rcpf(1.0f + __builtin_amdgcn_exp2f(-1.4426950408889634f * x)); }
; __device__ __forceinline__ u32x4 pack8(const f32x4& v0, const f32x4& v1) { u32x4 w; w.x = cvt_pk_bf16(v0[0], v0[1]); w.y = cvt_pk_bf16(v0[2], v0[3]); w.z = cvt_pk_bf16(v1[0], v1[1]); w.w = cvt_pk_bf16(v1[2], v1[3]); return w; }
; __device__ __forceinline__ u32x4 xor8_16B(u32x4 v) { u32x4 r; r.x = (unsigned)__shfl_xor((int)v.x, 8); r.y = (unsigned)__shfl_xor((int)v.y, 8); r.z = (unsigned)__shfl_xor((int)v.z, 8); r.w = (unsigned)__shfl_xor((int)v.w, 8); return r; }
; __device__ __forceinline__ u32x4 bperm_16B(int src_byte, u32x4 v) { u32x4 r; r.x = (unsigned)__builtin_amdgcn_ds_bpermute(src_byte, (int)v.x); r.y = (unsigned)__builtin_amdgcn_ds_bpermute(src_byte, (int)v.y); r.z = (unsigned)__builtin_amdgcn_ds_bpermute(src_byte, (int)v.z); r.w = (unsigned)__builtin_amdgcn_ds_bpermute(src_byte, (int)v.w); return r; }
; __device__ __forceinline__ void store_rows_bf16(bf16_t* O, size_t ldc, int r0, int c0, int fr, int fq, u32x4 w0, u32x4 w1) {
;     const bool h = fr & 8; const u32x4 recv = xor8_16B(h ? w0 : w1);
;     const u32x4 d1 = h ? recv : w0, d2 = h ? w1 : recv;
;     const int lane = fr + 16 * fq, src = ((lane >> 3) + 8 * ((lane >> 2) & 1) + 16 * (lane & 3)) * 4;
;     const u32x4 e1 = bperm_16B(src, d1), e2 = bperm_16B(src, d2);
;     bf16_t* p = O + (size_t)(r0 + (lane >> 3)) * ldc + c0 + 8 * (lane & 7);
;     *(u32x4*)p = e1; *(u32x4*)(p + 8 * ldc) = e2;
;     __device__ __forceinline__ void operator()(const f32x4 (&acc)[2][2][4][2], const Unit& u, int wr, int wc, int fr, int fq) const {
;     ...
;                 for (int bj = 0; bj < 2; ++bj) { f32x4 v0 = acc[ai][bj][m][0], v1 = acc[ai][bj][m][1];
;                     if (mode == 1) { _Pragma("unroll") for (int i = 0; i < 4; ++i) { v0[i] = sigm(v0[i]); v1[i] = sigm(v1[i]); } }
;                     else { v0 = v0 * sc; v1 = v1 * sc; }
;                     w[bj] = pack8(v0, v1); }
;                 store_rows_bf16(base, (size_t)ldc, u.pm * BM + wr * 64 + ai * HALF + m * 16, colt + wc * 64, fr, fq, w[0], w[1]); }
.LBB0_271:
	v_cvt_pk_bf16_f32 v6, v6, v7
	v_cvt_pk_bf16_f32 v7, v8, v9
	v_cvt_pk_bf16_f32 v8, v10, v11
	v_cvt_pk_bf16_f32 v9, v12, v13
	s_and_b64 vcc, exec, s[2:3]
	v_cndmask_b32_e64 v10, v19, v9, s[4:5]
	v_cndmask_b32_e64 v11, v18, v8, s[4:5]
	v_cndmask_b32_e64 v12, v17, v7, s[4:5]
	v_cndmask_b32_e64 v13, v16, v6, s[4:5]
	v_mov_b32_dpp v10, v10 row_ror:8 row_mask:0xf bank_mask:0xf
	v_mov_b32_dpp v11, v11 row_ror:8 row_mask:0xf bank_mask:0xf
	v_mov_b32_dpp v12, v12 row_ror:8 row_mask:0xf bank_mask:0xf
	v_mov_b32_dpp v13, v13 row_ror:8 row_mask:0xf bank_mask:0xf
	s_waitcnt lgkmcnt(0)
	v_cndmask_b32_e64 v19, v10, v19, s[4:5]
	v_cndmask_b32_e64 v18, v11, v18, s[4:5]
	v_cndmask_b32_e64 v17, v12, v17, s[4:5]
	v_cndmask_b32_e64 v16, v13, v16, s[4:5]
	v_cndmask_b32_e64 v20, v9, v10, s[4:5]
	v_cndmask_b32_e64 v21, v8, v11, s[4:5]
	v_cndmask_b32_e64 v11, v7, v12, s[4:5]
	v_cndmask_b32_e64 v10, v6, v13, s[4:5]
	ds_bpermute_b32 v6, v198, v16
	ds_bpermute_b32 v7, v198, v17
	ds_bpermute_b32 v8, v198, v18
	ds_bpermute_b32 v9, v198, v19
	v_add_u32_e32 v16, 0x90, v15
	ds_bpermute_b32 v10, v198, v10
	ds_bpermute_b32 v11, v198, v11
	ds_bpermute_b32 v12, v198, v21
	ds_bpermute_b32 v13, v198, v20
	v_ashrrev_i32_e32 v17, 31, v16
	v_mul_lo_u32 v18, s48, v17
	v_mul_lo_u32 v19, s49, v16
	v_mad_u64_u32 v[16:17], s[52:53], s48, v16, 0
	v_add3_u32 v17, v17, v18, v19
	v_lshl_add_u64 v[16:17], v[16:17], 1, v[4:5]
	s_waitcnt lgkmcnt(0)
	global_store_dwordx4 v[16:17], v[6:9], off
	s_mov_b64 s[52:53], -1
	s_nop 0
	v_lshl_add_u64 v[6:7], v[16:17], 0, s[50:51]
	global_store_dwordx4 v[6:7], v[10:13], off
	s_cbranch_vccnz .LBB0_273
	s_nop 0
	v_mov_b32_e32 v10, v2
	v_mov_b32_e32 v11, v2
	v_pk_mul_f32 v[8:9], v[64:65], v[10:11]
	v_pk_mul_f32 v[6:7], v[62:63], v[2:3]
	v_pk_mul_f32 v[12:13], v[60:61], v[10:11]
	v_pk_mul_f32 v[10:11], v[58:59], v[2:3]
	s_mov_b64 s[52:53], 0

; __device__ __forceinline__ float sigm(float x) { return __builtin_amdgcn_rcpf(1.0f + __builtin_amdgcn_exp2f(-1.4426950408889634f * x)); }
; __device__ __forceinline__ u32x4 pack8(const f32x4& v0, const f32x4& v1) { u32x4 w; w.x = cvt_pk_bf16(v0[0], v0[1]); w.y = cvt_pk_bf16(v0[2], v0[3]); w.z = cvt_pk_bf16(v1[0], v1[1]); w.w = cvt_pk_bf16(v1[2], v1[3]); return w; }
; __device__ __forceinline__ u32x4 xor8_16B(u32x4 v) { u32x4 r; r.x = (unsigned)__shfl_xor((int)v.x, 8); r.y = (unsigned)__shfl_xor((int)v.y, 8); r.z = (unsigned)__shfl_xor((int)v.z, 8); r.w = (unsigned)__shfl_xor((int)v.w, 8); return r; }
; __device__ __forceinline__ u32x4 bperm_16B(int src_byte, u32x4 v) { u32x4 r; r.x = (unsigned)__builtin_amdgcn_ds_bpermute(src_byte, (int)v.x); r.y = (unsigned)__builtin_amdgcn_ds_bpermute(src_byte, (int)v.y); r.z = (unsigned)__builtin_amdgcn_ds_bpermute(src_byte, (int)v.z); r.w = (unsigned)__builtin_amdgcn_ds_bpermute(src_byte, (int)v.w); return r; }
; __device__ __forceinline__ void store_rows_bf16(bf16_t* O, size_t ldc, int r0, int c0, int fr, int fq, u32x4 w0, u32x4 w1) {
;     const bool h = fr & 8; const u32x4 recv = xor8_16B(h ? w0 : w1);
;     const u32x4 d1 = h ? recv : w0, d2 = h ? w1 : recv;
;     const int lane = fr + 16 * fq, src = ((lane >> 3) + 8 * ((lane >> 2) & 1) + 16 * (lane & 3)) * 4;
;     const u32x4 e1 = bperm_16B(src, d1), e2 = bperm_16B(src, d2);
;     bf16_t* p = O + (size_t)(r0 + (lane >> 3)) * ldc + c0 + 8 * (lane & 7);
;     *(u32x4*)p = e1; *(u32x4*)(p + 8 * ldc) = e2;
;     __device__ __forceinline__ void operator()(const f32x4 (&acc)[2][2][4][2], const Unit& u, int wr, int wc, int fr, int fq) const {
;     ...
;                 for (int bj = 0; bj < 2; ++bj) { f32x4 v0 = acc[ai][bj][m][0], v1 = acc[ai][bj][m][1];
;                     if (mode == 1) { _Pragma("unroll") for (int i = 0; i < 4; ++i) { v0[i] = sigm(v0[i]); v1[i] = sigm(v1[i]); } }
;                     else { v0 = v0 * sc; v1 = v1 * sc; }
;                     w[bj] = pack8(v0, v1); }
;                 store_rows_bf16(base, (size_t)ldc, u.pm * BM + wr * 64 + ai * HALF + m * 16, colt + wc * 64, fr, fq, w[0], w[1]); }
.LBB0_279:
	v_cvt_pk_bf16_f32 v6, v6, v7
	v_cvt_pk_bf16_f32 v7, v8, v9
	v_cvt_pk_bf16_f32 v8, v10, v11
	v_cvt_pk_bf16_f32 v9, v12, v13
	s_and_b64 vcc, exec, s[2:3]
	v_cndmask_b32_e64 v10, v19, v9, s[4:5]
	v_cndmask_b32_e64 v11, v18, v8, s[4:5]
	v_cndmask_b32_e64 v12, v17, v7, s[4:5]
	v_cndmask_b32_e64 v13, v16, v6, s[4:5]
	v_mov_b32_dpp v10, v10 row_ror:8 row_mask:0xf bank_mask:0xf
	v_mov_b32_dpp v11, v11 row_ror:8 row_mask:0xf bank_mask:0xf
	v_mov_b32_dpp v12, v12 row_ror:8 row_mask:0xf bank_mask:0xf
	v_mov_b32_dpp v13, v13 row_ror:8 row_mask:0xf bank_mask:0xf
	s_waitcnt lgkmcnt(0)
	v_cndmask_b32_e64 v19, v10, v19, s[4:5]
	v_cndmask_b32_e64 v18, v11, v18, s[4:5]
	v_cndmask_b32_e64 v17, v12, v17, s[4:5]
	v_cndmask_b32_e64 v16, v13, v16, s[4:5]
	v_cndmask_b32_e64 v20, v9, v10, s[4:5]
	v_cndmask_b32_e64 v21, v8, v11, s[4:5]
	v_cndmask_b32_e64 v11, v7, v12, s[4:5]
	v_cndmask_b32_e64 v10, v6, v13, s[4:5]
	ds_bpermute_b32 v6, v198, v16
	ds_bpermute_b32 v7, v198, v17
	ds_bpermute_b32 v8, v198, v18
	ds_bpermute_b32 v9, v198, v19
	v_add_u32_e32 v16, 0xa0, v15
	ds_bpermute_b32 v10, v198, v10
	ds_bpermute_b32 v11, v198, v11
	ds_bpermute_b32 v12, v198, v21
	ds_bpermute_b32 v13, v198, v20
	v_ashrrev_i32_e32 v17, 31, v16
	v_mul_lo_u32 v18, s48, v17
	v_mul_lo_u32 v19, s49, v16
	v_mad_u64_u32 v[16:17], s[52:53], s48, v16, 0
	v_add3_u32 v17, v17, v18, v19
	v_lshl_add_u64 v[16:17], v[16:17], 1, v[4:5]
	s_waitcnt lgkmcnt(0)
	global_store_dwordx4 v[16:17], v[6:9], off
	s_mov_b64 s[52:53], -1
	s_nop 0
	v_lshl_add_u64 v[6:7], v[16:17], 0, s[50:51]
	global_store_dwordx4 v[6:7], v[10:13], off
	s_cbranch_vccnz .LBB0_281
	s_nop 0
	v_mov_b32_e32 v10, v2
	v_mov_b32_e32 v11, v2
	v_pk_mul_f32 v[8:9], v[48:49], v[10:11]
	v_pk_mul_f32 v[6:7], v[46:47], v[2:3]
	v_pk_mul_f32 v[12:13], v[44:45], v[10:11]
	v_pk_mul_f32 v[10:11], v[42:43], v[2:3]
	s_mov_b64 s[52:53], 0

; __device__ __forceinline__ float sigm(float x) { return __builtin_amdgcn_rcpf(1.0f + __builtin_amdgcn_exp2f(-1.4426950408889634f * x)); }
; __device__ __forceinline__ u32x4 pack8(const f32x4& v0, const f32x4& v1) { u32x4 w; w.x = cvt_pk_bf16(v0[0], v0[1]); w.y = cvt_pk_bf16(v0[2], v0[3]); w.z = cvt_pk_bf16(v1[0], v1[1]); w.w = cvt_pk_bf16(v1[2], v1[3]); return w; }
; __device__ __forceinline__ u32x4 xor8_16B(u32x4 v) { u32x4 r; r.x = (unsigned)__shfl_xor((int)v.x, 8); r.y = (unsigned)__shfl_xor((int)v.y, 8); r.z = (unsigned)__shfl_xor((int)v.z, 8); r.w = (unsigned)__shfl_xor((int)v.w, 8); return r; }
; __device__ __forceinline__ void store_rows_bf16(bf16_t* O, size_t ldc, int r0, int c0, int fr, int fq, u32x4 w0, u32x4 w1) {
;     const bool h = fr & 8; const u32x4 recv = xor8_16B(h ? w0 : w1);
;     const u32x4 d1 = h ? recv : w0, d2 = h ? w1 : recv;
;     const int lane = fr + 16 * fq, src = ((lane >> 3) + 8 * ((lane >> 2) & 1) + 16 * (lane & 3)) * 4;
;     const u32x4 e1 = bperm_16B(src, d1), e2 = bperm_16B(src, d2);
;     bf16_t* p = O + (size_t)(r0 + (lane >> 3)) * ldc + c0 + 8 * (lane & 7);
;     *(u32x4*)p = e1; *(u32x4*)(p + 8 * ldc) = e2;
;     __device__ __forceinline__ void operator()(const f32x4 (&acc)[2][2][4][2], const Unit& u, int wr, int wc, int fr, int fq) const {
;     ...
;                         for (int n = 0; n < 2; ++n)
; #pragma unroll
;                             for (int i = 0; i < 4; ++i) p[n] = __builtin_amdgcn_cvt_pk_u8_f32(fmaxf(sigm(acc[ai][bj][m][n][i]) * 255.0f, 1.0f), i, p[n]);
;                         uint2 pv; pv.x = p[0]; pv.y = p[1];
;                         *(uint2*)(g8 + (size_t)(u.pm * BM + wr * 64 + ai * HALF + m * 16 + fr) * 2048 + colt8 + wc * 64 + bj * 32 + 8 * fq) = pv; }
;             return; }
; #pragma unroll
;         for (int ai = 0; ai < 2; ++ai)
; #pragma unroll
;             for (int m = 0; m < 4; ++m) { u32x4 w[2];
; #pragma unroll
;                 for (int bj = 0; bj < 2; ++bj) { f32x4 v0 = acc[ai][bj][m][0], v1 = acc[ai][bj][m][1];
;                     if (mode == 1) { _Pragma("unroll") for (int i = 0; i < 4; ++i) { v0[i] = sigm(v0[i]); v1[i] = sigm(v1[i]); } }
;                     else { v0 = v0 * sc; v1 = v1 * sc; }
;                     w[bj] = pack8(v0, v1); }
;                 store_rows_bf16(base, (size_t)ldc, u.pm * BM + wr * 64 + ai * HALF + m * 16, colt + wc * 64, fr, fq, w[0], w[1]); }
.LBB0_287:
	v_cvt_pk_bf16_f32 v2, v6, v7
	v_cvt_pk_bf16_f32 v3, v10, v11
	v_cvt_pk_bf16_f32 v6, v8, v9
	v_cvt_pk_bf16_f32 v7, v12, v13
	s_nop 0
	v_cndmask_b32_e64 v8, v19, v7, s[4:5]
	v_cndmask_b32_e64 v9, v18, v6, s[4:5]
	v_cndmask_b32_e64 v10, v17, v3, s[4:5]
	v_cndmask_b32_e64 v11, v16, v2, s[4:5]
	v_mov_b32_dpp v8, v8 row_ror:8 row_mask:0xf bank_mask:0xf
	v_mov_b32_dpp v9, v9 row_ror:8 row_mask:0xf bank_mask:0xf
	v_mov_b32_dpp v10, v10 row_ror:8 row_mask:0xf bank_mask:0xf
	v_mov_b32_dpp v11, v11 row_ror:8 row_mask:0xf bank_mask:0xf
	s_waitcnt lgkmcnt(0)
	v_cndmask_b32_e64 v12, v8, v19, s[4:5]
	v_cndmask_b32_e64 v13, v9, v18, s[4:5]
	v_cndmask_b32_e64 v14, v10, v17, s[4:5]
	v_cndmask_b32_e64 v16, v11, v16, s[4:5]
	v_cndmask_b32_e64 v2, v2, v11, s[4:5]
	v_cndmask_b32_e64 v17, v7, v8, s[4:5]
	v_cndmask_b32_e64 v18, v6, v9, s[4:5]
	v_cndmask_b32_e64 v3, v3, v10, s[4:5]
	ds_bpermute_b32 v6, v198, v16
	ds_bpermute_b32 v7, v198, v14
	ds_bpermute_b32 v8, v198, v13
	ds_bpermute_b32 v9, v198, v12
	ds_bpermute_b32 v10, v198, v2
	v_add_u32_e32 v2, 0xb0, v15
	ds_bpermute_b32 v11, v198, v3
	ds_bpermute_b32 v12, v198, v18
	ds_bpermute_b32 v13, v198, v17
	v_ashrrev_i32_e32 v3, 31, v2
	v_mul_lo_u32 v14, s48, v3
	v_mul_lo_u32 v15, s49, v2
	v_mad_u64_u32 v[2:3], s[2:3], s48, v2, 0
	v_add3_u32 v3, v3, v14, v15
	v_lshl_add_u64 v[2:3], v[2:3], 1, v[4:5]
	s_waitcnt lgkmcnt(0)
	global_store_dwordx4 v[2:3], v[6:9], off
	v_lshl_add_u64 v[2:3], v[2:3], 0, s[50:51]
	global_store_dwordx4 v[2:3], v[10:13], off
	s_and_b64 vcc, exec, s[6:7]
	s_mov_b64 s[2:3], -1
	s_cbranch_vccnz .LBB0_195
	s_branch .LBB0_289

; __device__ __forceinline__ u32x4 pack8(const f32x4& v0, const f32x4& v1) { u32x4 w; w.x = cvt_pk_bf16(v0[0], v0[1]); w.y = cvt_pk_bf16(v0[2], v0[3]); w.z = cvt_pk_bf16(v1[0], v1[1]); w.w = cvt_pk_bf16(v1[2], v1[3]); return w; }
; __device__ __forceinline__ u32x4 xor8_16B(u32x4 v) { u32x4 r; r.x = (unsigned)__shfl_xor((int)v.x, 8); r.y = (unsigned)__shfl_xor((int)v.y, 8); r.z = (unsigned)__shfl_xor((int)v.z, 8); r.w = (unsigned)__shfl_xor((int)v.w, 8); return r; }
; __device__ __forceinline__ void store_rows_bf16(bf16_t* O, size_t ldc, int r0, int c0, int fr, int fq, u32x4 w0, u32x4 w1) {
;     const bool h = fr & 8; const u32x4 recv = xor8_16B(h ? w0 : w1);
;     const u32x4 d1 = h ? recv : w0, d2 = h ? w1 : recv;
;     const int lane = fr + 16 * fq, src = ((lane >> 3) + 8 * ((lane >> 2) & 1) + 16 * (lane & 3)) * 4;
;     const u32x4 e1 = bperm_16B(src, d1), e2 = bperm_16B(src, d2);
;     bf16_t* p = O + (size_t)(r0 + (lane >> 3)) * ldc + c0 + 8 * (lane & 7);
;     *(u32x4*)p = e1; *(u32x4*)(p + 8 * ldc) = e2;
;     __device__ __forceinline__ void operator()(const f32x4 (&acc)[2][2][4][2], const Unit& u, int wr, int wc, int fr, int fq) const {
; #pragma unroll
;         for (int ai = 0; ai < 2; ++ai)
; #pragma unroll
;             for (int mp = 0; mp < 2; ++mp) {
;                 uint2 gm[2][2];
; #pragma unroll
;                 for (int mm = 0; mm < 2; ++mm)
; #pragma unroll
;                     for (int bj = 0; bj < 2; ++bj) gm[mm][bj] = *(const uint2*)(gate + (size_t)(u.pm * BM + wr * 64 + fr + ai * HALF + (2 * mp + mm) * 16) * 2048 + 1024 + u.pn * BM + wc * 64 + bj * 32 + 8 * fq);
; #pragma unroll
;                 for (int mm = 0; mm < 2; ++mm) { const int m = 2 * mp + mm; u32x4 w[2];
; #pragma unroll
;                     for (int bj = 0; bj < 2; ++bj) { f32x4 m0, m1; ub4(gm[mm][bj].x, m0); ub4(gm[mm][bj].y, m1); w[bj] = pack8(acc[ai][bj][m][0] * (m0 * (1.0f / 255.0f)), acc[ai][bj][m][1] * (m1 * (1.0f / 255.0f))); }
;                     store_rows_bf16(O, 1024, u.pm * BM + wr * 64 + ai * HALF + m * 16, u.pn * BM + wc * 64, fr, fq, w[0], w[1]); }
.LBB0_987:
	s_lshl_b32 s0, s69, 8
	s_add_i32 s1, s0, s55
	v_or_b32_e32 v150, s1, v1
	v_ashrrev_i32_e32 v151, 31, v150
	s_lshl_b32 s40, s71, 8
	v_lshlrev_b64 v[148:149], 11, v[150:151]
	s_ashr_i32 s41, s40, 31
	v_lshl_add_u64 v[148:149], s[24:25], 0, v[148:149]
	v_lshl_add_u64 v[148:149], v[148:149], 0, s[40:41]
	v_lshl_add_u64 v[148:149], v[148:149], 0, s[18:19]
	v_lshl_add_u64 v[148:149], v[148:149], 0, v[140:141]
	global_load_dwordx2 v[152:153], v[148:149], off offset:1024
	global_load_dwordx2 v[154:155], v[148:149], off offset:1056
	v_or_b32_e32 v156, 16, v150
	v_ashrrev_i32_e32 v157, 31, v156
	v_lshlrev_b64 v[156:157], 11, v[156:157]
	v_lshl_add_u64 v[156:157], s[24:25], 0, v[156:157]
	v_lshl_add_u64 v[156:157], v[156:157], 0, s[40:41]
	v_lshl_add_u64 v[156:157], v[156:157], 0, s[18:19]
	v_lshl_add_u64 v[156:157], v[156:157], 0, v[140:141]
	global_load_dwordx2 v[158:159], v[156:157], off offset:1024
	v_and_b32_e32 v148, 64, v177
	global_load_dwordx2 v[156:157], v[156:157], off offset:1056
	v_xor_b32_e32 v149, 8, v177
	v_add_u32_e32 v151, 64, v148
	v_cmp_lt_i32_e32 vcc, v149, v151
	v_or_b32_e32 v148, s1, v174
	s_or_b32 s0, s40, s18
	v_cndmask_b32_e32 v149, v177, v149, vcc
	v_lshlrev_b32_e32 v151, 2, v149
	v_ashrrev_i32_e32 v149, 31, v148
	s_ashr_i32 s1, s0, 31
	v_lshlrev_b64 v[160:161], 11, v[148:149]
	s_lshl_b64 s[38:39], s[0:1], 1
	v_lshl_add_u64 v[160:161], s[22:23], 0, v[160:161]
	v_lshl_add_u64 v[160:161], v[160:161], 0, s[38:39]
	s_waitcnt vmcnt(0)
	v_cvt_f32_ubyte0_e32 v162, v152
	v_cvt_f32_ubyte1_e32 v163, v152
	v_cvt_f32_ubyte2_e32 v164, v152
	v_cvt_f32_ubyte3_e32 v165, v152
	v_cvt_f32_ubyte0_e32 v166, v153
	v_cvt_f32_ubyte1_e32 v167, v153
	v_cvt_f32_ubyte2_e32 v152, v153
	v_cvt_f32_ubyte3_e32 v153, v153
	v_cvt_f32_ubyte0_e32 v168, v154
	v_cvt_f32_ubyte1_e32 v169, v154
	v_cvt_f32_ubyte2_e32 v170, v154
	v_cvt_f32_ubyte3_e32 v171, v154
	v_cvt_f32_ubyte0_e32 v178, v155
	v_cvt_f32_ubyte1_e32 v179, v155
	v_cvt_f32_ubyte2_e32 v154, v155
	v_cvt_f32_ubyte3_e32 v155, v155
	v_pk_mul_f32 v[162:163], v[162:163], s[34:35] op_sel_hi:[1,0]
	v_pk_mul_f32 v[164:165], v[164:165], s[34:35] op_sel_hi:[1,0]
	v_pk_mul_f32 v[152:153], v[152:153], s[34:35] op_sel_hi:[1,0]
	v_pk_mul_f32 v[168:169], v[168:169], s[34:35] op_sel_hi:[1,0]
	v_pk_mul_f32 v[170:171], v[170:171], s[34:35] op_sel_hi:[1,0]
	v_pk_mul_f32 v[178:179], v[178:179], s[34:35] op_sel_hi:[1,0]
	v_pk_mul_f32 v[154:155], v[154:155], s[34:35] op_sel_hi:[1,0]
	v_pk_mul_f32 v[166:167], v[166:167], s[34:35] op_sel_hi:[1,0]
	v_pk_mul_f32 v[128:129], v[128:129], v[164:165]
	v_pk_mul_f32 v[126:127], v[126:127], v[162:163]
	v_pk_mul_f32 v[124:125], v[124:125], v[152:153]
	v_pk_mul_f32 v[120:121], v[120:121], v[170:171]
	v_pk_mul_f32 v[118:119], v[118:119], v[168:169]
	v_pk_mul_f32 v[116:117], v[116:117], v[154:155]
	v_pk_mul_f32 v[114:115], v[114:115], v[178:179]
	v_pk_mul_f32 v[122:123], v[122:123], v[166:167]
	v_cvt_pk_bf16_f32 v126, v126, v127
	v_cvt_pk_bf16_f32 v127, v128, v129
	s_nop 0
	v_cvt_pk_bf16_f32 v128, v122, v123
	v_cvt_pk_bf16_f32 v124, v124, v125
	v_cvt_pk_bf16_f32 v118, v118, v119
	v_cvt_pk_bf16_f32 v119, v120, v121
	v_cvt_pk_bf16_f32 v114, v114, v115
	v_cvt_pk_bf16_f32 v115, v116, v117
	v_lshl_add_u64 v[122:123], v[160:161], 0, v[138:139]
	v_cndmask_b32_e64 v116, v124, v115, s[4:5]
	v_cndmask_b32_e64 v117, v128, v114, s[4:5]
	v_cndmask_b32_e64 v120, v127, v119, s[4:5]
	v_cndmask_b32_e64 v121, v126, v118, s[4:5]
	v_mov_b32_dpp v116, v116 row_ror:8 row_mask:0xf bank_mask:0xf
	v_mov_b32_dpp v117, v117 row_ror:8 row_mask:0xf bank_mask:0xf
	v_mov_b32_dpp v120, v120 row_ror:8 row_mask:0xf bank_mask:0xf
	v_mov_b32_dpp v121, v121 row_ror:8 row_mask:0xf bank_mask:0xf
	s_waitcnt lgkmcnt(0)
	v_cndmask_b32_e64 v124, v116, v124, s[4:5]
	v_cndmask_b32_e64 v125, v117, v128, s[4:5]
	v_cndmask_b32_e64 v127, v120, v127, s[4:5]
	v_cndmask_b32_e64 v126, v121, v126, s[4:5]
	v_cndmask_b32_e64 v128, v115, v116, s[4:5]
	v_cndmask_b32_e64 v129, v114, v117, s[4:5]
	v_cndmask_b32_e64 v119, v119, v120, s[4:5]
	v_cndmask_b32_e64 v118, v118, v121, s[4:5]
	ds_bpermute_b32 v114, v175, v126
	ds_bpermute_b32 v115, v175, v127
	ds_bpermute_b32 v116, v175, v125
	ds_bpermute_b32 v117, v175, v124
	ds_bpermute_b32 v118, v175, v118
	ds_bpermute_b32 v119, v175, v119
	ds_bpermute_b32 v120, v175, v129
	ds_bpermute_b32 v121, v175, v128
	v_add_co_u32_e32 v124, vcc, s51, v122
	s_nop 1
	v_addc_co_u32_e32 v125, vcc, 0, v123, vcc
	s_waitcnt lgkmcnt(4)
	global_store_dwordx4 v[122:123], v[114:117], off
	s_waitcnt lgkmcnt(0)
	global_store_dwordx4 v[124:125], v[118:121], off
	v_cvt_f32_ubyte0_e32 v114, v158
	v_cvt_f32_ubyte1_e32 v115, v158
	v_cvt_f32_ubyte2_e32 v116, v158
	v_cvt_f32_ubyte3_e32 v117, v158
	v_cvt_f32_ubyte0_e32 v118, v159
	v_cvt_f32_ubyte1_e32 v119, v159
	v_cvt_f32_ubyte2_e32 v120, v159
	v_cvt_f32_ubyte3_e32 v121, v159
	v_pk_mul_f32 v[114:115], v[114:115], s[34:35] op_sel_hi:[1,0]
	v_pk_mul_f32 v[116:117], v[116:117], s[34:35] op_sel_hi:[1,0]
	v_pk_mul_f32 v[110:111], v[110:111], v[114:115]
	v_pk_mul_f32 v[112:113], v[112:113], v[116:117]
	v_pk_mul_f32 v[114:115], v[118:119], s[34:35] op_sel_hi:[1,0]
	v_pk_mul_f32 v[116:117], v[120:121], s[34:35] op_sel_hi:[1,0]
	v_pk_mul_f32 v[106:107], v[106:107], v[114:115]
	v_pk_mul_f32 v[108:109], v[108:109], v[116:117]
	v_cvt_pk_bf16_f32 v114, v110, v111
	v_cvt_pk_bf16_f32 v115, v112, v113
	v_cvt_pk_bf16_f32 v116, v106, v107
	v_cvt_f32_ubyte0_e32 v106, v156
	v_cvt_pk_bf16_f32 v117, v108, v109
	v_cvt_f32_ubyte1_e32 v107, v156
	v_cvt_f32_ubyte2_e32 v108, v156
	v_cvt_f32_ubyte3_e32 v109, v156
	v_cvt_f32_ubyte0_e32 v110, v157
	v_cvt_f32_ubyte1_e32 v111, v157
	v_cvt_f32_ubyte2_e32 v112, v157
	v_cvt_f32_ubyte3_e32 v113, v157
	v_pk_mul_f32 v[106:107], v[106:107], s[34:35] op_sel_hi:[1,0]
	v_pk_mul_f32 v[108:109], v[108:109], s[34:35] op_sel_hi:[1,0]
	v_pk_mul_f32 v[102:103], v[102:103], v[106:107]
	v_pk_mul_f32 v[104:105], v[104:105], v[108:109]
	v_pk_mul_f32 v[106:107], v[110:111], s[34:35] op_sel_hi:[1,0]
	v_pk_mul_f32 v[108:109], v[112:113], s[34:35] op_sel_hi:[1,0]
	v_pk_mul_f32 v[98:99], v[98:99], v[106:107]
	v_pk_mul_f32 v[100:101], v[100:101], v[108:109]
	v_cvt_pk_bf16_f32 v102, v102, v103
	v_cvt_pk_bf16_f32 v103, v104, v105
	v_cvt_pk_bf16_f32 v98, v98, v99
	s_nop 0
	v_cvt_pk_bf16_f32 v99, v100, v101
	v_cndmask_b32_e64 v101, v116, v98, s[4:5]
	v_cndmask_b32_e64 v100, v117, v99, s[4:5]
	v_cndmask_b32_e64 v104, v115, v103, s[4:5]
	v_cndmask_b32_e64 v105, v114, v102, s[4:5]
	v_mov_b32_dpp v100, v100 row_ror:8 row_mask:0xf bank_mask:0xf
	v_mov_b32_dpp v101, v101 row_ror:8 row_mask:0xf bank_mask:0xf
	v_mov_b32_dpp v104, v104 row_ror:8 row_mask:0xf bank_mask:0xf
	v_mov_b32_dpp v105, v105 row_ror:8 row_mask:0xf bank_mask:0xf
	s_waitcnt lgkmcnt(0)
; __device__ __forceinline__ u32x4 pack8(const f32x4& v0, const f32x4& v1) { u32x4 w; w.x = cvt_pk_bf16(v0[0], v0[1]); w.y = cvt_pk_bf16(v0[2], v0[3]); w.z = cvt_pk_bf16(v1[0], v1[1]); w.w = cvt_pk_bf16(v1[2], v1[3]); return w; }
; __device__ __forceinline__ u32x4 xor8_16B(u32x4 v) { u32x4 r; r.x = (unsigned)__shfl_xor((int)v.x, 8); r.y = (unsigned)__shfl_xor((int)v.y, 8); r.z = (unsigned)__shfl_xor((int)v.z, 8); r.w = (unsigned)__shfl_xor((int)v.w, 8); return r; }
; __device__ __forceinline__ void store_rows_bf16(bf16_t* O, size_t ldc, int r0, int c0, int fr, int fq, u32x4 w0, u32x4 w1) {
;     const bool h = fr & 8; const u32x4 recv = xor8_16B(h ? w0 : w1);
;     const u32x4 d1 = h ? recv : w0, d2 = h ? w1 : recv;
;     const int lane = fr + 16 * fq, src = ((lane >> 3) + 8 * ((lane >> 2) & 1) + 16 * (lane & 3)) * 4;
;     const u32x4 e1 = bperm_16B(src, d1), e2 = bperm_16B(src, d2);
;     bf16_t* p = O + (size_t)(r0 + (lane >> 3)) * ldc + c0 + 8 * (lane & 7);
;     *(u32x4*)p = e1; *(u32x4*)(p + 8 * ldc) = e2;
;     __device__ __forceinline__ void operator()(const f32x4 (&acc)[2][2][4][2], const Unit& u, int wr, int wc, int fr, int fq) const {
; #pragma unroll
;         for (int ai = 0; ai < 2; ++ai)
; #pragma unroll
;             for (int mp = 0; mp < 2; ++mp) {
;                 uint2 gm[2][2];
; #pragma unroll
;                 for (int mm = 0; mm < 2; ++mm)
; #pragma unroll
;                     for (int bj = 0; bj < 2; ++bj) gm[mm][bj] = *(const uint2*)(gate + (size_t)(u.pm * BM + wr * 64 + fr + ai * HALF + (2 * mp + mm) * 16) * 2048 + 1024 + u.pn * BM + wc * 64 + bj * 32 + 8 * fq);
; #pragma unroll
;                 for (int mm = 0; mm < 2; ++mm) { const int m = 2 * mp + mm; u32x4 w[2];
; #pragma unroll
;                     for (int bj = 0; bj < 2; ++bj) { f32x4 m0, m1; ub4(gm[mm][bj].x, m0); ub4(gm[mm][bj].y, m1); w[bj] = pack8(acc[ai][bj][m][0] * (m0 * (1.0f / 255.0f)), acc[ai][bj][m][1] * (m1 * (1.0f / 255.0f))); }
;                     store_rows_bf16(O, 1024, u.pm * BM + wr * 64 + ai * HALF + m * 16, u.pn * BM + wc * 64, fr, fq, w[0], w[1]); }
	v_cndmask_b32_e64 v106, v100, v117, s[4:5]
	s_waitcnt lgkmcnt(0)
	v_cndmask_b32_e64 v107, v101, v116, s[4:5]
	s_waitcnt lgkmcnt(0)
	v_cndmask_b32_e64 v108, v104, v115, s[4:5]
	s_waitcnt lgkmcnt(0)
	v_cndmask_b32_e64 v109, v105, v114, s[4:5]
	v_cndmask_b32_e64 v111, v98, v101, s[4:5]
	ds_bpermute_b32 v101, v175, v106
	v_or_b32_e32 v106, 16, v148
	v_cndmask_b32_e64 v110, v99, v100, s[4:5]
	ds_bpermute_b32 v98, v175, v109
	ds_bpermute_b32 v99, v175, v108
	ds_bpermute_b32 v100, v175, v107
	v_ashrrev_i32_e32 v107, 31, v106
	v_cndmask_b32_e64 v103, v103, v104, s[4:5]
	v_cndmask_b32_e64 v102, v102, v105, s[4:5]
	v_lshlrev_b64 v[106:107], 11, v[106:107]
	ds_bpermute_b32 v102, v175, v102
	ds_bpermute_b32 v103, v175, v103
	ds_bpermute_b32 v104, v175, v111
	ds_bpermute_b32 v105, v175, v110
	v_lshl_add_u64 v[106:107], s[22:23], 0, v[106:107]
	v_lshl_add_u64 v[106:107], v[106:107], 0, s[38:39]
	v_lshl_add_u64 v[106:107], v[106:107], 0, v[138:139]
	s_waitcnt lgkmcnt(4)
	global_store_dwordx4 v[106:107], v[98:101], off
	s_nop 1
	v_add_co_u32_e32 v98, vcc, s51, v106
	s_nop 1
	v_addc_co_u32_e32 v99, vcc, 0, v107, vcc
	s_waitcnt lgkmcnt(0)
	global_store_dwordx4 v[98:99], v[102:105], off
	v_or_b32_e32 v98, 32, v150
	v_ashrrev_i32_e32 v99, 31, v98
	v_lshlrev_b64 v[98:99], 11, v[98:99]
	v_lshl_add_u64 v[98:99], s[24:25], 0, v[98:99]
	v_lshl_add_u64 v[98:99], v[98:99], 0, s[40:41]
	v_lshl_add_u64 v[98:99], v[98:99], 0, s[18:19]
	v_lshl_add_u64 v[98:99], v[98:99], 0, v[140:141]
	global_load_dwordx2 v[100:101], v[98:99], off offset:1024
	s_nop 0
	global_load_dwordx2 v[98:99], v[98:99], off offset:1056
	v_or_b32_e32 v102, 48, v150
	v_ashrrev_i32_e32 v103, 31, v102
	v_lshlrev_b64 v[102:103], 11, v[102:103]
	v_lshl_add_u64 v[102:103], s[24:25], 0, v[102:103]
	v_lshl_add_u64 v[102:103], v[102:103], 0, s[40:41]
	v_lshl_add_u64 v[102:103], v[102:103], 0, s[18:19]
	v_lshl_add_u64 v[102:103], v[102:103], 0, v[140:141]
	global_load_dwordx2 v[104:105], v[102:103], off offset:1024
	s_nop 0
	global_load_dwordx2 v[102:103], v[102:103], off offset:1056
	s_waitcnt vmcnt(3)
	v_cvt_f32_ubyte0_e32 v106, v100
	v_cvt_f32_ubyte1_e32 v107, v100
	v_cvt_f32_ubyte2_e32 v108, v100
	v_cvt_f32_ubyte3_e32 v109, v100
	v_cvt_f32_ubyte0_e32 v110, v101
	v_cvt_f32_ubyte1_e32 v111, v101
	v_cvt_f32_ubyte2_e32 v100, v101
	v_cvt_f32_ubyte3_e32 v101, v101
	v_pk_mul_f32 v[106:107], v[106:107], s[34:35] op_sel_hi:[1,0]
	v_pk_mul_f32 v[100:101], v[100:101], s[34:35] op_sel_hi:[1,0]
	v_pk_mul_f32 v[94:95], v[94:95], v[106:107]
	v_pk_mul_f32 v[106:107], v[110:111], s[34:35] op_sel_hi:[1,0]
	v_pk_mul_f32 v[108:109], v[108:109], s[34:35] op_sel_hi:[1,0]
	v_pk_mul_f32 v[92:93], v[92:93], v[100:101]
	v_pk_mul_f32 v[90:91], v[90:91], v[106:107]
	v_pk_mul_f32 v[96:97], v[96:97], v[108:109]
	v_cvt_pk_bf16_f32 v100, v94, v95
	s_waitcnt vmcnt(2)
	v_cvt_f32_ubyte0_e32 v94, v99
	v_cvt_pk_bf16_f32 v101, v96, v97
	v_cvt_pk_bf16_f32 v106, v90, v91
	v_cvt_pk_bf16_f32 v107, v92, v93
	v_cvt_f32_ubyte0_e32 v90, v98
	v_cvt_f32_ubyte1_e32 v91, v98
	v_cvt_f32_ubyte2_e32 v92, v98
	v_cvt_f32_ubyte3_e32 v93, v98
	v_cvt_f32_ubyte1_e32 v95, v99
	v_cvt_f32_ubyte2_e32 v96, v99
	v_cvt_f32_ubyte3_e32 v97, v99
	v_pk_mul_f32 v[90:91], v[90:91], s[34:35] op_sel_hi:[1,0]
	v_pk_mul_f32 v[92:93], v[92:93], s[34:35] op_sel_hi:[1,0]
	v_pk_mul_f32 v[86:87], v[86:87], v[90:91]
	v_pk_mul_f32 v[88:89], v[88:89], v[92:93]
	v_pk_mul_f32 v[90:91], v[94:95], s[34:35] op_sel_hi:[1,0]
	v_pk_mul_f32 v[92:93], v[96:97], s[34:35] op_sel_hi:[1,0]
	v_pk_mul_f32 v[82:83], v[82:83], v[90:91]
	v_pk_mul_f32 v[84:85], v[84:85], v[92:93]
	v_cvt_pk_bf16_f32 v86, v86, v87
	v_cvt_pk_bf16_f32 v87, v88, v89
	v_cvt_pk_bf16_f32 v82, v82, v83
	s_nop 0
	v_cvt_pk_bf16_f32 v83, v84, v85
	v_cndmask_b32_e64 v85, v106, v82, s[4:5]
	v_cndmask_b32_e64 v84, v107, v83, s[4:5]
	v_cndmask_b32_e64 v88, v101, v87, s[4:5]
	v_cndmask_b32_e64 v89, v100, v86, s[4:5]
	v_mov_b32_dpp v84, v84 row_ror:8 row_mask:0xf bank_mask:0xf
	v_mov_b32_dpp v85, v85 row_ror:8 row_mask:0xf bank_mask:0xf
	v_mov_b32_dpp v88, v88 row_ror:8 row_mask:0xf bank_mask:0xf
	v_mov_b32_dpp v89, v89 row_ror:8 row_mask:0xf bank_mask:0xf
	s_waitcnt lgkmcnt(0)
	v_cndmask_b32_e64 v90, v84, v107, s[4:5]
	s_waitcnt lgkmcnt(0)
	v_cndmask_b32_e64 v91, v85, v106, s[4:5]
	s_waitcnt lgkmcnt(0)
	v_cndmask_b32_e64 v92, v88, v101, s[4:5]
	s_waitcnt lgkmcnt(0)
	v_cndmask_b32_e64 v93, v89, v100, s[4:5]
	v_cndmask_b32_e64 v95, v82, v85, s[4:5]
	ds_bpermute_b32 v85, v175, v90
	v_or_b32_e32 v90, 32, v148
	v_cndmask_b32_e64 v94, v83, v84, s[4:5]
	ds_bpermute_b32 v82, v175, v93
	ds_bpermute_b32 v83, v175, v92
	ds_bpermute_b32 v84, v175, v91
	v_ashrrev_i32_e32 v91, 31, v90
	v_cndmask_b32_e64 v87, v87, v88, s[4:5]
	v_cndmask_b32_e64 v86, v86, v89, s[4:5]
	v_lshlrev_b64 v[90:91], 11, v[90:91]
	ds_bpermute_b32 v86, v175, v86
	ds_bpermute_b32 v87, v175, v87
	ds_bpermute_b32 v88, v175, v95
	ds_bpermute_b32 v89, v175, v94
	v_lshl_add_u64 v[90:91], s[22:23], 0, v[90:91]
	v_lshl_add_u64 v[90:91], v[90:91], 0, s[38:39]
	v_lshl_add_u64 v[90:91], v[90:91], 0, v[138:139]
	s_waitcnt lgkmcnt(4)
	global_store_dwordx4 v[90:91], v[82:85], off
	s_nop 1
	v_add_co_u32_e32 v82, vcc, s51, v90
	s_waitcnt vmcnt(2)
	v_cvt_f32_ubyte2_e32 v84, v104
	v_addc_co_u32_e32 v83, vcc, 0, v91, vcc
	s_waitcnt lgkmcnt(0)
; __device__ __forceinline__ u32x4 pack8(const f32x4& v0, const f32x4& v1) { u32x4 w; w.x = cvt_pk_bf16(v0[0], v0[1]); w.y = cvt_pk_bf16(v0[2], v0[3]); w.z = cvt_pk_bf16(v1[0], v1[1]); w.w = cvt_pk_bf16(v1[2], v1[3]); return w; }
; __device__ __forceinline__ u32x4 xor8_16B(u32x4 v) { u32x4 r; r.x = (unsigned)__shfl_xor((int)v.x, 8); r.y = (unsigned)__shfl_xor((int)v.y, 8); r.z = (unsigned)__shfl_xor((int)v.z, 8); r.w = (unsigned)__shfl_xor((int)v.w, 8); return r; }
; __device__ __forceinline__ void store_rows_bf16(bf16_t* O, size_t ldc, int r0, int c0, int fr, int fq, u32x4 w0, u32x4 w1) {
;     const bool h = fr & 8; const u32x4 recv = xor8_16B(h ? w0 : w1);
;     const u32x4 d1 = h ? recv : w0, d2 = h ? w1 : recv;
;     const int lane = fr + 16 * fq, src = ((lane >> 3) + 8 * ((lane >> 2) & 1) + 16 * (lane & 3)) * 4;
;     const u32x4 e1 = bperm_16B(src, d1), e2 = bperm_16B(src, d2);
;     bf16_t* p = O + (size_t)(r0 + (lane >> 3)) * ldc + c0 + 8 * (lane & 7);
;     *(u32x4*)p = e1; *(u32x4*)(p + 8 * ldc) = e2;
;     __device__ __forceinline__ void operator()(const f32x4 (&acc)[2][2][4][2], const Unit& u, int wr, int wc, int fr, int fq) const {
; #pragma unroll
;         for (int ai = 0; ai < 2; ++ai)
; #pragma unroll
;             for (int mp = 0; mp < 2; ++mp) {
;                 uint2 gm[2][2];
; #pragma unroll
;                 for (int mm = 0; mm < 2; ++mm)
; #pragma unroll
;                     for (int bj = 0; bj < 2; ++bj) gm[mm][bj] = *(const uint2*)(gate + (size_t)(u.pm * BM + wr * 64 + fr + ai * HALF + (2 * mp + mm) * 16) * 2048 + 1024 + u.pn * BM + wc * 64 + bj * 32 + 8 * fq);
; #pragma unroll
;                 for (int mm = 0; mm < 2; ++mm) { const int m = 2 * mp + mm; u32x4 w[2];
; #pragma unroll
;                     for (int bj = 0; bj < 2; ++bj) { f32x4 m0, m1; ub4(gm[mm][bj].x, m0); ub4(gm[mm][bj].y, m1); w[bj] = pack8(acc[ai][bj][m][0] * (m0 * (1.0f / 255.0f)), acc[ai][bj][m][1] * (m1 * (1.0f / 255.0f))); }
;                     store_rows_bf16(O, 1024, u.pm * BM + wr * 64 + ai * HALF + m * 16, u.pn * BM + wc * 64, fr, fq, w[0], w[1]); }
	global_store_dwordx4 v[82:83], v[86:89], off
	v_cvt_f32_ubyte0_e32 v82, v104
	v_cvt_f32_ubyte1_e32 v83, v104
	v_cvt_f32_ubyte3_e32 v85, v104
	v_cvt_f32_ubyte0_e32 v86, v105
	v_cvt_f32_ubyte1_e32 v87, v105
	v_cvt_f32_ubyte2_e32 v88, v105
	v_cvt_f32_ubyte3_e32 v89, v105
	v_pk_mul_f32 v[82:83], v[82:83], s[34:35] op_sel_hi:[1,0]
	v_pk_mul_f32 v[84:85], v[84:85], s[34:35] op_sel_hi:[1,0]
	v_pk_mul_f32 v[78:79], v[78:79], v[82:83]
	v_pk_mul_f32 v[80:81], v[80:81], v[84:85]
	v_pk_mul_f32 v[82:83], v[86:87], s[34:35] op_sel_hi:[1,0]
	v_pk_mul_f32 v[84:85], v[88:89], s[34:35] op_sel_hi:[1,0]
	v_pk_mul_f32 v[74:75], v[74:75], v[82:83]
	v_pk_mul_f32 v[76:77], v[76:77], v[84:85]
	v_cvt_pk_bf16_f32 v82, v78, v79
	v_cvt_pk_bf16_f32 v83, v80, v81
	v_cvt_pk_bf16_f32 v84, v74, v75
	s_waitcnt vmcnt(2)
	v_cvt_f32_ubyte0_e32 v74, v102
	v_cvt_pk_bf16_f32 v85, v76, v77
	v_cvt_f32_ubyte1_e32 v75, v102
	v_cvt_f32_ubyte2_e32 v76, v102
	v_cvt_f32_ubyte3_e32 v77, v102
	v_cvt_f32_ubyte0_e32 v78, v103
	v_cvt_f32_ubyte1_e32 v79, v103
	v_cvt_f32_ubyte2_e32 v80, v103
	v_cvt_f32_ubyte3_e32 v81, v103
	v_pk_mul_f32 v[74:75], v[74:75], s[34:35] op_sel_hi:[1,0]
	v_pk_mul_f32 v[76:77], v[76:77], s[34:35] op_sel_hi:[1,0]
	v_pk_mul_f32 v[70:71], v[70:71], v[74:75]
	v_pk_mul_f32 v[72:73], v[72:73], v[76:77]
	v_pk_mul_f32 v[74:75], v[78:79], s[34:35] op_sel_hi:[1,0]
	v_pk_mul_f32 v[76:77], v[80:81], s[34:35] op_sel_hi:[1,0]
	v_pk_mul_f32 v[66:67], v[66:67], v[74:75]
	v_pk_mul_f32 v[68:69], v[68:69], v[76:77]
	v_cvt_pk_bf16_f32 v70, v70, v71
	v_cvt_pk_bf16_f32 v71, v72, v73
	v_cvt_pk_bf16_f32 v66, v66, v67
	s_nop 0
	v_cvt_pk_bf16_f32 v67, v68, v69
	v_cndmask_b32_e64 v69, v84, v66, s[4:5]
	v_cndmask_b32_e64 v68, v85, v67, s[4:5]
	v_cndmask_b32_e64 v72, v83, v71, s[4:5]
	v_cndmask_b32_e64 v73, v82, v70, s[4:5]
	v_mov_b32_dpp v68, v68 row_ror:8 row_mask:0xf bank_mask:0xf
	v_mov_b32_dpp v69, v69 row_ror:8 row_mask:0xf bank_mask:0xf
	v_mov_b32_dpp v72, v72 row_ror:8 row_mask:0xf bank_mask:0xf
	v_mov_b32_dpp v73, v73 row_ror:8 row_mask:0xf bank_mask:0xf
	s_waitcnt lgkmcnt(0)
	v_cndmask_b32_e64 v74, v68, v85, s[4:5]
	s_waitcnt lgkmcnt(0)
	v_cndmask_b32_e64 v75, v69, v84, s[4:5]
	s_waitcnt lgkmcnt(0)
	v_cndmask_b32_e64 v76, v72, v83, s[4:5]
	s_waitcnt lgkmcnt(0)
	v_cndmask_b32_e64 v77, v73, v82, s[4:5]
	v_cndmask_b32_e64 v79, v66, v69, s[4:5]
	ds_bpermute_b32 v69, v175, v74
	v_or_b32_e32 v74, 48, v148
	v_cndmask_b32_e64 v78, v67, v68, s[4:5]
	ds_bpermute_b32 v66, v175, v77
	ds_bpermute_b32 v67, v175, v76
	ds_bpermute_b32 v68, v175, v75
	v_ashrrev_i32_e32 v75, 31, v74
	v_cndmask_b32_e64 v71, v71, v72, s[4:5]
	v_cndmask_b32_e64 v70, v70, v73, s[4:5]
	v_lshlrev_b64 v[74:75], 11, v[74:75]
	ds_bpermute_b32 v70, v175, v70
	ds_bpermute_b32 v71, v175, v71
	ds_bpermute_b32 v72, v175, v79
	ds_bpermute_b32 v73, v175, v78
	v_lshl_add_u64 v[74:75], s[22:23], 0, v[74:75]
	v_lshl_add_u64 v[74:75], v[74:75], 0, s[38:39]
	v_lshl_add_u64 v[74:75], v[74:75], 0, v[138:139]
	s_waitcnt lgkmcnt(4)
	global_store_dwordx4 v[74:75], v[66:69], off
	s_nop 1
	v_add_co_u32_e32 v66, vcc, s51, v74
	s_nop 1
	v_addc_co_u32_e32 v67, vcc, 0, v75, vcc
	s_waitcnt lgkmcnt(0)
	global_store_dwordx4 v[66:67], v[70:73], off
	v_add_u32_e32 v66, 0x80, v150
	v_ashrrev_i32_e32 v67, 31, v66
	v_lshlrev_b64 v[66:67], 11, v[66:67]
	v_lshl_add_u64 v[66:67], s[24:25], 0, v[66:67]
	v_lshl_add_u64 v[66:67], v[66:67], 0, s[40:41]
	v_lshl_add_u64 v[66:67], v[66:67], 0, s[18:19]
	v_lshl_add_u64 v[66:67], v[66:67], 0, v[140:141]
	global_load_dwordx2 v[68:69], v[66:67], off offset:1024
	s_nop 0
	global_load_dwordx2 v[66:67], v[66:67], off offset:1056
	v_add_u32_e32 v70, 0x90, v150
	v_ashrrev_i32_e32 v71, 31, v70
	v_lshlrev_b64 v[70:71], 11, v[70:71]
	v_lshl_add_u64 v[70:71], s[24:25], 0, v[70:71]
	v_lshl_add_u64 v[70:71], v[70:71], 0, s[40:41]
	v_lshl_add_u64 v[70:71], v[70:71], 0, s[18:19]
	v_lshl_add_u64 v[70:71], v[70:71], 0, v[140:141]
	global_load_dwordx2 v[72:73], v[70:71], off offset:1024
	s_nop 0
	global_load_dwordx2 v[70:71], v[70:71], off offset:1056
	s_waitcnt vmcnt(3)
	v_cvt_f32_ubyte0_e32 v74, v68
	v_cvt_f32_ubyte1_e32 v75, v68
	v_cvt_f32_ubyte2_e32 v76, v68
	v_cvt_f32_ubyte3_e32 v77, v68
	v_cvt_f32_ubyte0_e32 v78, v69
	v_cvt_f32_ubyte1_e32 v79, v69
	v_cvt_f32_ubyte2_e32 v68, v69
	v_cvt_f32_ubyte3_e32 v69, v69
	v_pk_mul_f32 v[74:75], v[74:75], s[34:35] op_sel_hi:[1,0]
	v_pk_mul_f32 v[68:69], v[68:69], s[34:35] op_sel_hi:[1,0]
	v_pk_mul_f32 v[62:63], v[62:63], v[74:75]
	v_pk_mul_f32 v[74:75], v[78:79], s[34:35] op_sel_hi:[1,0]
	v_pk_mul_f32 v[76:77], v[76:77], s[34:35] op_sel_hi:[1,0]
	v_pk_mul_f32 v[60:61], v[60:61], v[68:69]
	v_pk_mul_f32 v[58:59], v[58:59], v[74:75]
	v_pk_mul_f32 v[64:65], v[64:65], v[76:77]
	v_cvt_pk_bf16_f32 v68, v62, v63
	s_waitcnt vmcnt(2)
	v_cvt_f32_ubyte0_e32 v62, v67
	v_cvt_pk_bf16_f32 v69, v64, v65
	v_cvt_pk_bf16_f32 v74, v58, v59
	v_cvt_pk_bf16_f32 v75, v60, v61
	v_cvt_f32_ubyte0_e32 v58, v66
	v_cvt_f32_ubyte1_e32 v59, v66
	v_cvt_f32_ubyte2_e32 v60, v66
	v_cvt_f32_ubyte3_e32 v61, v66
	v_cvt_f32_ubyte1_e32 v63, v67
	v_cvt_f32_ubyte2_e32 v64, v67
	v_cvt_f32_ubyte3_e32 v65, v67
	v_pk_mul_f32 v[58:59], v[58:59], s[34:35] op_sel_hi:[1,0]
	v_pk_mul_f32 v[60:61], v[60:61], s[34:35] op_sel_hi:[1,0]
	v_pk_mul_f32 v[54:55], v[54:55], v[58:59]
	v_pk_mul_f32 v[56:57], v[56:57], v[60:61]
	v_pk_mul_f32 v[58:59], v[62:63], s[34:35] op_sel_hi:[1,0]
	v_pk_mul_f32 v[60:61], v[64:65], s[34:35] op_sel_hi:[1,0]
	v_pk_mul_f32 v[50:51], v[50:51], v[58:59]
	v_pk_mul_f32 v[52:53], v[52:53], v[60:61]
	v_cvt_pk_bf16_f32 v54, v54, v55
	v_cvt_pk_bf16_f32 v55, v56, v57
	v_cvt_pk_bf16_f32 v50, v50, v51
	v_add_u32_e32 v58, 0x80, v148
	v_cvt_pk_bf16_f32 v51, v52, v53
	v_cndmask_b32_e64 v53, v74, v50, s[4:5]
	v_cndmask_b32_e64 v52, v75, v51, s[4:5]
	v_cndmask_b32_e64 v56, v69, v55, s[4:5]
	v_cndmask_b32_e64 v57, v68, v54, s[4:5]
	v_mov_b32_dpp v52, v52 row_ror:8 row_mask:0xf bank_mask:0xf
	v_mov_b32_dpp v53, v53 row_ror:8 row_mask:0xf bank_mask:0xf
	v_mov_b32_dpp v56, v56 row_ror:8 row_mask:0xf bank_mask:0xf
	v_mov_b32_dpp v57, v57 row_ror:8 row_mask:0xf bank_mask:0xf
	s_waitcnt lgkmcnt(0)
; __device__ __forceinline__ u32x4 pack8(const f32x4& v0, const f32x4& v1) { u32x4 w; w.x = cvt_pk_bf16(v0[0], v0[1]); w.y = cvt_pk_bf16(v0[2], v0[3]); w.z = cvt_pk_bf16(v1[0], v1[1]); w.w = cvt_pk_bf16(v1[2], v1[3]); return w; }
; __device__ __forceinline__ u32x4 xor8_16B(u32x4 v) { u32x4 r; r.x = (unsigned)__shfl_xor((int)v.x, 8); r.y = (unsigned)__shfl_xor((int)v.y, 8); r.z = (unsigned)__shfl_xor((int)v.z, 8); r.w = (unsigned)__shfl_xor((int)v.w, 8); return r; }
; __device__ __forceinline__ void store_rows_bf16(bf16_t* O, size_t ldc, int r0, int c0, int fr, int fq, u32x4 w0, u32x4 w1) {
;     const bool h = fr & 8; const u32x4 recv = xor8_16B(h ? w0 : w1);
;     const u32x4 d1 = h ? recv : w0, d2 = h ? w1 : recv;
;     const int lane = fr + 16 * fq, src = ((lane >> 3) + 8 * ((lane >> 2) & 1) + 16 * (lane & 3)) * 4;
;     const u32x4 e1 = bperm_16B(src, d1), e2 = bperm_16B(src, d2);
;     bf16_t* p = O + (size_t)(r0 + (lane >> 3)) * ldc + c0 + 8 * (lane & 7);
;     *(u32x4*)p = e1; *(u32x4*)(p + 8 * ldc) = e2;
;     __device__ __forceinline__ void operator()(const f32x4 (&acc)[2][2][4][2], const Unit& u, int wr, int wc, int fr, int fq) const {
; #pragma unroll
;         for (int ai = 0; ai < 2; ++ai)
; #pragma unroll
;             for (int mp = 0; mp < 2; ++mp) {
;                 uint2 gm[2][2];
; #pragma unroll
;                 for (int mm = 0; mm < 2; ++mm)
; #pragma unroll
;                     for (int bj = 0; bj < 2; ++bj) gm[mm][bj] = *(const uint2*)(gate + (size_t)(u.pm * BM + wr * 64 + fr + ai * HALF + (2 * mp + mm) * 16) * 2048 + 1024 + u.pn * BM + wc * 64 + bj * 32 + 8 * fq);
; #pragma unroll
;                 for (int mm = 0; mm < 2; ++mm) { const int m = 2 * mp + mm; u32x4 w[2];
; #pragma unroll
;                     for (int bj = 0; bj < 2; ++bj) { f32x4 m0, m1; ub4(gm[mm][bj].x, m0); ub4(gm[mm][bj].y, m1); w[bj] = pack8(acc[ai][bj][m][0] * (m0 * (1.0f / 255.0f)), acc[ai][bj][m][1] * (m1 * (1.0f / 255.0f))); }
;                     store_rows_bf16(O, 1024, u.pm * BM + wr * 64 + ai * HALF + m * 16, u.pn * BM + wc * 64, fr, fq, w[0], w[1]); }
	v_cndmask_b32_e64 v59, v52, v75, s[4:5]
	s_waitcnt lgkmcnt(0)
	v_cndmask_b32_e64 v60, v53, v74, s[4:5]
	s_waitcnt lgkmcnt(0)
	v_cndmask_b32_e64 v61, v56, v69, s[4:5]
	s_waitcnt lgkmcnt(0)
	v_cndmask_b32_e64 v62, v57, v68, s[4:5]
	v_cndmask_b32_e64 v63, v51, v52, s[4:5]
	v_cndmask_b32_e64 v64, v50, v53, s[4:5]
	ds_bpermute_b32 v50, v175, v62
	ds_bpermute_b32 v51, v175, v61
	ds_bpermute_b32 v52, v175, v60
	ds_bpermute_b32 v53, v175, v59
	v_ashrrev_i32_e32 v59, 31, v58
	v_cndmask_b32_e64 v55, v55, v56, s[4:5]
	v_cndmask_b32_e64 v54, v54, v57, s[4:5]
	v_lshlrev_b64 v[58:59], 11, v[58:59]
	ds_bpermute_b32 v54, v175, v54
	ds_bpermute_b32 v55, v175, v55
	ds_bpermute_b32 v56, v175, v64
	ds_bpermute_b32 v57, v175, v63
	v_lshl_add_u64 v[58:59], s[22:23], 0, v[58:59]
	v_lshl_add_u64 v[58:59], v[58:59], 0, s[38:39]
	v_lshl_add_u64 v[58:59], v[58:59], 0, v[138:139]
	s_waitcnt lgkmcnt(4)
	global_store_dwordx4 v[58:59], v[50:53], off
	s_nop 1
	v_add_co_u32_e32 v50, vcc, s51, v58
	s_waitcnt vmcnt(2)
	v_cvt_f32_ubyte2_e32 v52, v72
	v_addc_co_u32_e32 v51, vcc, 0, v59, vcc
	s_waitcnt lgkmcnt(0)
	global_store_dwordx4 v[50:51], v[54:57], off
	v_cvt_f32_ubyte0_e32 v50, v72
	v_cvt_f32_ubyte1_e32 v51, v72
	v_cvt_f32_ubyte3_e32 v53, v72
	v_cvt_f32_ubyte0_e32 v54, v73
	v_cvt_f32_ubyte1_e32 v55, v73
	v_cvt_f32_ubyte2_e32 v56, v73
	v_cvt_f32_ubyte3_e32 v57, v73
	v_pk_mul_f32 v[50:51], v[50:51], s[34:35] op_sel_hi:[1,0]
	v_pk_mul_f32 v[52:53], v[52:53], s[34:35] op_sel_hi:[1,0]
	v_pk_mul_f32 v[46:47], v[46:47], v[50:51]
	v_pk_mul_f32 v[48:49], v[48:49], v[52:53]
	v_pk_mul_f32 v[50:51], v[54:55], s[34:35] op_sel_hi:[1,0]
	v_pk_mul_f32 v[52:53], v[56:57], s[34:35] op_sel_hi:[1,0]
	v_pk_mul_f32 v[42:43], v[42:43], v[50:51]
	v_pk_mul_f32 v[44:45], v[44:45], v[52:53]
	v_cvt_pk_bf16_f32 v50, v46, v47
	v_cvt_pk_bf16_f32 v51, v48, v49
	v_cvt_pk_bf16_f32 v52, v42, v43
	s_waitcnt vmcnt(2)
	v_cvt_f32_ubyte0_e32 v42, v70
	v_cvt_pk_bf16_f32 v53, v44, v45
	v_cvt_f32_ubyte1_e32 v43, v70
	v_cvt_f32_ubyte2_e32 v44, v70
	v_cvt_f32_ubyte3_e32 v45, v70
	v_cvt_f32_ubyte0_e32 v46, v71
	v_cvt_f32_ubyte1_e32 v47, v71
	v_cvt_f32_ubyte2_e32 v48, v71
	v_cvt_f32_ubyte3_e32 v49, v71
	v_pk_mul_f32 v[42:43], v[42:43], s[34:35] op_sel_hi:[1,0]
	v_pk_mul_f32 v[44:45], v[44:45], s[34:35] op_sel_hi:[1,0]
	v_pk_mul_f32 v[38:39], v[38:39], v[42:43]
	v_pk_mul_f32 v[40:41], v[40:41], v[44:45]
	v_pk_mul_f32 v[42:43], v[46:47], s[34:35] op_sel_hi:[1,0]
	v_pk_mul_f32 v[44:45], v[48:49], s[34:35] op_sel_hi:[1,0]
	v_pk_mul_f32 v[34:35], v[34:35], v[42:43]
	v_pk_mul_f32 v[36:37], v[36:37], v[44:45]
	v_cvt_pk_bf16_f32 v38, v38, v39
	v_cvt_pk_bf16_f32 v39, v40, v41
	v_cvt_pk_bf16_f32 v34, v34, v35
	s_nop 0
	v_cvt_pk_bf16_f32 v35, v36, v37
	v_cndmask_b32_e64 v37, v52, v34, s[4:5]
	v_cndmask_b32_e64 v36, v53, v35, s[4:5]
	v_cndmask_b32_e64 v40, v51, v39, s[4:5]
	v_cndmask_b32_e64 v41, v50, v38, s[4:5]
	v_mov_b32_dpp v36, v36 row_ror:8 row_mask:0xf bank_mask:0xf
	v_mov_b32_dpp v37, v37 row_ror:8 row_mask:0xf bank_mask:0xf
	v_mov_b32_dpp v40, v40 row_ror:8 row_mask:0xf bank_mask:0xf
	v_mov_b32_dpp v41, v41 row_ror:8 row_mask:0xf bank_mask:0xf
	s_waitcnt lgkmcnt(0)
	v_cndmask_b32_e64 v42, v36, v53, s[4:5]
	s_waitcnt lgkmcnt(0)
	v_cndmask_b32_e64 v43, v37, v52, s[4:5]
	s_waitcnt lgkmcnt(0)
	v_cndmask_b32_e64 v44, v40, v51, s[4:5]
	s_waitcnt lgkmcnt(0)
	v_cndmask_b32_e64 v45, v41, v50, s[4:5]
	v_cndmask_b32_e64 v47, v34, v37, s[4:5]
	ds_bpermute_b32 v37, v175, v42
	v_add_u32_e32 v42, 0x90, v148
	v_cndmask_b32_e64 v46, v35, v36, s[4:5]
	ds_bpermute_b32 v34, v175, v45
	ds_bpermute_b32 v35, v175, v44
	ds_bpermute_b32 v36, v175, v43
	v_ashrrev_i32_e32 v43, 31, v42
	v_cndmask_b32_e64 v39, v39, v40, s[4:5]
	v_cndmask_b32_e64 v38, v38, v41, s[4:5]
	v_lshlrev_b64 v[42:43], 11, v[42:43]
	ds_bpermute_b32 v38, v175, v38
	ds_bpermute_b32 v39, v175, v39
	ds_bpermute_b32 v40, v175, v47
	ds_bpermute_b32 v41, v175, v46
	v_lshl_add_u64 v[42:43], s[22:23], 0, v[42:43]
	v_lshl_add_u64 v[42:43], v[42:43], 0, s[38:39]
	v_lshl_add_u64 v[42:43], v[42:43], 0, v[138:139]
	s_waitcnt lgkmcnt(4)
	global_store_dwordx4 v[42:43], v[34:37], off
	s_nop 1
	v_add_co_u32_e32 v34, vcc, s51, v42
	s_nop 1
	v_addc_co_u32_e32 v35, vcc, 0, v43, vcc
	s_waitcnt lgkmcnt(0)
	global_store_dwordx4 v[34:35], v[38:41], off
	v_add_u32_e32 v34, 0xa0, v150
	v_ashrrev_i32_e32 v35, 31, v34
	v_lshlrev_b64 v[34:35], 11, v[34:35]
	v_lshl_add_u64 v[34:35], s[24:25], 0, v[34:35]
	v_lshl_add_u64 v[34:35], v[34:35], 0, s[40:41]
	v_lshl_add_u64 v[34:35], v[34:35], 0, s[18:19]
	v_lshl_add_u64 v[34:35], v[34:35], 0, v[140:141]
	global_load_dwordx2 v[36:37], v[34:35], off offset:1024
	s_nop 0
	global_load_dwordx2 v[34:35], v[34:35], off offset:1056
	v_add_u32_e32 v38, 0xb0, v150
	v_ashrrev_i32_e32 v39, 31, v38
	v_lshlrev_b64 v[38:39], 11, v[38:39]
	v_lshl_add_u64 v[38:39], s[24:25], 0, v[38:39]
	v_lshl_add_u64 v[38:39], v[38:39], 0, s[40:41]
	v_lshl_add_u64 v[38:39], v[38:39], 0, s[18:19]
	v_lshl_add_u64 v[38:39], v[38:39], 0, v[140:141]
	global_load_dwordx2 v[40:41], v[38:39], off offset:1024
	s_nop 0
	global_load_dwordx2 v[38:39], v[38:39], off offset:1056
	s_waitcnt vmcnt(3)
	v_cvt_f32_ubyte0_e32 v42, v36
	v_cvt_f32_ubyte1_e32 v43, v36
	v_cvt_f32_ubyte2_e32 v44, v36
	v_cvt_f32_ubyte3_e32 v45, v36
	v_cvt_f32_ubyte0_e32 v46, v37
	v_cvt_f32_ubyte1_e32 v47, v37
	v_cvt_f32_ubyte2_e32 v36, v37
	v_cvt_f32_ubyte3_e32 v37, v37
	v_pk_mul_f32 v[42:43], v[42:43], s[34:35] op_sel_hi:[1,0]
	v_pk_mul_f32 v[36:37], v[36:37], s[34:35] op_sel_hi:[1,0]
	v_pk_mul_f32 v[30:31], v[30:31], v[42:43]
	v_pk_mul_f32 v[42:43], v[46:47], s[34:35] op_sel_hi:[1,0]
	v_pk_mul_f32 v[44:45], v[44:45], s[34:35] op_sel_hi:[1,0]
	v_pk_mul_f32 v[28:29], v[28:29], v[36:37]
	v_pk_mul_f32 v[26:27], v[26:27], v[42:43]
	v_pk_mul_f32 v[32:33], v[32:33], v[44:45]
	v_cvt_pk_bf16_f32 v36, v30, v31
	s_waitcnt vmcnt(2)
; __device__ __forceinline__ u32x4 pack8(const f32x4& v0, const f32x4& v1) { u32x4 w; w.x = cvt_pk_bf16(v0[0], v0[1]); w.y = cvt_pk_bf16(v0[2], v0[3]); w.z = cvt_pk_bf16(v1[0], v1[1]); w.w = cvt_pk_bf16(v1[2], v1[3]); return w; }
; #define PG8_BAR __builtin_amdgcn_s_barrier()
;     __device__ __forceinline__ void operator()(const f32x4 (&acc)[2][2][4][2], const Unit& u, int wr, int wc, int fr, int fq) const {
; #pragma unroll
;         for (int ai = 0; ai < 2; ++ai)
; #pragma unroll
;             for (int mp = 0; mp < 2; ++mp) {
;                 uint2 gm[2][2];
; #pragma unroll
;                 for (int mm = 0; mm < 2; ++mm)
; #pragma unroll
;                     for (int bj = 0; bj < 2; ++bj) gm[mm][bj] = *(const uint2*)(gate + (size_t)(u.pm * BM + wr * 64 + fr + ai * HALF + (2 * mp + mm) * 16) * 2048 + 1024 + u.pn * BM + wc * 64 + bj * 32 + 8 * fq);
; #pragma unroll
;                 for (int mm = 0; mm < 2; ++mm) { const int m = 2 * mp + mm; u32x4 w[2];
; #pragma unroll
;                     for (int bj = 0; bj < 2; ++bj) { f32x4 m0, m1; ub4(gm[mm][bj].x, m0); ub4(gm[mm][bj].y, m1); w[bj] = pack8(acc[ai][bj][m][0] * (m0 * (1.0f / 255.0f)), acc[ai][bj][m][1] * (m1 * (1.0f / 255.0f))); }
;                     store_rows_bf16(O, 1024, u.pm * BM + wr * 64 + ai * HALF + m * 16, u.pn * BM + wc * 64, fr, fq, w[0], w[1]); }
;             }
; template <class Epi, class Sched, bool ALIGN_EPI = false, bool SP2 = false>
; __device__ __forceinline__ void gemm_phase(PG8_LAS unsigned char* lds, const Gemm g, const Sched& S, const Epi& E) {
;     ...
;         if constexpr (ALIGN_EPI) { if (wr == 0) PG8_BAR; }
;         if constexpr (Epi::FINAL) { E.run(acc, cur, wr, wc, fr, fq, lds, wid); S.done(cur); }
;         else if constexpr (!Epi::AFTER_DRAIN) { E(acc, cur, wr, wc, fr, fq); S.done(cur); }
;         if (!has_next) break;
; #pragma unroll
;         for (int a = 0; a < 2; ++a)
; #pragma unroll
;             for (int b = 0; b < 2; ++b)
; #pragma unroll
;                 for (int m = 0; m < 4; ++m)
; #pragma unroll
;                     for (int n = 0; n < 2; ++n) acc[a][b][m][n] = (f32x4){0.f, 0.f, 0.f, 0.f};
;         cur = nxt; cA = nA; cB = nB; ++ui;
;         if constexpr (ALIGN_EPI) { if (wr == 1) PG8_BAR; }
	v_cvt_f32_ubyte0_e32 v30, v35
	v_cvt_pk_bf16_f32 v37, v32, v33
	v_cvt_pk_bf16_f32 v42, v26, v27
	v_cvt_pk_bf16_f32 v43, v28, v29
	v_cvt_f32_ubyte0_e32 v26, v34
	v_cvt_f32_ubyte1_e32 v27, v34
	v_cvt_f32_ubyte2_e32 v28, v34
	v_cvt_f32_ubyte3_e32 v29, v34
	v_cvt_f32_ubyte1_e32 v31, v35
	v_cvt_f32_ubyte2_e32 v32, v35
	v_cvt_f32_ubyte3_e32 v33, v35
	v_pk_mul_f32 v[26:27], v[26:27], s[34:35] op_sel_hi:[1,0]
	v_pk_mul_f32 v[28:29], v[28:29], s[34:35] op_sel_hi:[1,0]
	v_pk_mul_f32 v[22:23], v[22:23], v[26:27]
	v_pk_mul_f32 v[24:25], v[24:25], v[28:29]
	v_pk_mul_f32 v[26:27], v[30:31], s[34:35] op_sel_hi:[1,0]
	v_pk_mul_f32 v[28:29], v[32:33], s[34:35] op_sel_hi:[1,0]
	v_pk_mul_f32 v[18:19], v[18:19], v[26:27]
	v_pk_mul_f32 v[20:21], v[20:21], v[28:29]
	v_cvt_pk_bf16_f32 v22, v22, v23
	v_cvt_pk_bf16_f32 v23, v24, v25
	v_cvt_pk_bf16_f32 v18, v18, v19
	s_nop 0
	v_cvt_pk_bf16_f32 v19, v20, v21
	v_cndmask_b32_e64 v21, v42, v18, s[4:5]
	v_cndmask_b32_e64 v20, v43, v19, s[4:5]
	v_cndmask_b32_e64 v24, v37, v23, s[4:5]
	v_cndmask_b32_e64 v25, v36, v22, s[4:5]
	v_mov_b32_dpp v20, v20 row_ror:8 row_mask:0xf bank_mask:0xf
	v_mov_b32_dpp v21, v21 row_ror:8 row_mask:0xf bank_mask:0xf
	v_mov_b32_dpp v24, v24 row_ror:8 row_mask:0xf bank_mask:0xf
	v_mov_b32_dpp v25, v25 row_ror:8 row_mask:0xf bank_mask:0xf
	s_waitcnt lgkmcnt(0)
	v_cndmask_b32_e64 v26, v20, v43, s[4:5]
	s_waitcnt lgkmcnt(0)
	v_cndmask_b32_e64 v27, v21, v42, s[4:5]
	s_waitcnt lgkmcnt(0)
	v_cndmask_b32_e64 v28, v24, v37, s[4:5]
	s_waitcnt lgkmcnt(0)
	v_cndmask_b32_e64 v29, v25, v36, s[4:5]
	v_cndmask_b32_e64 v31, v18, v21, s[4:5]
	ds_bpermute_b32 v21, v175, v26
	v_add_u32_e32 v26, 0xa0, v148
	v_cndmask_b32_e64 v30, v19, v20, s[4:5]
	ds_bpermute_b32 v18, v175, v29
	ds_bpermute_b32 v19, v175, v28
	ds_bpermute_b32 v20, v175, v27
	v_ashrrev_i32_e32 v27, 31, v26
	v_cndmask_b32_e64 v23, v23, v24, s[4:5]
	v_cndmask_b32_e64 v22, v22, v25, s[4:5]
	v_lshlrev_b64 v[26:27], 11, v[26:27]
	ds_bpermute_b32 v22, v175, v22
	ds_bpermute_b32 v23, v175, v23
	ds_bpermute_b32 v24, v175, v31
	ds_bpermute_b32 v25, v175, v30
	v_lshl_add_u64 v[26:27], s[22:23], 0, v[26:27]
	v_lshl_add_u64 v[26:27], v[26:27], 0, s[38:39]
	v_lshl_add_u64 v[26:27], v[26:27], 0, v[138:139]
	s_waitcnt lgkmcnt(4)
	global_store_dwordx4 v[26:27], v[18:21], off
	s_nop 1
	v_add_co_u32_e32 v18, vcc, s51, v26
	s_waitcnt vmcnt(2)
	v_cvt_f32_ubyte2_e32 v20, v40
	v_addc_co_u32_e32 v19, vcc, 0, v27, vcc
	s_waitcnt lgkmcnt(0)
	global_store_dwordx4 v[18:19], v[22:25], off
	v_cvt_f32_ubyte0_e32 v18, v40
	v_cvt_f32_ubyte1_e32 v19, v40
	v_cvt_f32_ubyte3_e32 v21, v40
	v_cvt_f32_ubyte0_e32 v22, v41
	v_cvt_f32_ubyte1_e32 v23, v41
	v_cvt_f32_ubyte2_e32 v24, v41
	v_cvt_f32_ubyte3_e32 v25, v41
	v_pk_mul_f32 v[18:19], v[18:19], s[34:35] op_sel_hi:[1,0]
	v_pk_mul_f32 v[20:21], v[20:21], s[34:35] op_sel_hi:[1,0]
	v_pk_mul_f32 v[14:15], v[14:15], v[18:19]
	v_pk_mul_f32 v[16:17], v[16:17], v[20:21]
	v_pk_mul_f32 v[18:19], v[22:23], s[34:35] op_sel_hi:[1,0]
	v_pk_mul_f32 v[20:21], v[24:25], s[34:35] op_sel_hi:[1,0]
	v_pk_mul_f32 v[10:11], v[10:11], v[18:19]
	v_pk_mul_f32 v[12:13], v[12:13], v[20:21]
	v_cvt_pk_bf16_f32 v18, v14, v15
	v_cvt_pk_bf16_f32 v19, v16, v17
	v_cvt_pk_bf16_f32 v20, v10, v11
	s_waitcnt vmcnt(2)
	v_cvt_f32_ubyte0_e32 v10, v38
	v_cvt_pk_bf16_f32 v21, v12, v13
	v_cvt_f32_ubyte1_e32 v11, v38
	v_cvt_f32_ubyte2_e32 v12, v38
	v_cvt_f32_ubyte3_e32 v13, v38
	v_cvt_f32_ubyte0_e32 v14, v39
	v_cvt_f32_ubyte1_e32 v15, v39
	v_cvt_f32_ubyte2_e32 v16, v39
	v_cvt_f32_ubyte3_e32 v17, v39
	v_pk_mul_f32 v[10:11], v[10:11], s[34:35] op_sel_hi:[1,0]
	v_pk_mul_f32 v[12:13], v[12:13], s[34:35] op_sel_hi:[1,0]
	v_pk_mul_f32 v[6:7], v[6:7], v[10:11]
	v_pk_mul_f32 v[8:9], v[8:9], v[12:13]
	v_pk_mul_f32 v[10:11], v[14:15], s[34:35] op_sel_hi:[1,0]
	v_pk_mul_f32 v[12:13], v[16:17], s[34:35] op_sel_hi:[1,0]
	v_pk_mul_f32 v[2:3], v[2:3], v[10:11]
	v_pk_mul_f32 v[4:5], v[4:5], v[12:13]
	v_cvt_pk_bf16_f32 v6, v6, v7
	v_cvt_pk_bf16_f32 v7, v8, v9
	v_cvt_pk_bf16_f32 v2, v2, v3
	s_nop 0
	v_cvt_pk_bf16_f32 v3, v4, v5
	v_cndmask_b32_e64 v5, v20, v2, s[4:5]
	v_cndmask_b32_e64 v4, v21, v3, s[4:5]
	v_cndmask_b32_e64 v8, v19, v7, s[4:5]
	v_cndmask_b32_e64 v9, v18, v6, s[4:5]
	v_mov_b32_dpp v4, v4 row_ror:8 row_mask:0xf bank_mask:0xf
	v_mov_b32_dpp v5, v5 row_ror:8 row_mask:0xf bank_mask:0xf
	v_mov_b32_dpp v8, v8 row_ror:8 row_mask:0xf bank_mask:0xf
	v_mov_b32_dpp v9, v9 row_ror:8 row_mask:0xf bank_mask:0xf
	s_waitcnt lgkmcnt(0)
	v_cndmask_b32_e64 v10, v4, v21, s[4:5]
	s_waitcnt lgkmcnt(0)
	v_cndmask_b32_e64 v11, v5, v20, s[4:5]
	s_waitcnt lgkmcnt(0)
	v_cndmask_b32_e64 v12, v8, v19, s[4:5]
	s_waitcnt lgkmcnt(0)
	v_cndmask_b32_e64 v13, v9, v18, s[4:5]
	v_cndmask_b32_e64 v15, v2, v5, s[4:5]
	ds_bpermute_b32 v5, v175, v10
	v_add_u32_e32 v10, 0xb0, v148
	v_cndmask_b32_e64 v14, v3, v4, s[4:5]
	ds_bpermute_b32 v2, v175, v13
	ds_bpermute_b32 v3, v175, v12
	ds_bpermute_b32 v4, v175, v11
	v_ashrrev_i32_e32 v11, 31, v10
	v_lshlrev_b64 v[10:11], 11, v[10:11]
	v_cndmask_b32_e64 v7, v7, v8, s[4:5]
	v_cndmask_b32_e64 v6, v6, v9, s[4:5]
	v_lshl_add_u64 v[10:11], s[22:23], 0, v[10:11]
	ds_bpermute_b32 v6, v175, v6
	ds_bpermute_b32 v7, v175, v7
	ds_bpermute_b32 v8, v175, v15
	ds_bpermute_b32 v9, v175, v14
	v_lshl_add_u64 v[10:11], v[10:11], 0, s[38:39]
	v_lshl_add_u64 v[10:11], v[10:11], 0, v[138:139]
	s_waitcnt lgkmcnt(4)
	global_store_dwordx4 v[10:11], v[2:5], off
	s_nop 1
	v_add_co_u32_e32 v2, vcc, 0x4000, v10
	s_nop 1
	v_addc_co_u32_e32 v3, vcc, 0, v11, vcc
	s_and_b64 vcc, exec, s[6:7]
	s_mov_b64 s[6:7], -1
	s_waitcnt lgkmcnt(0)
	global_store_dwordx4 v[2:3], v[6:9], off
	s_cbranch_vccnz .LBB0_969
	s_andn2_b64 vcc, exec, s[20:21]
	s_cbranch_vccnz .LBB0_968
	s_barrier
	s_branch .LBB0_968

; #define PG8_RLD(k) do { const float* p_ = rbase + (size_t)(((k) >> 2) * HALF + ((k) & 3) * 16) * 1024; rg[k][0] = *(const f32x4*)p_; rg[k][1] = *(const f32x4*)(p_ + 4); rg[k][2] = *(const f32x4*)(p_ + 32); rg[k][3] = *(const f32x4*)(p_ + 36); } while (0)
;     __device__ __forceinline__ void operator()(f32x4 (&acc)[2][2][4][2], const Unit& u, int wr, int wc, int fr, int fq) const {
;         const float* rbase = res + (size_t)(u.pm * BM + wr * 64 + fr) * 1024 + u.pn * BM + wc * 64 + 8 * fq;
;         f32x4 rg[8][4];
;     ...
;         PG8_RLD(0); PG8_RLD(1);
; #pragma unroll
;         for (int k = 0; k < 8; ++k) { const int ai = k >> 2, m = k & 3;
;             if (k + 2 < 8) PG8_RLD(k + 2);
;             acc[ai][0][m][0] += rg[k][0]; acc[ai][0][m][1] += rg[k][1]; acc[ai][1][m][0] += rg[k][2]; acc[ai][1][m][1] += rg[k][3];
;             asm volatile("" : "+v"(acc[ai][0][m][0]), "+v"(acc[ai][0][m][1]), "+v"(acc[ai][1][m][0]), "+v"(acc[ai][1][m][1]) :: "memory"); }
.LBB0_1074:
	s_lshl_b32 s58, s92, 8
	s_load_dwordx2 s[0:1], s[94:95], 0x0
	s_add_i32 s58, s58, s77
	v_or_b32_e32 v186, s58, v1
	v_ashrrev_i32_e32 v187, 31, v186
	v_lshlrev_b64 v[130:131], 12, v[186:187]
	s_lshl_b32 s56, s20, 8
	s_waitcnt lgkmcnt(0)
	v_lshl_add_u64 v[130:131], s[0:1], 0, v[130:131]
	s_ashr_i32 s57, s56, 31
	v_lshl_add_u64 v[130:131], s[56:57], 2, v[130:131]
	s_lshl_b32 s20, s79, 2
	v_lshl_add_u64 v[130:131], v[130:131], 0, s[20:21]
	v_mov_b32_e32 v185, v175
	v_lshl_add_u64 v[188:189], v[130:131], 0, v[184:185]
	s_mov_b64 s[0:1], 0x10000
	v_lshl_add_u64 v[134:135], v[188:189], 0, s[0:1]
	s_mov_b32 s0, 0x10000
	global_load_dwordx4 v[130:133], v[188:189], off offset:16
	global_load_dwordx4 v[150:153], v[188:189], off
	global_load_dwordx4 v[154:157], v[188:189], off offset:144
	global_load_dwordx4 v[158:161], v[188:189], off offset:128
	v_add_co_u32_e32 v136, vcc, s0, v188
	s_mov_b64 s[0:1], 0x10080
	s_nop 0
	v_addc_co_u32_e32 v137, vcc, 0, v189, vcc
	global_load_dwordx4 v[198:201], v[136:137], off
	global_load_dwordx4 v[202:205], v[134:135], off offset:16
	v_lshl_add_u64 v[134:135], v[188:189], 0, s[0:1]
	global_load_dwordx4 v[206:209], v[136:137], off offset:128
	global_load_dwordx4 v[212:215], v[134:135], off offset:16
	s_mov_b64 s[0:1], 0x20000
	v_lshl_add_u64 v[134:135], v[188:189], 0, s[0:1]
	s_mov_b32 s0, 0x20000
	v_add_co_u32_e32 v142, vcc, s0, v188
	s_mov_b64 s[0:1], 0x20080
	s_nop 0
	v_addc_co_u32_e32 v143, vcc, 0, v189, vcc
	v_lshl_add_u64 v[144:145], v[188:189], 0, s[0:1]
	s_mov_b64 s[0:1], 0x30000
	global_load_dwordx4 v[138:141], v[142:143], off
	s_nop 0
	global_load_dwordx4 v[134:137], v[134:135], off offset:16
	s_nop 0
	global_load_dwordx4 v[146:149], v[142:143], off offset:128
	s_nop 0
	global_load_dwordx4 v[142:145], v[144:145], off offset:16
	s_or_b32 s56, s56, s79
	s_ashr_i32 s57, s56, 31
	s_waitcnt vmcnt(0)
	v_pk_add_f32 v[132:133], v[124:125], v[132:133]
	v_pk_add_f32 v[128:129], v[128:129], v[152:153]
	v_pk_add_f32 v[126:127], v[126:127], v[150:151]
	v_pk_add_f32 v[130:131], v[122:123], v[130:131]
	v_pk_add_f32 v[120:121], v[120:121], v[160:161]
	v_pk_add_f32 v[118:119], v[118:119], v[158:159]
	v_pk_add_f32 v[124:125], v[116:117], v[156:157]
	v_pk_add_f32 v[122:123], v[114:115], v[154:155]
	v_add_co_u32_e32 v116, vcc, s84, v188
	v_lshl_add_u64 v[114:115], v[188:189], 0, s[0:1]
	s_nop 0
	v_addc_co_u32_e32 v117, vcc, 0, v189, vcc
	global_load_dwordx4 v[154:157], v[116:117], off
	global_load_dwordx4 v[150:153], v[114:115], off offset:16
	v_lshl_add_u64 v[114:115], v[188:189], 0, s[36:37]
	global_load_dwordx4 v[162:165], v[116:117], off offset:128
	global_load_dwordx4 v[158:161], v[114:115], off offset:16
	v_pk_add_f32 v[60:61], v[60:61], v[200:201]
	v_pk_add_f32 v[58:59], v[58:59], v[198:199]
	v_pk_add_f32 v[64:65], v[64:65], v[204:205]
	v_pk_add_f32 v[62:63], v[62:63], v[202:203]
	v_pk_add_f32 v[52:53], v[52:53], v[208:209]
	v_pk_add_f32 v[50:51], v[50:51], v[206:207]
	v_pk_add_f32 v[56:57], v[56:57], v[214:215]
	v_pk_add_f32 v[54:55], v[54:55], v[212:213]
	v_add_co_u32_e32 v116, vcc, s85, v188
	v_lshl_add_u64 v[114:115], v[188:189], 0, s[38:39]
	s_nop 0
	v_addc_co_u32_e32 v117, vcc, 0, v189, vcc
	global_load_dwordx4 v[198:201], v[116:117], off
	global_load_dwordx4 v[202:205], v[114:115], off offset:16
	v_lshl_add_u64 v[114:115], v[188:189], 0, s[40:41]
	global_load_dwordx4 v[206:209], v[116:117], off offset:128
	global_load_dwordx4 v[212:215], v[114:115], off offset:16
	v_pk_add_f32 v[106:107], v[106:107], v[138:139]
	v_add_co_u32_e32 v138, vcc, s86, v188
	v_pk_add_f32 v[108:109], v[108:109], v[140:141]
	s_nop 0
	v_addc_co_u32_e32 v139, vcc, 0, v189, vcc
	v_pk_add_f32 v[112:113], v[112:113], v[136:137]
	v_pk_add_f32 v[110:111], v[110:111], v[134:135]
	v_pk_add_f32 v[92:93], v[92:93], v[148:149]
	v_pk_add_f32 v[90:91], v[90:91], v[146:147]
	v_pk_add_f32 v[96:97], v[96:97], v[144:145]
	v_pk_add_f32 v[94:95], v[94:95], v[142:143]
	v_lshl_add_u64 v[114:115], v[188:189], 0, s[42:43]
	v_lshl_add_u64 v[140:141], v[188:189], 0, s[44:45]
	global_load_dwordx4 v[134:137], v[138:139], off
	s_nop 0
	global_load_dwordx4 v[114:117], v[114:115], off offset:16
	s_nop 0
	global_load_dwordx4 v[142:145], v[138:139], off offset:128
	s_nop 0
	global_load_dwordx4 v[138:141], v[140:141], off offset:16
	v_lshl_add_u64 v[146:147], v[188:189], 0, s[46:47]
	s_movk_i32 s0, 0x4000
	s_waitcnt vmcnt(11)
	v_pk_add_f32 v[98:99], v[98:99], v[154:155]
	v_add_co_u32_e32 v154, vcc, s87, v188
	v_pk_add_f32 v[100:101], v[100:101], v[156:157]
	s_waitcnt vmcnt(10)
	v_pk_add_f32 v[104:105], v[104:105], v[152:153]
	v_pk_add_f32 v[102:103], v[102:103], v[150:151]
	s_waitcnt vmcnt(9)
	v_pk_add_f32 v[76:77], v[76:77], v[164:165]
	v_pk_add_f32 v[74:75], v[74:75], v[162:163]
	s_waitcnt vmcnt(8)
	v_pk_add_f32 v[80:81], v[80:81], v[160:161]
	v_pk_add_f32 v[78:79], v[78:79], v[158:159]
	v_addc_co_u32_e32 v155, vcc, 0, v189, vcc
	v_lshl_add_u64 v[156:157], v[188:189], 0, s[48:49]
	global_load_dwordx4 v[150:153], v[154:155], off
	s_nop 0
	global_load_dwordx4 v[146:149], v[146:147], off offset:16
	s_nop 0
	global_load_dwordx4 v[158:161], v[154:155], off offset:128
	s_nop 0
	global_load_dwordx4 v[154:157], v[156:157], off offset:16
	s_waitcnt vmcnt(11)
	v_pk_add_f32 v[84:85], v[84:85], v[200:201]
	v_pk_add_f32 v[82:83], v[82:83], v[198:199]
	s_waitcnt vmcnt(10)
	v_pk_add_f32 v[88:89], v[88:89], v[204:205]
	v_pk_add_f32 v[86:87], v[86:87], v[202:203]
	s_waitcnt vmcnt(9)
	v_pk_add_f32 v[68:69], v[68:69], v[208:209]
	v_pk_add_f32 v[66:67], v[66:67], v[206:207]
	s_waitcnt vmcnt(8)
; __device__ __forceinline__ u32x4 pack8(const f32x4& v0, const f32x4& v1) { u32x4 w; w.x = cvt_pk_bf16(v0[0], v0[1]); w.y = cvt_pk_bf16(v0[2], v0[3]); w.z = cvt_pk_bf16(v1[0], v1[1]); w.w = cvt_pk_bf16(v1[2], v1[3]); return w; }
; __device__ __forceinline__ u32x4 xor8_16B(u32x4 v) { u32x4 r; r.x = (unsigned)__shfl_xor((int)v.x, 8); r.y = (unsigned)__shfl_xor((int)v.y, 8); r.z = (unsigned)__shfl_xor((int)v.z, 8); r.w = (unsigned)__shfl_xor((int)v.w, 8); return r; }
; __device__ __forceinline__ void store_rows_bf16(bf16_t* O, size_t ldc, int r0, int c0, int fr, int fq, u32x4 w0, u32x4 w1) {
;     const bool h = fr & 8; const u32x4 recv = xor8_16B(h ? w0 : w1);
;     const u32x4 d1 = h ? recv : w0, d2 = h ? w1 : recv;
;     const int lane = fr + 16 * fq, src = ((lane >> 3) + 8 * ((lane >> 2) & 1) + 16 * (lane & 3)) * 4;
;     const u32x4 e1 = bperm_16B(src, d1), e2 = bperm_16B(src, d2);
;     bf16_t* p = O + (size_t)(r0 + (lane >> 3)) * ldc + c0 + 8 * (lane & 7);
;     *(u32x4*)p = e1; *(u32x4*)(p + 8 * ldc) = e2;
;     __device__ __forceinline__ void operator()(f32x4 (&acc)[2][2][4][2], const Unit& u, int wr, int wc, int fr, int fq) const {
;     ...
;             acc[ai][0][m][0] += rg[k][0]; acc[ai][0][m][1] += rg[k][1]; acc[ai][1][m][0] += rg[k][2]; acc[ai][1][m][1] += rg[k][3];
;             asm volatile("" : "+v"(acc[ai][0][m][0]), "+v"(acc[ai][0][m][1]), "+v"(acc[ai][1][m][0]), "+v"(acc[ai][1][m][1]) :: "memory"); }
;     ...
; #pragma unroll
;         for (int ai = 0; ai < 2; ++ai)
; #pragma unroll
;             for (int m = 0; m < 4; ++m) { const int row = u.pm * BM + wr * 64 + fr + ai * HALF + m * 16; float s = 0.f; u32x4 wx[2];
; #pragma unroll
;                 for (int bj = 0; bj < 2; ++bj) { const f32x4 v0 = acc[ai][bj][m][0], v1 = acc[ai][bj][m][1];
;                     s += (v0[0] * v0[0] + v0[1] * v0[1]) + (v0[2] * v0[2] + v0[3] * v0[3]) + (v1[0] * v1[0] + v1[1] * v1[1]) + (v1[2] * v1[2] + v1[3] * v1[3]);
;                     wx[bj] = pack8(v0, v1); }
;                 store_rows_bf16(xb, 1024, u.pm * BM + wr * 64 + ai * HALF + m * 16, u.pn * BM + wc * 64, fr, fq, wx[0], wx[1]);
;                 s += __shfl_xor(s, 16); s += __shfl_xor(s, 32);
;                 if (fq == 0) atomicAdd(ssq + row, s);
;                 asm volatile("" ::: "memory"); }
	v_pk_add_f32 v[72:73], v[72:73], v[214:215]
	v_pk_add_f32 v[70:71], v[70:71], v[212:213]
	v_add_co_u32_e32 v202, vcc, s88, v188
	v_lshl_add_u64 v[198:199], v[188:189], 0, s[50:51]
	s_nop 0
	v_addc_co_u32_e32 v203, vcc, 0, v189, vcc
	global_load_dwordx4 v[162:165], v[202:203], off
	s_nop 0
	global_load_dwordx4 v[198:201], v[198:199], off offset:16
	v_lshl_add_u64 v[188:189], v[188:189], 0, s[52:53]
	global_load_dwordx4 v[202:205], v[202:203], off offset:128
	s_nop 0
	global_load_dwordx4 v[206:209], v[188:189], off offset:16
	s_waitcnt vmcnt(11)
	v_pk_add_f32 v[48:49], v[48:49], v[136:137]
	s_waitcnt vmcnt(10)
	v_pk_add_f32 v[116:117], v[44:45], v[116:117]
	v_pk_add_f32 v[114:115], v[42:43], v[114:115]
	s_waitcnt vmcnt(8)
	v_pk_add_f32 v[44:45], v[36:37], v[140:141]
	v_pk_add_f32 v[42:43], v[34:35], v[138:139]
	v_pk_add_f32 v[46:47], v[46:47], v[134:135]
	v_pk_add_f32 v[40:41], v[40:41], v[144:145]
	v_pk_add_f32 v[38:39], v[38:39], v[142:143]
	s_waitcnt vmcnt(7)
	v_pk_add_f32 v[32:33], v[32:33], v[152:153]
	s_waitcnt vmcnt(6)
	v_pk_add_f32 v[36:37], v[28:29], v[148:149]
	v_pk_add_f32 v[34:35], v[26:27], v[146:147]
	s_waitcnt vmcnt(4)
	v_pk_add_f32 v[28:29], v[20:21], v[156:157]
	v_pk_add_f32 v[26:27], v[18:19], v[154:155]
	v_pk_add_f32 v[30:31], v[30:31], v[150:151]
	v_pk_add_f32 v[24:25], v[24:25], v[160:161]
	v_pk_add_f32 v[22:23], v[22:23], v[158:159]
	s_waitcnt vmcnt(3)
	v_pk_add_f32 v[16:17], v[16:17], v[164:165]
	s_waitcnt vmcnt(2)
	v_pk_add_f32 v[20:21], v[8:9], v[200:201]
	v_pk_add_f32 v[18:19], v[6:7], v[198:199]
	s_waitcnt vmcnt(1)
	v_pk_add_f32 v[8:9], v[12:13], v[204:205]
	v_pk_add_f32 v[6:7], v[10:11], v[202:203]
	v_mul_f32_e32 v11, v127, v127
	v_mul_f32_e32 v12, v129, v129
	v_fmac_f32_e32 v11, v126, v126
	v_fmac_f32_e32 v12, v128, v128
	v_add_f32_e32 v11, v11, v12
	v_mul_f32_e32 v12, v131, v131
	v_fmac_f32_e32 v12, v130, v130
	v_add_f32_e32 v11, v12, v11
	v_mul_f32_e32 v12, v133, v133
	v_pk_add_f32 v[14:15], v[14:15], v[162:163]
	s_waitcnt vmcnt(0)
	v_pk_add_f32 v[4:5], v[4:5], v[208:209]
	v_pk_add_f32 v[2:3], v[2:3], v[206:207]
	v_fmac_f32_e32 v12, v132, v132
	v_add_f32_e32 v11, v12, v11
	v_cvt_pk_bf16_f32 v13, v126, v127
	v_cvt_pk_bf16_f32 v126, v128, v129
	v_mul_f32_e32 v12, v119, v119
	v_mul_f32_e32 v129, v121, v121
	v_fmac_f32_e32 v12, v118, v118
	v_fmac_f32_e32 v129, v120, v120
	v_add_f32_e32 v12, v12, v129
	v_mul_f32_e32 v129, v123, v123
	v_fmac_f32_e32 v129, v122, v122
	v_add_f32_e32 v12, v129, v12
	v_mul_f32_e32 v129, v125, v125
	v_fmac_f32_e32 v129, v124, v124
	v_add_f32_e32 v12, v129, v12
	v_and_b32_e32 v129, 64, v196
	v_cvt_pk_bf16_f32 v127, v130, v131
	v_cvt_pk_bf16_f32 v128, v132, v133
	v_add_f32_e32 v12, v11, v12
	v_cvt_pk_bf16_f32 v11, v118, v119
	v_xor_b32_e32 v118, 8, v196
	v_add_u32_e32 v130, 64, v129
	v_cmp_lt_i32_e32 vcc, v118, v130
	v_cvt_pk_bf16_f32 v119, v120, v121
	v_cvt_pk_bf16_f32 v120, v122, v123
	v_cvt_pk_bf16_f32 v121, v124, v125
	v_cndmask_b32_e64 v125, v13, v11, s[4:5]
	v_cndmask_b32_e64 v122, v128, v121, s[4:5]
	v_cndmask_b32_e32 v118, v196, v118, vcc
	v_cndmask_b32_e64 v123, v127, v120, s[4:5]
	v_cndmask_b32_e64 v124, v126, v119, s[4:5]
	v_lshlrev_b32_e32 v118, 2, v118
	v_mov_b32_dpp v125, v125 row_ror:8 row_mask:0xf bank_mask:0xf
	v_mov_b32_dpp v124, v124 row_ror:8 row_mask:0xf bank_mask:0xf
	v_mov_b32_dpp v123, v123 row_ror:8 row_mask:0xf bank_mask:0xf
	v_mov_b32_dpp v122, v122 row_ror:8 row_mask:0xf bank_mask:0xf
	v_or_b32_e32 v10, s58, v191
	s_waitcnt lgkmcnt(0)
	v_cndmask_b32_e64 v13, v125, v13, s[4:5]
	s_waitcnt lgkmcnt(0)
	v_cndmask_b32_e64 v126, v124, v126, s[4:5]
	s_waitcnt lgkmcnt(0)
	v_cndmask_b32_e64 v127, v123, v127, s[4:5]
	s_waitcnt lgkmcnt(0)
	v_cndmask_b32_e64 v128, v122, v128, s[4:5]
	v_cndmask_b32_e64 v11, v11, v125, s[4:5]
	v_cndmask_b32_e64 v129, v121, v122, s[4:5]
	v_cndmask_b32_e64 v131, v120, v123, s[4:5]
	v_cndmask_b32_e64 v119, v119, v124, s[4:5]
	ds_bpermute_b32 v120, v192, v13
	ds_bpermute_b32 v121, v192, v126
	ds_bpermute_b32 v122, v192, v127
	ds_bpermute_b32 v123, v192, v128
	ds_bpermute_b32 v124, v192, v11
	v_ashrrev_i32_e32 v11, 31, v10
	ds_bpermute_b32 v127, v192, v129
	v_lshlrev_b64 v[128:129], 11, v[10:11]
	v_lshl_add_u64 v[128:129], s[24:25], 0, v[128:129]
	v_lshl_add_u64 v[128:129], s[56:57], 1, v[128:129]
	v_lshl_add_u64 v[128:129], v[128:129], 0, v[174:175]
	s_waitcnt lgkmcnt(2)
	global_store_dwordx4 v[128:129], v[120:123], off
	v_xor_b32_e32 v11, 16, v196
	ds_bpermute_b32 v125, v192, v119
	v_add_co_u32_e32 v120, vcc, s0, v128
	ds_bpermute_b32 v126, v192, v131
	s_nop 0
	v_addc_co_u32_e32 v121, vcc, 0, v129, vcc
	v_cmp_lt_i32_e32 vcc, v11, v130
	s_waitcnt lgkmcnt(0)
	global_store_dwordx4 v[120:121], v[124:127], off
	v_cndmask_b32_e32 v11, v196, v11, vcc
	v_lshlrev_b32_e32 v11, 2, v11
	ds_bpermute_b32 v13, v11, v12
	s_waitcnt lgkmcnt(0)
	v_add_f32_e32 v120, v12, v13
	v_xor_b32_e32 v12, 32, v196
	v_cmp_lt_i32_e32 vcc, v12, v130
	s_nop 1
	v_cndmask_b32_e32 v12, v196, v12, vcc
	v_lshlrev_b32_e32 v119, 2, v12
	ds_bpermute_b32 v121, v119, v120
	v_lshl_add_u64 v[12:13], v[186:187], 2, s[26:27]
	s_and_saveexec_b64 s[58:59], s[6:7]
	s_cbranch_execz .LBB0_1076
	s_waitcnt lgkmcnt(0)
	v_add_f32_e32 v120, v120, v121
	global_atomic_add_f32 v[12:13], v120, off
; __device__ __forceinline__ u32x4 pack8(const f32x4& v0, const f32x4& v1) { u32x4 w; w.x = cvt_pk_bf16(v0[0], v0[1]); w.y = cvt_pk_bf16(v0[2], v0[3]); w.z = cvt_pk_bf16(v1[0], v1[1]); w.w = cvt_pk_bf16(v1[2], v1[3]); return w; }
; __device__ __forceinline__ u32x4 xor8_16B(u32x4 v) { u32x4 r; r.x = (unsigned)__shfl_xor((int)v.x, 8); r.y = (unsigned)__shfl_xor((int)v.y, 8); r.z = (unsigned)__shfl_xor((int)v.z, 8); r.w = (unsigned)__shfl_xor((int)v.w, 8); return r; }
; __device__ __forceinline__ u32x4 bperm_16B(int src_byte, u32x4 v) { u32x4 r; r.x = (unsigned)__builtin_amdgcn_ds_bpermute(src_byte, (int)v.x); r.y = (unsigned)__builtin_amdgcn_ds_bpermute(src_byte, (int)v.y); r.z = (unsigned)__builtin_amdgcn_ds_bpermute(src_byte, (int)v.z); r.w = (unsigned)__builtin_amdgcn_ds_bpermute(src_byte, (int)v.w); return r; }
; __device__ __forceinline__ void store_rows_bf16(bf16_t* O, size_t ldc, int r0, int c0, int fr, int fq, u32x4 w0, u32x4 w1) {
;     const bool h = fr & 8; const u32x4 recv = xor8_16B(h ? w0 : w1);
;     const u32x4 d1 = h ? recv : w0, d2 = h ? w1 : recv;
;     const int lane = fr + 16 * fq, src = ((lane >> 3) + 8 * ((lane >> 2) & 1) + 16 * (lane & 3)) * 4;
;     const u32x4 e1 = bperm_16B(src, d1), e2 = bperm_16B(src, d2);
;     bf16_t* p = O + (size_t)(r0 + (lane >> 3)) * ldc + c0 + 8 * (lane & 7);
;     *(u32x4*)p = e1; *(u32x4*)(p + 8 * ldc) = e2;
;     __device__ __forceinline__ void operator()(f32x4 (&acc)[2][2][4][2], const Unit& u, int wr, int wc, int fr, int fq) const {
;     ...
;             for (int m = 0; m < 4; ++m) { const int row = u.pm * BM + wr * 64 + fr + ai * HALF + m * 16; float s = 0.f; u32x4 wx[2];
; #pragma unroll
;                 for (int bj = 0; bj < 2; ++bj) { const f32x4 v0 = acc[ai][bj][m][0], v1 = acc[ai][bj][m][1];
;                     s += (v0[0] * v0[0] + v0[1] * v0[1]) + (v0[2] * v0[2] + v0[3] * v0[3]) + (v1[0] * v1[0] + v1[1] * v1[1]) + (v1[2] * v1[2] + v1[3] * v1[3]);
;                     wx[bj] = pack8(v0, v1); }
;                 store_rows_bf16(xb, 1024, u.pm * BM + wr * 64 + ai * HALF + m * 16, u.pn * BM + wc * 64, fr, fq, wx[0], wx[1]);
;                 s += __shfl_xor(s, 16); s += __shfl_xor(s, 32);
;                 if (fq == 0) atomicAdd(ssq + row, s);
;                 asm volatile("" ::: "memory"); }
.LBB0_1076:
	s_or_b64 exec, exec, s[58:59]
	v_mul_f32_e32 v120, v59, v59
	s_waitcnt lgkmcnt(0)
	v_mul_f32_e32 v121, v61, v61
	v_fmac_f32_e32 v120, v58, v58
	v_fmac_f32_e32 v121, v60, v60
	v_add_f32_e32 v120, v120, v121
	v_mul_f32_e32 v121, v63, v63
	v_fmac_f32_e32 v121, v62, v62
	v_cvt_pk_bf16_f32 v58, v58, v59
	v_cvt_pk_bf16_f32 v59, v60, v61
	v_cvt_pk_bf16_f32 v60, v62, v63
	v_mul_f32_e32 v62, v51, v51
	v_mul_f32_e32 v63, v53, v53
	v_fmac_f32_e32 v62, v50, v50
	v_fmac_f32_e32 v63, v52, v52
	v_add_f32_e32 v62, v62, v63
	v_mul_f32_e32 v63, v55, v55
	v_fmac_f32_e32 v63, v54, v54
	v_cvt_pk_bf16_f32 v61, v64, v65
	v_add_f32_e32 v62, v63, v62
	v_mul_f32_e32 v63, v57, v57
	v_cvt_pk_bf16_f32 v50, v50, v51
	v_cvt_pk_bf16_f32 v51, v52, v53
	v_cvt_pk_bf16_f32 v52, v54, v55
	v_cvt_pk_bf16_f32 v53, v56, v57
	v_fmac_f32_e32 v63, v56, v56
	v_cndmask_b32_e64 v57, v58, v50, s[4:5]
	v_cndmask_b32_e64 v54, v61, v53, s[4:5]
	v_cndmask_b32_e64 v55, v60, v52, s[4:5]
	v_cndmask_b32_e64 v56, v59, v51, s[4:5]
	v_mov_b32_dpp v57, v57 row_ror:8 row_mask:0xf bank_mask:0xf
	v_mov_b32_dpp v54, v54 row_ror:8 row_mask:0xf bank_mask:0xf
	v_mov_b32_dpp v55, v55 row_ror:8 row_mask:0xf bank_mask:0xf
	v_mov_b32_dpp v56, v56 row_ror:8 row_mask:0xf bank_mask:0xf
	v_add_f32_e32 v120, v121, v120
	v_mul_f32_e32 v121, v65, v65
	v_fmac_f32_e32 v121, v64, v64
	v_add_f32_e32 v120, v121, v120
	v_add_f32_e32 v62, v63, v62
	s_waitcnt lgkmcnt(0)
	v_cndmask_b32_e64 v58, v57, v58, s[4:5]
	v_add_f32_e32 v62, v120, v62
	s_waitcnt lgkmcnt(0)
	v_cndmask_b32_e64 v61, v54, v61, s[4:5]
	s_waitcnt lgkmcnt(0)
	v_cndmask_b32_e64 v60, v55, v60, s[4:5]
	s_waitcnt lgkmcnt(0)
	v_cndmask_b32_e64 v59, v56, v59, s[4:5]
	v_cndmask_b32_e64 v63, v53, v54, s[4:5]
	v_cndmask_b32_e64 v54, v50, v57, s[4:5]
	ds_bpermute_b32 v50, v192, v58
	v_or_b32_e32 v58, 16, v10
	v_cndmask_b32_e64 v64, v52, v55, s[4:5]
	v_cndmask_b32_e64 v55, v51, v56, s[4:5]
	ds_bpermute_b32 v51, v192, v59
	ds_bpermute_b32 v52, v192, v60
	ds_bpermute_b32 v53, v192, v61
	v_ashrrev_i32_e32 v59, 31, v58
	ds_bpermute_b32 v60, v11, v62
	v_lshlrev_b64 v[58:59], 11, v[58:59]
	v_lshl_add_u64 v[58:59], s[24:25], 0, v[58:59]
	v_lshl_add_u64 v[58:59], s[56:57], 1, v[58:59]
	v_lshl_add_u64 v[58:59], v[58:59], 0, v[174:175]
	s_waitcnt lgkmcnt(1)
	global_store_dwordx4 v[58:59], v[50:53], off
	ds_bpermute_b32 v54, v192, v54
	ds_bpermute_b32 v55, v192, v55
	s_waitcnt lgkmcnt(2)
	v_add_f32_e32 v50, v62, v60
	ds_bpermute_b32 v56, v192, v64
	ds_bpermute_b32 v57, v192, v63
	ds_bpermute_b32 v51, v119, v50
	v_add_co_u32_e32 v52, vcc, 0x4000, v58
	s_nop 1
	v_addc_co_u32_e32 v53, vcc, 0, v59, vcc
	s_waitcnt lgkmcnt(1)
	global_store_dwordx4 v[52:53], v[54:57], off
	s_and_saveexec_b64 s[58:59], s[6:7]
	s_cbranch_execz .LBB0_1078
	s_waitcnt lgkmcnt(0)
	v_add_f32_e32 v50, v50, v51
	global_atomic_add_f32 v[12:13], v50, off offset:64
.LBB0_1078:
	s_or_b64 exec, exec, s[58:59]
	v_mul_f32_e32 v50, v107, v107
	s_waitcnt lgkmcnt(0)
	v_mul_f32_e32 v51, v109, v109
	v_mul_f32_e32 v55, v91, v91
	v_mul_f32_e32 v56, v93, v93
	v_fmac_f32_e32 v50, v106, v106
	v_fmac_f32_e32 v51, v108, v108
	v_fmac_f32_e32 v55, v90, v90
	v_fmac_f32_e32 v56, v92, v92
	v_add_f32_e32 v50, v50, v51
	v_mul_f32_e32 v51, v111, v111
	v_add_f32_e32 v55, v55, v56
	v_mul_f32_e32 v56, v95, v95
	v_fmac_f32_e32 v51, v110, v110
	v_fmac_f32_e32 v56, v94, v94
	v_add_f32_e32 v50, v51, v50
	v_mul_f32_e32 v51, v113, v113
	v_add_f32_e32 v55, v56, v55
	v_mul_f32_e32 v56, v97, v97
	v_fmac_f32_e32 v51, v112, v112
	v_fmac_f32_e32 v56, v96, v96
	v_add_f32_e32 v50, v51, v50
	v_cvt_pk_bf16_f32 v51, v106, v107
	v_cvt_pk_bf16_f32 v52, v108, v109
	v_cvt_pk_bf16_f32 v53, v110, v111
	v_cvt_pk_bf16_f32 v54, v112, v113
	v_add_f32_e32 v55, v56, v55
	v_cvt_pk_bf16_f32 v56, v90, v91
	v_cvt_pk_bf16_f32 v57, v92, v93
	v_cvt_pk_bf16_f32 v58, v94, v95
	v_cvt_pk_bf16_f32 v59, v96, v97
	v_add_f32_e32 v64, v50, v55
	v_cndmask_b32_e64 v60, v54, v59, s[4:5]
	v_cndmask_b32_e64 v61, v53, v58, s[4:5]
	v_cndmask_b32_e64 v62, v52, v57, s[4:5]
	v_cndmask_b32_e64 v63, v51, v56, s[4:5]
	v_mov_b32_dpp v60, v60 row_ror:8 row_mask:0xf bank_mask:0xf
	v_mov_b32_dpp v61, v61 row_ror:8 row_mask:0xf bank_mask:0xf
	v_mov_b32_dpp v62, v62 row_ror:8 row_mask:0xf bank_mask:0xf
	v_mov_b32_dpp v63, v63 row_ror:8 row_mask:0xf bank_mask:0xf
	s_waitcnt lgkmcnt(0)
	v_cndmask_b32_e64 v54, v60, v54, s[4:5]
	s_waitcnt lgkmcnt(0)
	v_cndmask_b32_e64 v53, v61, v53, s[4:5]
	s_waitcnt lgkmcnt(0)
	v_cndmask_b32_e64 v52, v62, v52, s[4:5]
	v_cndmask_b32_e64 v58, v58, v61, s[4:5]
	s_waitcnt lgkmcnt(0)
	v_cndmask_b32_e64 v56, v56, v63, s[4:5]
	v_cndmask_b32_e64 v50, v63, v51, s[4:5]
	v_cndmask_b32_e64 v59, v59, v60, s[4:5]
	ds_bpermute_b32 v51, v192, v52
	ds_bpermute_b32 v52, v192, v53
	ds_bpermute_b32 v53, v192, v54
	ds_bpermute_b32 v54, v192, v56
	ds_bpermute_b32 v56, v192, v58
	v_or_b32_e32 v58, 32, v10
	v_cndmask_b32_e64 v55, v57, v62, s[4:5]
	ds_bpermute_b32 v50, v192, v50
	ds_bpermute_b32 v57, v192, v59
	v_ashrrev_i32_e32 v59, 31, v58
	ds_bpermute_b32 v60, v11, v64
	v_lshlrev_b64 v[58:59], 11, v[58:59]
	v_lshl_add_u64 v[58:59], s[24:25], 0, v[58:59]
	v_lshl_add_u64 v[58:59], s[56:57], 1, v[58:59]
	v_lshl_add_u64 v[58:59], v[58:59], 0, v[174:175]
	s_waitcnt lgkmcnt(2)
	global_store_dwordx4 v[58:59], v[50:53], off
	ds_bpermute_b32 v55, v192, v55
	s_waitcnt lgkmcnt(1)
	v_add_f32_e32 v50, v64, v60
	ds_bpermute_b32 v51, v119, v50
	v_add_co_u32_e32 v52, vcc, 0x4000, v58
	s_nop 1
	v_addc_co_u32_e32 v53, vcc, 0, v59, vcc
	s_waitcnt lgkmcnt(1)
	global_store_dwordx4 v[52:53], v[54:57], off
	s_and_saveexec_b64 s[58:59], s[6:7]
	s_cbranch_execz .LBB0_1080
	s_waitcnt lgkmcnt(0)
	v_add_f32_e32 v50, v50, v51
	global_atomic_add_f32 v[12:13], v50, off offset:128
; __device__ __forceinline__ u32x4 pack8(const f32x4& v0, const f32x4& v1) { u32x4 w; w.x = cvt_pk_bf16(v0[0], v0[1]); w.y = cvt_pk_bf16(v0[2], v0[3]); w.z = cvt_pk_bf16(v1[0], v1[1]); w.w = cvt_pk_bf16(v1[2], v1[3]); return w; }
; __device__ __forceinline__ u32x4 xor8_16B(u32x4 v) { u32x4 r; r.x = (unsigned)__shfl_xor((int)v.x, 8); r.y = (unsigned)__shfl_xor((int)v.y, 8); r.z = (unsigned)__shfl_xor((int)v.z, 8); r.w = (unsigned)__shfl_xor((int)v.w, 8); return r; }
; __device__ __forceinline__ u32x4 bperm_16B(int src_byte, u32x4 v) { u32x4 r; r.x = (unsigned)__builtin_amdgcn_ds_bpermute(src_byte, (int)v.x); r.y = (unsigned)__builtin_amdgcn_ds_bpermute(src_byte, (int)v.y); r.z = (unsigned)__builtin_amdgcn_ds_bpermute(src_byte, (int)v.z); r.w = (unsigned)__builtin_amdgcn_ds_bpermute(src_byte, (int)v.w); return r; }
; __device__ __forceinline__ void store_rows_bf16(bf16_t* O, size_t ldc, int r0, int c0, int fr, int fq, u32x4 w0, u32x4 w1) {
;     const bool h = fr & 8; const u32x4 recv = xor8_16B(h ? w0 : w1);
;     const u32x4 d1 = h ? recv : w0, d2 = h ? w1 : recv;
;     const int lane = fr + 16 * fq, src = ((lane >> 3) + 8 * ((lane >> 2) & 1) + 16 * (lane & 3)) * 4;
;     const u32x4 e1 = bperm_16B(src, d1), e2 = bperm_16B(src, d2);
;     bf16_t* p = O + (size_t)(r0 + (lane >> 3)) * ldc + c0 + 8 * (lane & 7);
;     *(u32x4*)p = e1; *(u32x4*)(p + 8 * ldc) = e2;
;     __device__ __forceinline__ void operator()(f32x4 (&acc)[2][2][4][2], const Unit& u, int wr, int wc, int fr, int fq) const {
;     ...
;             for (int m = 0; m < 4; ++m) { const int row = u.pm * BM + wr * 64 + fr + ai * HALF + m * 16; float s = 0.f; u32x4 wx[2];
; #pragma unroll
;                 for (int bj = 0; bj < 2; ++bj) { const f32x4 v0 = acc[ai][bj][m][0], v1 = acc[ai][bj][m][1];
;                     s += (v0[0] * v0[0] + v0[1] * v0[1]) + (v0[2] * v0[2] + v0[3] * v0[3]) + (v1[0] * v1[0] + v1[1] * v1[1]) + (v1[2] * v1[2] + v1[3] * v1[3]);
;                     wx[bj] = pack8(v0, v1); }
;                 store_rows_bf16(xb, 1024, u.pm * BM + wr * 64 + ai * HALF + m * 16, u.pn * BM + wc * 64, fr, fq, wx[0], wx[1]);
;                 s += __shfl_xor(s, 16); s += __shfl_xor(s, 32);
;                 if (fq == 0) atomicAdd(ssq + row, s);
;                 asm volatile("" ::: "memory"); }
.LBB0_1080:
	s_or_b64 exec, exec, s[58:59]
	v_mul_f32_e32 v50, v99, v99
	s_waitcnt lgkmcnt(0)
	v_mul_f32_e32 v51, v101, v101
	v_mul_f32_e32 v55, v75, v75
	v_mul_f32_e32 v56, v77, v77
	v_fmac_f32_e32 v50, v98, v98
	v_fmac_f32_e32 v51, v100, v100
	v_fmac_f32_e32 v55, v74, v74
	v_fmac_f32_e32 v56, v76, v76
	v_add_f32_e32 v50, v50, v51
	v_mul_f32_e32 v51, v103, v103
	v_add_f32_e32 v55, v55, v56
	v_mul_f32_e32 v56, v79, v79
	v_fmac_f32_e32 v51, v102, v102
	v_fmac_f32_e32 v56, v78, v78
	v_add_f32_e32 v50, v51, v50
	v_mul_f32_e32 v51, v105, v105
	v_add_f32_e32 v55, v56, v55
	v_mul_f32_e32 v56, v81, v81
	v_fmac_f32_e32 v51, v104, v104
	v_fmac_f32_e32 v56, v80, v80
	v_add_f32_e32 v50, v51, v50
	v_cvt_pk_bf16_f32 v51, v98, v99
	v_cvt_pk_bf16_f32 v52, v100, v101
	v_cvt_pk_bf16_f32 v53, v102, v103
	v_cvt_pk_bf16_f32 v54, v104, v105
	v_add_f32_e32 v55, v56, v55
	v_cvt_pk_bf16_f32 v56, v74, v75
	v_cvt_pk_bf16_f32 v57, v76, v77
	v_cvt_pk_bf16_f32 v58, v78, v79
	v_cvt_pk_bf16_f32 v59, v80, v81
	v_add_f32_e32 v64, v50, v55
	v_cndmask_b32_e64 v60, v54, v59, s[4:5]
	v_cndmask_b32_e64 v61, v53, v58, s[4:5]
	v_cndmask_b32_e64 v62, v52, v57, s[4:5]
	v_cndmask_b32_e64 v63, v51, v56, s[4:5]
	v_mov_b32_dpp v60, v60 row_ror:8 row_mask:0xf bank_mask:0xf
	v_mov_b32_dpp v61, v61 row_ror:8 row_mask:0xf bank_mask:0xf
	v_mov_b32_dpp v62, v62 row_ror:8 row_mask:0xf bank_mask:0xf
	v_mov_b32_dpp v63, v63 row_ror:8 row_mask:0xf bank_mask:0xf
	s_waitcnt lgkmcnt(0)
	v_cndmask_b32_e64 v54, v60, v54, s[4:5]
	s_waitcnt lgkmcnt(0)
	v_cndmask_b32_e64 v53, v61, v53, s[4:5]
	s_waitcnt lgkmcnt(0)
	v_cndmask_b32_e64 v52, v62, v52, s[4:5]
	v_cndmask_b32_e64 v58, v58, v61, s[4:5]
	s_waitcnt lgkmcnt(0)
	v_cndmask_b32_e64 v56, v56, v63, s[4:5]
	v_cndmask_b32_e64 v50, v63, v51, s[4:5]
	v_cndmask_b32_e64 v59, v59, v60, s[4:5]
	ds_bpermute_b32 v51, v192, v52
	ds_bpermute_b32 v52, v192, v53
	ds_bpermute_b32 v53, v192, v54
	ds_bpermute_b32 v54, v192, v56
	ds_bpermute_b32 v56, v192, v58
	v_or_b32_e32 v58, 48, v10
	v_cndmask_b32_e64 v55, v57, v62, s[4:5]
	ds_bpermute_b32 v50, v192, v50
	ds_bpermute_b32 v57, v192, v59
	v_ashrrev_i32_e32 v59, 31, v58
	ds_bpermute_b32 v60, v11, v64
	v_lshlrev_b64 v[58:59], 11, v[58:59]
	v_lshl_add_u64 v[58:59], s[24:25], 0, v[58:59]
	v_lshl_add_u64 v[58:59], s[56:57], 1, v[58:59]
	v_lshl_add_u64 v[58:59], v[58:59], 0, v[174:175]
	s_waitcnt lgkmcnt(2)
	global_store_dwordx4 v[58:59], v[50:53], off
	ds_bpermute_b32 v55, v192, v55
	s_waitcnt lgkmcnt(1)
	v_add_f32_e32 v50, v64, v60
	ds_bpermute_b32 v51, v119, v50
	v_add_co_u32_e32 v52, vcc, 0x4000, v58
	s_nop 1
	v_addc_co_u32_e32 v53, vcc, 0, v59, vcc
	s_waitcnt lgkmcnt(1)
	global_store_dwordx4 v[52:53], v[54:57], off
	s_and_saveexec_b64 s[58:59], s[6:7]
	s_cbranch_execz .LBB0_1082
	s_waitcnt lgkmcnt(0)
	v_add_f32_e32 v50, v50, v51
	global_atomic_add_f32 v[12:13], v50, off offset:192
.LBB0_1082:
	s_or_b64 exec, exec, s[58:59]
	v_mul_f32_e32 v50, v83, v83
	s_waitcnt lgkmcnt(0)
	v_mul_f32_e32 v51, v85, v85
	v_mul_f32_e32 v55, v67, v67
	v_mul_f32_e32 v56, v69, v69
	v_fmac_f32_e32 v50, v82, v82
	v_fmac_f32_e32 v51, v84, v84
	v_fmac_f32_e32 v55, v66, v66
	v_fmac_f32_e32 v56, v68, v68
	v_add_f32_e32 v50, v50, v51
	v_mul_f32_e32 v51, v87, v87
	v_add_f32_e32 v55, v55, v56
	v_mul_f32_e32 v56, v71, v71
	v_fmac_f32_e32 v51, v86, v86
	v_fmac_f32_e32 v56, v70, v70
	v_add_f32_e32 v50, v51, v50
	v_mul_f32_e32 v51, v89, v89
	v_add_f32_e32 v55, v56, v55
	v_mul_f32_e32 v56, v73, v73
	v_fmac_f32_e32 v51, v88, v88
	v_fmac_f32_e32 v56, v72, v72
	v_add_f32_e32 v50, v51, v50
	v_cvt_pk_bf16_f32 v51, v82, v83
	v_cvt_pk_bf16_f32 v52, v84, v85
	v_cvt_pk_bf16_f32 v53, v86, v87
	v_cvt_pk_bf16_f32 v54, v88, v89
	v_add_f32_e32 v55, v56, v55
	v_cvt_pk_bf16_f32 v56, v66, v67
	v_cvt_pk_bf16_f32 v57, v68, v69
	v_cvt_pk_bf16_f32 v59, v70, v71
	v_cvt_pk_bf16_f32 v60, v72, v73
	v_add_u32_e32 v58, 0x80, v10
	v_cndmask_b32_e64 v61, v54, v60, s[4:5]
	v_cndmask_b32_e64 v62, v53, v59, s[4:5]
	v_cndmask_b32_e64 v63, v52, v57, s[4:5]
	v_cndmask_b32_e64 v64, v51, v56, s[4:5]
	v_mov_b32_dpp v61, v61 row_ror:8 row_mask:0xf bank_mask:0xf
	v_mov_b32_dpp v62, v62 row_ror:8 row_mask:0xf bank_mask:0xf
	v_mov_b32_dpp v63, v63 row_ror:8 row_mask:0xf bank_mask:0xf
	v_mov_b32_dpp v64, v64 row_ror:8 row_mask:0xf bank_mask:0xf
	v_add_f32_e32 v65, v50, v55
	s_waitcnt lgkmcnt(0)
	v_cndmask_b32_e64 v54, v61, v54, s[4:5]
	s_waitcnt lgkmcnt(0)
	v_cndmask_b32_e64 v53, v62, v53, s[4:5]
	s_waitcnt lgkmcnt(0)
	v_cndmask_b32_e64 v52, v63, v52, s[4:5]
	s_waitcnt lgkmcnt(0)
	v_cndmask_b32_e64 v50, v64, v51, s[4:5]
	v_cndmask_b32_e64 v60, v60, v61, s[4:5]
	v_cndmask_b32_e64 v59, v59, v62, s[4:5]
	v_cndmask_b32_e64 v56, v56, v64, s[4:5]
	v_cndmask_b32_e64 v55, v57, v63, s[4:5]
	ds_bpermute_b32 v50, v192, v50
	ds_bpermute_b32 v51, v192, v52
	ds_bpermute_b32 v52, v192, v53
	ds_bpermute_b32 v53, v192, v54
	ds_bpermute_b32 v54, v192, v56
	ds_bpermute_b32 v56, v192, v59
	ds_bpermute_b32 v57, v192, v60
	v_ashrrev_i32_e32 v59, 31, v58
	ds_bpermute_b32 v60, v11, v65
	v_lshlrev_b64 v[58:59], 11, v[58:59]
	v_lshl_add_u64 v[58:59], s[24:25], 0, v[58:59]
	v_lshl_add_u64 v[58:59], s[56:57], 1, v[58:59]
	v_lshl_add_u64 v[58:59], v[58:59], 0, v[174:175]
	s_waitcnt lgkmcnt(4)
	global_store_dwordx4 v[58:59], v[50:53], off
	ds_bpermute_b32 v55, v192, v55
	s_waitcnt lgkmcnt(1)
	v_add_f32_e32 v50, v65, v60
	ds_bpermute_b32 v51, v119, v50
	v_add_co_u32_e32 v52, vcc, 0x4000, v58
	s_nop 1
	v_addc_co_u32_e32 v53, vcc, 0, v59, vcc
	s_waitcnt lgkmcnt(1)
	global_store_dwordx4 v[52:53], v[54:57], off
	s_and_saveexec_b64 s[58:59], s[6:7]
	s_cbranch_execz .LBB0_1084
	s_waitcnt lgkmcnt(0)
	v_add_f32_e32 v50, v50, v51
	global_atomic_add_f32 v[12:13], v50, off offset:512
; __device__ __forceinline__ u32x4 pack8(const f32x4& v0, const f32x4& v1) { u32x4 w; w.x = cvt_pk_bf16(v0[0], v0[1]); w.y = cvt_pk_bf16(v0[2], v0[3]); w.z = cvt_pk_bf16(v1[0], v1[1]); w.w = cvt_pk_bf16(v1[2], v1[3]); return w; }
; __device__ __forceinline__ u32x4 xor8_16B(u32x4 v) { u32x4 r; r.x = (unsigned)__shfl_xor((int)v.x, 8); r.y = (unsigned)__shfl_xor((int)v.y, 8); r.z = (unsigned)__shfl_xor((int)v.z, 8); r.w = (unsigned)__shfl_xor((int)v.w, 8); return r; }
; __device__ __forceinline__ u32x4 bperm_16B(int src_byte, u32x4 v) { u32x4 r; r.x = (unsigned)__builtin_amdgcn_ds_bpermute(src_byte, (int)v.x); r.y = (unsigned)__builtin_amdgcn_ds_bpermute(src_byte, (int)v.y); r.z = (unsigned)__builtin_amdgcn_ds_bpermute(src_byte, (int)v.z); r.w = (unsigned)__builtin_amdgcn_ds_bpermute(src_byte, (int)v.w); return r; }
; __device__ __forceinline__ void store_rows_bf16(bf16_t* O, size_t ldc, int r0, int c0, int fr, int fq, u32x4 w0, u32x4 w1) {
;     const bool h = fr & 8; const u32x4 recv = xor8_16B(h ? w0 : w1);
;     const u32x4 d1 = h ? recv : w0, d2 = h ? w1 : recv;
;     const int lane = fr + 16 * fq, src = ((lane >> 3) + 8 * ((lane >> 2) & 1) + 16 * (lane & 3)) * 4;
;     const u32x4 e1 = bperm_16B(src, d1), e2 = bperm_16B(src, d2);
;     bf16_t* p = O + (size_t)(r0 + (lane >> 3)) * ldc + c0 + 8 * (lane & 7);
;     *(u32x4*)p = e1; *(u32x4*)(p + 8 * ldc) = e2;
;     __device__ __forceinline__ void operator()(f32x4 (&acc)[2][2][4][2], const Unit& u, int wr, int wc, int fr, int fq) const {
;     ...
;             for (int m = 0; m < 4; ++m) { const int row = u.pm * BM + wr * 64 + fr + ai * HALF + m * 16; float s = 0.f; u32x4 wx[2];
; #pragma unroll
;                 for (int bj = 0; bj < 2; ++bj) { const f32x4 v0 = acc[ai][bj][m][0], v1 = acc[ai][bj][m][1];
;                     s += (v0[0] * v0[0] + v0[1] * v0[1]) + (v0[2] * v0[2] + v0[3] * v0[3]) + (v1[0] * v1[0] + v1[1] * v1[1]) + (v1[2] * v1[2] + v1[3] * v1[3]);
;                     wx[bj] = pack8(v0, v1); }
;                 store_rows_bf16(xb, 1024, u.pm * BM + wr * 64 + ai * HALF + m * 16, u.pn * BM + wc * 64, fr, fq, wx[0], wx[1]);
;                 s += __shfl_xor(s, 16); s += __shfl_xor(s, 32);
;                 if (fq == 0) atomicAdd(ssq + row, s);
;                 asm volatile("" ::: "memory"); }
.LBB0_1084:
	s_or_b64 exec, exec, s[58:59]
	v_mul_f32_e32 v50, v47, v47
	s_waitcnt lgkmcnt(0)
	v_mul_f32_e32 v51, v49, v49
	v_fmac_f32_e32 v50, v46, v46
	v_fmac_f32_e32 v51, v48, v48
	v_add_f32_e32 v50, v50, v51
	v_mul_f32_e32 v51, v115, v115
	v_fmac_f32_e32 v51, v114, v114
	v_add_f32_e32 v50, v51, v50
	v_mul_f32_e32 v51, v117, v117
	v_fmac_f32_e32 v51, v116, v116
	v_add_f32_e32 v50, v51, v50
	v_mul_f32_e32 v51, v39, v39
	v_mul_f32_e32 v52, v41, v41
	v_fmac_f32_e32 v51, v38, v38
	v_fmac_f32_e32 v52, v40, v40
	v_add_f32_e32 v51, v51, v52
	v_mul_f32_e32 v52, v43, v43
	v_fmac_f32_e32 v52, v42, v42
	v_cvt_pk_bf16_f32 v46, v46, v47
	v_cvt_pk_bf16_f32 v47, v48, v49
	v_cvt_pk_bf16_f32 v48, v114, v115
	v_cvt_pk_bf16_f32 v49, v116, v117
	v_add_f32_e32 v51, v52, v51
	v_mul_f32_e32 v52, v45, v45
	v_cvt_pk_bf16_f32 v38, v38, v39
	v_cvt_pk_bf16_f32 v39, v40, v41
	v_cvt_pk_bf16_f32 v40, v42, v43
	v_cvt_pk_bf16_f32 v41, v44, v45
	v_fmac_f32_e32 v52, v44, v44
	v_cndmask_b32_e64 v45, v46, v38, s[4:5]
	v_cndmask_b32_e64 v42, v49, v41, s[4:5]
	v_cndmask_b32_e64 v43, v48, v40, s[4:5]
	v_cndmask_b32_e64 v44, v47, v39, s[4:5]
	v_mov_b32_dpp v45, v45 row_ror:8 row_mask:0xf bank_mask:0xf
	v_mov_b32_dpp v42, v42 row_ror:8 row_mask:0xf bank_mask:0xf
	v_mov_b32_dpp v43, v43 row_ror:8 row_mask:0xf bank_mask:0xf
	v_mov_b32_dpp v44, v44 row_ror:8 row_mask:0xf bank_mask:0xf
	v_add_f32_e32 v51, v52, v51
	s_waitcnt lgkmcnt(0)
	v_cndmask_b32_e64 v46, v45, v46, s[4:5]
	v_add_f32_e32 v50, v50, v51
	s_waitcnt lgkmcnt(0)
	v_cndmask_b32_e64 v49, v42, v49, s[4:5]
	s_waitcnt lgkmcnt(0)
	v_cndmask_b32_e64 v48, v43, v48, s[4:5]
	s_waitcnt lgkmcnt(0)
	v_cndmask_b32_e64 v47, v44, v47, s[4:5]
	v_cndmask_b32_e64 v51, v41, v42, s[4:5]
	v_cndmask_b32_e64 v42, v38, v45, s[4:5]
	ds_bpermute_b32 v38, v192, v46
	v_add_u32_e32 v46, 0x90, v10
	v_cndmask_b32_e64 v52, v40, v43, s[4:5]
	v_cndmask_b32_e64 v43, v39, v44, s[4:5]
	ds_bpermute_b32 v39, v192, v47
	ds_bpermute_b32 v40, v192, v48
	ds_bpermute_b32 v41, v192, v49
	v_ashrrev_i32_e32 v47, 31, v46
	ds_bpermute_b32 v48, v11, v50
	v_lshlrev_b64 v[46:47], 11, v[46:47]
	v_lshl_add_u64 v[46:47], s[24:25], 0, v[46:47]
	v_lshl_add_u64 v[46:47], s[56:57], 1, v[46:47]
	v_lshl_add_u64 v[46:47], v[46:47], 0, v[174:175]
	s_waitcnt lgkmcnt(1)
	global_store_dwordx4 v[46:47], v[38:41], off
	ds_bpermute_b32 v42, v192, v42
	ds_bpermute_b32 v43, v192, v43
	s_waitcnt lgkmcnt(2)
	v_add_f32_e32 v38, v50, v48
	ds_bpermute_b32 v44, v192, v52
	ds_bpermute_b32 v45, v192, v51
	ds_bpermute_b32 v39, v119, v38
	v_add_co_u32_e32 v40, vcc, 0x4000, v46
	s_nop 1
	v_addc_co_u32_e32 v41, vcc, 0, v47, vcc
	s_waitcnt lgkmcnt(1)
	global_store_dwordx4 v[40:41], v[42:45], off
	s_and_saveexec_b64 s[58:59], s[6:7]
	s_cbranch_execz .LBB0_1086
	s_waitcnt lgkmcnt(0)
	v_add_f32_e32 v38, v38, v39
	global_atomic_add_f32 v[12:13], v38, off offset:576
; __device__ __forceinline__ u32x4 pack8(const f32x4& v0, const f32x4& v1) { u32x4 w; w.x = cvt_pk_bf16(v0[0], v0[1]); w.y = cvt_pk_bf16(v0[2], v0[3]); w.z = cvt_pk_bf16(v1[0], v1[1]); w.w = cvt_pk_bf16(v1[2], v1[3]); return w; }
; __device__ __forceinline__ u32x4 xor8_16B(u32x4 v) { u32x4 r; r.x = (unsigned)__shfl_xor((int)v.x, 8); r.y = (unsigned)__shfl_xor((int)v.y, 8); r.z = (unsigned)__shfl_xor((int)v.z, 8); r.w = (unsigned)__shfl_xor((int)v.w, 8); return r; }
; __device__ __forceinline__ u32x4 bperm_16B(int src_byte, u32x4 v) { u32x4 r; r.x = (unsigned)__builtin_amdgcn_ds_bpermute(src_byte, (int)v.x); r.y = (unsigned)__builtin_amdgcn_ds_bpermute(src_byte, (int)v.y); r.z = (unsigned)__builtin_amdgcn_ds_bpermute(src_byte, (int)v.z); r.w = (unsigned)__builtin_amdgcn_ds_bpermute(src_byte, (int)v.w); return r; }
; __device__ __forceinline__ void store_rows_bf16(bf16_t* O, size_t ldc, int r0, int c0, int fr, int fq, u32x4 w0, u32x4 w1) {
;     const bool h = fr & 8; const u32x4 recv = xor8_16B(h ? w0 : w1);
;     const u32x4 d1 = h ? recv : w0, d2 = h ? w1 : recv;
;     const int lane = fr + 16 * fq, src = ((lane >> 3) + 8 * ((lane >> 2) & 1) + 16 * (lane & 3)) * 4;
;     const u32x4 e1 = bperm_16B(src, d1), e2 = bperm_16B(src, d2);
;     bf16_t* p = O + (size_t)(r0 + (lane >> 3)) * ldc + c0 + 8 * (lane & 7);
;     *(u32x4*)p = e1; *(u32x4*)(p + 8 * ldc) = e2;
;     __device__ __forceinline__ void operator()(f32x4 (&acc)[2][2][4][2], const Unit& u, int wr, int wc, int fr, int fq) const {
;     ...
;             for (int m = 0; m < 4; ++m) { const int row = u.pm * BM + wr * 64 + fr + ai * HALF + m * 16; float s = 0.f; u32x4 wx[2];
; #pragma unroll
;                 for (int bj = 0; bj < 2; ++bj) { const f32x4 v0 = acc[ai][bj][m][0], v1 = acc[ai][bj][m][1];
;                     s += (v0[0] * v0[0] + v0[1] * v0[1]) + (v0[2] * v0[2] + v0[3] * v0[3]) + (v1[0] * v1[0] + v1[1] * v1[1]) + (v1[2] * v1[2] + v1[3] * v1[3]);
;                     wx[bj] = pack8(v0, v1); }
;                 store_rows_bf16(xb, 1024, u.pm * BM + wr * 64 + ai * HALF + m * 16, u.pn * BM + wc * 64, fr, fq, wx[0], wx[1]);
;                 s += __shfl_xor(s, 16); s += __shfl_xor(s, 32);
;                 if (fq == 0) atomicAdd(ssq + row, s);
;                 asm volatile("" ::: "memory"); }
.LBB0_1086:
	s_or_b64 exec, exec, s[58:59]
	v_mul_f32_e32 v38, v31, v31
	s_waitcnt lgkmcnt(0)
	v_mul_f32_e32 v39, v33, v33
	v_fmac_f32_e32 v38, v30, v30
	v_fmac_f32_e32 v39, v32, v32
	v_add_f32_e32 v38, v38, v39
	v_mul_f32_e32 v39, v35, v35
	v_fmac_f32_e32 v39, v34, v34
	v_cvt_pk_bf16_f32 v30, v30, v31
	v_cvt_pk_bf16_f32 v31, v32, v33
	v_cvt_pk_bf16_f32 v32, v34, v35
	v_mul_f32_e32 v34, v23, v23
	v_mul_f32_e32 v35, v25, v25
	v_fmac_f32_e32 v34, v22, v22
	v_fmac_f32_e32 v35, v24, v24
	v_add_f32_e32 v34, v34, v35
	v_mul_f32_e32 v35, v27, v27
	v_fmac_f32_e32 v35, v26, v26
	v_cvt_pk_bf16_f32 v33, v36, v37
	v_add_f32_e32 v34, v35, v34
	v_mul_f32_e32 v35, v29, v29
	v_cvt_pk_bf16_f32 v22, v22, v23
	v_cvt_pk_bf16_f32 v23, v24, v25
	v_cvt_pk_bf16_f32 v24, v26, v27
	v_cvt_pk_bf16_f32 v25, v28, v29
	v_fmac_f32_e32 v35, v28, v28
	v_cndmask_b32_e64 v29, v30, v22, s[4:5]
	v_cndmask_b32_e64 v26, v33, v25, s[4:5]
	v_cndmask_b32_e64 v27, v32, v24, s[4:5]
	v_cndmask_b32_e64 v28, v31, v23, s[4:5]
	v_mov_b32_dpp v29, v29 row_ror:8 row_mask:0xf bank_mask:0xf
	v_mov_b32_dpp v26, v26 row_ror:8 row_mask:0xf bank_mask:0xf
	v_mov_b32_dpp v27, v27 row_ror:8 row_mask:0xf bank_mask:0xf
	v_mov_b32_dpp v28, v28 row_ror:8 row_mask:0xf bank_mask:0xf
	v_add_f32_e32 v38, v39, v38
	v_mul_f32_e32 v39, v37, v37
	v_fmac_f32_e32 v39, v36, v36
	v_add_f32_e32 v38, v39, v38
	v_add_f32_e32 v34, v35, v34
	s_waitcnt lgkmcnt(0)
	v_cndmask_b32_e64 v30, v29, v30, s[4:5]
	v_add_f32_e32 v34, v38, v34
	s_waitcnt lgkmcnt(0)
	v_cndmask_b32_e64 v33, v26, v33, s[4:5]
	s_waitcnt lgkmcnt(0)
	v_cndmask_b32_e64 v32, v27, v32, s[4:5]
	s_waitcnt lgkmcnt(0)
	v_cndmask_b32_e64 v31, v28, v31, s[4:5]
	v_cndmask_b32_e64 v35, v25, v26, s[4:5]
	v_cndmask_b32_e64 v26, v22, v29, s[4:5]
	ds_bpermute_b32 v22, v192, v30
	v_add_u32_e32 v30, 0xa0, v10
	v_cndmask_b32_e64 v36, v24, v27, s[4:5]
	v_cndmask_b32_e64 v27, v23, v28, s[4:5]
	ds_bpermute_b32 v23, v192, v31
	ds_bpermute_b32 v24, v192, v32
	ds_bpermute_b32 v25, v192, v33
	v_ashrrev_i32_e32 v31, 31, v30
	ds_bpermute_b32 v32, v11, v34
	v_lshlrev_b64 v[30:31], 11, v[30:31]
	v_lshl_add_u64 v[30:31], s[24:25], 0, v[30:31]
	v_lshl_add_u64 v[30:31], s[56:57], 1, v[30:31]
	v_lshl_add_u64 v[30:31], v[30:31], 0, v[174:175]
	s_waitcnt lgkmcnt(1)
	global_store_dwordx4 v[30:31], v[22:25], off
	ds_bpermute_b32 v26, v192, v26
	ds_bpermute_b32 v27, v192, v27
	s_waitcnt lgkmcnt(2)
	v_add_f32_e32 v22, v34, v32
	ds_bpermute_b32 v28, v192, v36
	ds_bpermute_b32 v29, v192, v35
	ds_bpermute_b32 v23, v119, v22
	v_add_co_u32_e32 v24, vcc, 0x4000, v30
	s_nop 1
	v_addc_co_u32_e32 v25, vcc, 0, v31, vcc
	s_waitcnt lgkmcnt(1)
	global_store_dwordx4 v[24:25], v[26:29], off
	s_and_saveexec_b64 s[58:59], s[6:7]
	s_cbranch_execz .LBB0_1088
	s_waitcnt lgkmcnt(0)
	v_add_f32_e32 v22, v22, v23
	global_atomic_add_f32 v[12:13], v22, off offset:640
.LBB0_1088:
	s_or_b64 exec, exec, s[58:59]
	v_mul_f32_e32 v22, v15, v15
	s_waitcnt lgkmcnt(0)
	v_mul_f32_e32 v23, v17, v17
	v_fmac_f32_e32 v22, v14, v14
	v_fmac_f32_e32 v23, v16, v16
	v_add_f32_e32 v22, v22, v23
	v_mul_f32_e32 v23, v19, v19
	v_fmac_f32_e32 v23, v18, v18
	v_cvt_pk_bf16_f32 v14, v14, v15
	v_cvt_pk_bf16_f32 v15, v16, v17
	v_cvt_pk_bf16_f32 v16, v18, v19
	v_mul_f32_e32 v18, v7, v7
	v_mul_f32_e32 v19, v9, v9
	v_fmac_f32_e32 v18, v6, v6
	v_fmac_f32_e32 v19, v8, v8
	v_add_f32_e32 v18, v18, v19
	v_mul_f32_e32 v19, v3, v3
	v_fmac_f32_e32 v19, v2, v2
	v_cvt_pk_bf16_f32 v17, v20, v21
	v_add_f32_e32 v18, v19, v18
	v_mul_f32_e32 v19, v5, v5
	v_cvt_pk_bf16_f32 v6, v6, v7
	v_cvt_pk_bf16_f32 v7, v8, v9
	v_fmac_f32_e32 v19, v4, v4
	v_cndmask_b32_e64 v9, v14, v6, s[4:5]
	v_cvt_pk_bf16_f32 v2, v2, v3
	v_cvt_pk_bf16_f32 v3, v4, v5
	v_cndmask_b32_e64 v8, v15, v7, s[4:5]
	v_cndmask_b32_e64 v4, v17, v3, s[4:5]
	v_cndmask_b32_e64 v5, v16, v2, s[4:5]
	v_mov_b32_dpp v9, v9 row_ror:8 row_mask:0xf bank_mask:0xf
	v_mov_b32_dpp v4, v4 row_ror:8 row_mask:0xf bank_mask:0xf
	v_mov_b32_dpp v5, v5 row_ror:8 row_mask:0xf bank_mask:0xf
	v_mov_b32_dpp v8, v8 row_ror:8 row_mask:0xf bank_mask:0xf
	v_add_f32_e32 v22, v23, v22
	v_mul_f32_e32 v23, v21, v21
	v_fmac_f32_e32 v23, v20, v20
	v_add_f32_e32 v22, v23, v22
	v_add_f32_e32 v18, v19, v18
	s_waitcnt lgkmcnt(0)
	v_cndmask_b32_e64 v14, v9, v14, s[4:5]
	v_add_f32_e32 v18, v22, v18
	s_waitcnt lgkmcnt(0)
	v_cndmask_b32_e64 v17, v4, v17, s[4:5]
	s_waitcnt lgkmcnt(0)
	v_cndmask_b32_e64 v16, v5, v16, s[4:5]
	s_waitcnt lgkmcnt(0)
	v_cndmask_b32_e64 v15, v8, v15, s[4:5]
	v_cndmask_b32_e64 v20, v2, v5, s[4:5]
	ds_bpermute_b32 v2, v192, v14
	v_add_u32_e32 v14, 0xb0, v10
	v_cndmask_b32_e64 v19, v3, v4, s[4:5]
	ds_bpermute_b32 v3, v192, v15
	ds_bpermute_b32 v4, v192, v16
	ds_bpermute_b32 v5, v192, v17
	v_ashrrev_i32_e32 v15, 31, v14
	ds_bpermute_b32 v16, v11, v18
	v_lshlrev_b64 v[14:15], 11, v[14:15]
	v_lshl_add_u64 v[14:15], s[24:25], 0, v[14:15]
	v_lshl_add_u64 v[14:15], s[56:57], 1, v[14:15]
	v_lshl_add_u64 v[10:11], v[14:15], 0, v[174:175]
	v_cndmask_b32_e64 v7, v7, v8, s[4:5]
	v_cndmask_b32_e64 v6, v6, v9, s[4:5]
	s_waitcnt lgkmcnt(1)
	global_store_dwordx4 v[10:11], v[2:5], off
	ds_bpermute_b32 v6, v192, v6
	ds_bpermute_b32 v7, v192, v7
	s_waitcnt lgkmcnt(2)
	v_add_f32_e32 v2, v18, v16
	ds_bpermute_b32 v8, v192, v20
	ds_bpermute_b32 v9, v192, v19
	ds_bpermute_b32 v3, v119, v2
	v_add_co_u32_e32 v4, vcc, 0x4000, v10
	s_nop 1
	v_addc_co_u32_e32 v5, vcc, 0, v11, vcc
	s_waitcnt lgkmcnt(1)
	global_store_dwordx4 v[4:5], v[6:9], off
	s_and_saveexec_b64 s[56:57], s[6:7]
	s_cbranch_execz .LBB0_1090
	s_waitcnt lgkmcnt(0)
	v_add_f32_e32 v2, v2, v3
	global_atomic_add_f32 v[12:13], v2, off offset:704

; __device__ __forceinline__ u32x4 pack8(const f32x4& v0, const f32x4& v1) { u32x4 w; w.x = cvt_pk_bf16(v0[0], v0[1]); w.y = cvt_pk_bf16(v0[2], v0[3]); w.z = cvt_pk_bf16(v1[0], v1[1]); w.w = cvt_pk_bf16(v1[2], v1[3]); return w; }
; __device__ __forceinline__ u32x4 xor8_16B(u32x4 v) { u32x4 r; r.x = (unsigned)__shfl_xor((int)v.x, 8); r.y = (unsigned)__shfl_xor((int)v.y, 8); r.z = (unsigned)__shfl_xor((int)v.z, 8); r.w = (unsigned)__shfl_xor((int)v.w, 8); return r; }
; __device__ __forceinline__ u32x4 bperm_16B(int src_byte, u32x4 v) { u32x4 r; r.x = (unsigned)__builtin_amdgcn_ds_bpermute(src_byte, (int)v.x); r.y = (unsigned)__builtin_amdgcn_ds_bpermute(src_byte, (int)v.y); r.z = (unsigned)__builtin_amdgcn_ds_bpermute(src_byte, (int)v.z); r.w = (unsigned)__builtin_amdgcn_ds_bpermute(src_byte, (int)v.w); return r; }
; __device__ __forceinline__ void store_rows_bf16(bf16_t* O, size_t ldc, int r0, int c0, int fr, int fq, u32x4 w0, u32x4 w1) {
;     const bool h = fr & 8; const u32x4 recv = xor8_16B(h ? w0 : w1);
;     const u32x4 d1 = h ? recv : w0, d2 = h ? w1 : recv;
;     const int lane = fr + 16 * fq, src = ((lane >> 3) + 8 * ((lane >> 2) & 1) + 16 * (lane & 3)) * 4;
;     const u32x4 e1 = bperm_16B(src, d1), e2 = bperm_16B(src, d2);
;     bf16_t* p = O + (size_t)(r0 + (lane >> 3)) * ldc + c0 + 8 * (lane & 7);
;     *(u32x4*)p = e1; *(u32x4*)(p + 8 * ldc) = e2;
;     __device__ __forceinline__ void operator()(const f32x4 (&acc)[2][2][4][2], const Unit& u, int wr, int wc, int fr, int fq) const {
; #pragma unroll
;         for (int ai = 0; ai < 2; ++ai)
; #pragma unroll
;             for (int m = 0; m < 4; ++m) store_rows_bf16(O, (size_t)ldc, u.pm * BM + wr * 64 + ai * HALF + m * 16, u.pn * BM + wc * 64, fr, fq, pack8(acc[ai][0][m][0], acc[ai][0][m][1]), pack8(acc[ai][1][m][0], acc[ai][1][m][1]));
;     }
.LBB0_1174:
	v_cvt_pk_bf16_f32 v126, v126, v127
	v_cvt_pk_bf16_f32 v127, v128, v129
	v_cvt_pk_bf16_f32 v122, v122, v123
	v_cvt_pk_bf16_f32 v123, v124, v125
	v_and_b32_e32 v125, 64, v155
	v_xor_b32_e32 v124, 8, v155
	v_add_u32_e32 v125, 64, v125
	v_cmp_lt_i32_e32 vcc, v124, v125
	v_cvt_pk_bf16_f32 v118, v118, v119
	v_cvt_pk_bf16_f32 v119, v120, v121
	v_cvt_pk_bf16_f32 v114, v114, v115
	v_cvt_pk_bf16_f32 v115, v116, v117
	s_lshl_b32 s0, s57, 8
	s_nop 0
	v_cndmask_b32_e32 v124, v155, v124, vcc
	v_cndmask_b32_e64 v116, v123, v115, s[2:3]
	v_cndmask_b32_e64 v117, v122, v114, s[2:3]
	v_cndmask_b32_e64 v120, v127, v119, s[2:3]
	v_cndmask_b32_e64 v121, v126, v118, s[2:3]
	v_lshlrev_b32_e32 v124, 2, v124
	v_mov_b32_dpp v116, v116 row_ror:8 row_mask:0xf bank_mask:0xf
	v_mov_b32_dpp v117, v117 row_ror:8 row_mask:0xf bank_mask:0xf
	v_mov_b32_dpp v120, v120 row_ror:8 row_mask:0xf bank_mask:0xf
	v_mov_b32_dpp v121, v121 row_ror:8 row_mask:0xf bank_mask:0xf
	v_lshl_add_u32 v148, s56, 8, v151
	s_waitcnt lgkmcnt(0)
	v_cndmask_b32_e64 v123, v116, v123, s[2:3]
	v_cndmask_b32_e64 v122, v117, v122, s[2:3]
	v_cndmask_b32_e64 v125, v120, v127, s[2:3]
	v_cndmask_b32_e64 v126, v121, v126, s[2:3]
	s_or_b32 s0, s0, s50
	v_cndmask_b32_e64 v127, v115, v116, s[2:3]
	v_cndmask_b32_e64 v128, v114, v117, s[2:3]
	ds_bpermute_b32 v114, v150, v126
	ds_bpermute_b32 v115, v150, v125
	ds_bpermute_b32 v116, v150, v122
	ds_bpermute_b32 v117, v150, v123
	v_ashrrev_i32_e32 v149, 31, v148
	s_ashr_i32 s1, s0, 31
	v_cndmask_b32_e64 v119, v119, v120, s[2:3]
	v_cndmask_b32_e64 v118, v118, v121, s[2:3]
	v_lshlrev_b64 v[122:123], 12, v[148:149]
	ds_bpermute_b32 v118, v150, v118
	ds_bpermute_b32 v119, v150, v119
	ds_bpermute_b32 v120, v150, v128
	ds_bpermute_b32 v121, v150, v127
	v_lshl_add_u64 v[122:123], s[20:21], 0, v[122:123]
	s_lshl_b64 s[30:31], s[0:1], 1
	v_lshl_add_u64 v[122:123], v[122:123], 0, s[30:31]
	v_lshl_add_u64 v[122:123], v[122:123], 0, v[138:139]
	s_waitcnt lgkmcnt(0)
	global_store_dwordx4 v[122:123], v[114:117], off
	s_nop 1
	v_add_co_u32_e32 v114, vcc, s48, v122
	s_nop 1
	v_addc_co_u32_e32 v115, vcc, 0, v123, vcc
	global_store_dwordx4 v[114:115], v[118:121], off
	v_cvt_pk_bf16_f32 v110, v110, v111
	v_cvt_pk_bf16_f32 v111, v112, v113
	v_cvt_pk_bf16_f32 v106, v106, v107
	v_cvt_pk_bf16_f32 v107, v108, v109
	v_cvt_pk_bf16_f32 v102, v102, v103
	v_cvt_pk_bf16_f32 v103, v104, v105
	v_cvt_pk_bf16_f32 v98, v98, v99
	v_cvt_pk_bf16_f32 v99, v100, v101
	s_nop 0
	v_cndmask_b32_e64 v101, v106, v98, s[2:3]
	v_cndmask_b32_e64 v100, v107, v99, s[2:3]
	v_cndmask_b32_e64 v104, v111, v103, s[2:3]
	v_cndmask_b32_e64 v105, v110, v102, s[2:3]
	v_mov_b32_dpp v101, v101 row_ror:8 row_mask:0xf bank_mask:0xf
	v_mov_b32_dpp v100, v100 row_ror:8 row_mask:0xf bank_mask:0xf
	v_mov_b32_dpp v104, v104 row_ror:8 row_mask:0xf bank_mask:0xf
	v_mov_b32_dpp v105, v105 row_ror:8 row_mask:0xf bank_mask:0xf
	s_waitcnt lgkmcnt(0)
	v_cndmask_b32_e64 v106, v101, v106, s[2:3]
	v_cndmask_b32_e64 v107, v100, v107, s[2:3]
	v_cndmask_b32_e64 v108, v104, v111, s[2:3]
	v_cndmask_b32_e64 v109, v105, v110, s[2:3]
	v_cndmask_b32_e64 v110, v99, v100, s[2:3]
	ds_bpermute_b32 v100, v150, v106
	v_or_b32_e32 v106, 16, v148
	v_cndmask_b32_e64 v111, v98, v101, s[2:3]
	ds_bpermute_b32 v98, v150, v109
	ds_bpermute_b32 v99, v150, v108
	ds_bpermute_b32 v101, v150, v107
	v_ashrrev_i32_e32 v107, 31, v106
	v_cndmask_b32_e64 v103, v103, v104, s[2:3]
	v_cndmask_b32_e64 v102, v102, v105, s[2:3]
	v_lshlrev_b64 v[106:107], 12, v[106:107]
	ds_bpermute_b32 v102, v150, v102
	ds_bpermute_b32 v103, v150, v103
	ds_bpermute_b32 v104, v150, v111
	ds_bpermute_b32 v105, v150, v110
	v_lshl_add_u64 v[106:107], s[20:21], 0, v[106:107]
	v_lshl_add_u64 v[106:107], v[106:107], 0, s[30:31]
	v_lshl_add_u64 v[106:107], v[106:107], 0, v[138:139]
	s_waitcnt lgkmcnt(0)
	global_store_dwordx4 v[106:107], v[98:101], off
	s_nop 1
	v_add_co_u32_e32 v98, vcc, s48, v106
	s_nop 1
	v_addc_co_u32_e32 v99, vcc, 0, v107, vcc
	global_store_dwordx4 v[98:99], v[102:105], off
	v_cvt_pk_bf16_f32 v94, v94, v95
	v_cvt_pk_bf16_f32 v95, v96, v97
	v_cvt_pk_bf16_f32 v90, v90, v91
	v_cvt_pk_bf16_f32 v91, v92, v93
	v_cvt_pk_bf16_f32 v86, v86, v87
	v_cvt_pk_bf16_f32 v87, v88, v89
	v_cvt_pk_bf16_f32 v82, v82, v83
	v_cvt_pk_bf16_f32 v83, v84, v85
	s_nop 0
	v_cndmask_b32_e64 v85, v90, v82, s[2:3]
	v_cndmask_b32_e64 v84, v91, v83, s[2:3]
	v_cndmask_b32_e64 v88, v95, v87, s[2:3]
	v_cndmask_b32_e64 v89, v94, v86, s[2:3]
	v_mov_b32_dpp v85, v85 row_ror:8 row_mask:0xf bank_mask:0xf
	v_mov_b32_dpp v84, v84 row_ror:8 row_mask:0xf bank_mask:0xf
	v_mov_b32_dpp v88, v88 row_ror:8 row_mask:0xf bank_mask:0xf
	v_mov_b32_dpp v89, v89 row_ror:8 row_mask:0xf bank_mask:0xf
	s_waitcnt lgkmcnt(0)
	v_cndmask_b32_e64 v90, v85, v90, s[2:3]
	v_cndmask_b32_e64 v91, v84, v91, s[2:3]
	v_cndmask_b32_e64 v92, v88, v95, s[2:3]
	v_cndmask_b32_e64 v93, v89, v94, s[2:3]
	v_cndmask_b32_e64 v94, v83, v84, s[2:3]
	ds_bpermute_b32 v84, v150, v90
	v_or_b32_e32 v90, 32, v148
	v_cndmask_b32_e64 v95, v82, v85, s[2:3]
	ds_bpermute_b32 v82, v150, v93
	ds_bpermute_b32 v83, v150, v92
	ds_bpermute_b32 v85, v150, v91
	v_ashrrev_i32_e32 v91, 31, v90
	v_cndmask_b32_e64 v87, v87, v88, s[2:3]
	v_cndmask_b32_e64 v86, v86, v89, s[2:3]
	v_lshlrev_b64 v[90:91], 12, v[90:91]
	ds_bpermute_b32 v86, v150, v86
	ds_bpermute_b32 v87, v150, v87
	ds_bpermute_b32 v88, v150, v95
	ds_bpermute_b32 v89, v150, v94
	v_lshl_add_u64 v[90:91], s[20:21], 0, v[90:91]
	v_lshl_add_u64 v[90:91], v[90:91], 0, s[30:31]
	v_lshl_add_u64 v[90:91], v[90:91], 0, v[138:139]
	s_waitcnt lgkmcnt(0)
; __device__ __forceinline__ u32x4 pack8(const f32x4& v0, const f32x4& v1) { u32x4 w; w.x = cvt_pk_bf16(v0[0], v0[1]); w.y = cvt_pk_bf16(v0[2], v0[3]); w.z = cvt_pk_bf16(v1[0], v1[1]); w.w = cvt_pk_bf16(v1[2], v1[3]); return w; }
; __device__ __forceinline__ u32x4 xor8_16B(u32x4 v) { u32x4 r; r.x = (unsigned)__shfl_xor((int)v.x, 8); r.y = (unsigned)__shfl_xor((int)v.y, 8); r.z = (unsigned)__shfl_xor((int)v.z, 8); r.w = (unsigned)__shfl_xor((int)v.w, 8); return r; }
; __device__ __forceinline__ u32x4 bperm_16B(int src_byte, u32x4 v) { u32x4 r; r.x = (unsigned)__builtin_amdgcn_ds_bpermute(src_byte, (int)v.x); r.y = (unsigned)__builtin_amdgcn_ds_bpermute(src_byte, (int)v.y); r.z = (unsigned)__builtin_amdgcn_ds_bpermute(src_byte, (int)v.z); r.w = (unsigned)__builtin_amdgcn_ds_bpermute(src_byte, (int)v.w); return r; }
; __device__ __forceinline__ void store_rows_bf16(bf16_t* O, size_t ldc, int r0, int c0, int fr, int fq, u32x4 w0, u32x4 w1) {
;     const bool h = fr & 8; const u32x4 recv = xor8_16B(h ? w0 : w1);
;     const u32x4 d1 = h ? recv : w0, d2 = h ? w1 : recv;
;     const int lane = fr + 16 * fq, src = ((lane >> 3) + 8 * ((lane >> 2) & 1) + 16 * (lane & 3)) * 4;
;     const u32x4 e1 = bperm_16B(src, d1), e2 = bperm_16B(src, d2);
;     bf16_t* p = O + (size_t)(r0 + (lane >> 3)) * ldc + c0 + 8 * (lane & 7);
;     *(u32x4*)p = e1; *(u32x4*)(p + 8 * ldc) = e2;
;     __device__ __forceinline__ void operator()(const f32x4 (&acc)[2][2][4][2], const Unit& u, int wr, int wc, int fr, int fq) const {
; #pragma unroll
;         for (int ai = 0; ai < 2; ++ai)
; #pragma unroll
;             for (int m = 0; m < 4; ++m) store_rows_bf16(O, (size_t)ldc, u.pm * BM + wr * 64 + ai * HALF + m * 16, u.pn * BM + wc * 64, fr, fq, pack8(acc[ai][0][m][0], acc[ai][0][m][1]), pack8(acc[ai][1][m][0], acc[ai][1][m][1]));
;     }
	global_store_dwordx4 v[90:91], v[82:85], off
	s_nop 1
	v_add_co_u32_e32 v82, vcc, s48, v90
	s_nop 1
	v_addc_co_u32_e32 v83, vcc, 0, v91, vcc
	global_store_dwordx4 v[82:83], v[86:89], off
	v_cvt_pk_bf16_f32 v78, v78, v79
	v_cvt_pk_bf16_f32 v79, v80, v81
	v_cvt_pk_bf16_f32 v74, v74, v75
	v_cvt_pk_bf16_f32 v75, v76, v77
	v_cvt_pk_bf16_f32 v70, v70, v71
	v_cvt_pk_bf16_f32 v71, v72, v73
	v_cvt_pk_bf16_f32 v66, v66, v67
	v_cvt_pk_bf16_f32 v67, v68, v69
	s_nop 0
	v_cndmask_b32_e64 v69, v74, v66, s[2:3]
	v_cndmask_b32_e64 v68, v75, v67, s[2:3]
	v_cndmask_b32_e64 v72, v79, v71, s[2:3]
	v_cndmask_b32_e64 v73, v78, v70, s[2:3]
	v_mov_b32_dpp v69, v69 row_ror:8 row_mask:0xf bank_mask:0xf
	v_mov_b32_dpp v68, v68 row_ror:8 row_mask:0xf bank_mask:0xf
	v_mov_b32_dpp v72, v72 row_ror:8 row_mask:0xf bank_mask:0xf
	v_mov_b32_dpp v73, v73 row_ror:8 row_mask:0xf bank_mask:0xf
	s_waitcnt lgkmcnt(0)
	v_cndmask_b32_e64 v74, v69, v74, s[2:3]
	v_cndmask_b32_e64 v75, v68, v75, s[2:3]
	v_cndmask_b32_e64 v76, v72, v79, s[2:3]
	v_cndmask_b32_e64 v77, v73, v78, s[2:3]
	v_cndmask_b32_e64 v78, v67, v68, s[2:3]
	ds_bpermute_b32 v68, v150, v74
	v_or_b32_e32 v74, 48, v148
	v_cndmask_b32_e64 v79, v66, v69, s[2:3]
	ds_bpermute_b32 v66, v150, v77
	ds_bpermute_b32 v67, v150, v76
	ds_bpermute_b32 v69, v150, v75
	v_ashrrev_i32_e32 v75, 31, v74
	v_cndmask_b32_e64 v71, v71, v72, s[2:3]
	v_cndmask_b32_e64 v70, v70, v73, s[2:3]
	v_lshlrev_b64 v[74:75], 12, v[74:75]
	ds_bpermute_b32 v70, v150, v70
	ds_bpermute_b32 v71, v150, v71
	ds_bpermute_b32 v72, v150, v79
	ds_bpermute_b32 v73, v150, v78
	v_lshl_add_u64 v[74:75], s[20:21], 0, v[74:75]
	v_lshl_add_u64 v[74:75], v[74:75], 0, s[30:31]
	v_lshl_add_u64 v[74:75], v[74:75], 0, v[138:139]
	s_waitcnt lgkmcnt(0)
	global_store_dwordx4 v[74:75], v[66:69], off
	s_nop 1
	v_add_co_u32_e32 v66, vcc, s48, v74
	s_nop 1
	v_addc_co_u32_e32 v67, vcc, 0, v75, vcc
	global_store_dwordx4 v[66:67], v[70:73], off
	v_cvt_pk_bf16_f32 v62, v62, v63
	v_cvt_pk_bf16_f32 v63, v64, v65
	v_cvt_pk_bf16_f32 v59, v58, v59
	v_cvt_pk_bf16_f32 v60, v60, v61
	v_cvt_pk_bf16_f32 v54, v54, v55
	v_cvt_pk_bf16_f32 v55, v56, v57
	v_cvt_pk_bf16_f32 v50, v50, v51
	v_cvt_pk_bf16_f32 v51, v52, v53
	v_add_u32_e32 v58, 0x80, v148
	v_cndmask_b32_e64 v52, v60, v51, s[2:3]
	v_cndmask_b32_e64 v53, v59, v50, s[2:3]
	v_cndmask_b32_e64 v56, v63, v55, s[2:3]
	v_cndmask_b32_e64 v57, v62, v54, s[2:3]
	v_mov_b32_dpp v52, v52 row_ror:8 row_mask:0xf bank_mask:0xf
	v_mov_b32_dpp v53, v53 row_ror:8 row_mask:0xf bank_mask:0xf
	v_mov_b32_dpp v56, v56 row_ror:8 row_mask:0xf bank_mask:0xf
	v_mov_b32_dpp v57, v57 row_ror:8 row_mask:0xf bank_mask:0xf
	s_waitcnt lgkmcnt(0)
	v_cndmask_b32_e64 v60, v52, v60, s[2:3]
	v_cndmask_b32_e64 v59, v53, v59, s[2:3]
	v_cndmask_b32_e64 v61, v56, v63, s[2:3]
	v_cndmask_b32_e64 v62, v57, v62, s[2:3]
	v_cndmask_b32_e64 v63, v51, v52, s[2:3]
	v_cndmask_b32_e64 v64, v50, v53, s[2:3]
	ds_bpermute_b32 v50, v150, v62
	ds_bpermute_b32 v51, v150, v61
	ds_bpermute_b32 v52, v150, v59
	ds_bpermute_b32 v53, v150, v60
	v_ashrrev_i32_e32 v59, 31, v58
	v_cndmask_b32_e64 v55, v55, v56, s[2:3]
	v_cndmask_b32_e64 v54, v54, v57, s[2:3]
	v_lshlrev_b64 v[58:59], 12, v[58:59]
	ds_bpermute_b32 v54, v150, v54
	ds_bpermute_b32 v55, v150, v55
	ds_bpermute_b32 v56, v150, v64
	ds_bpermute_b32 v57, v150, v63
	v_lshl_add_u64 v[58:59], s[20:21], 0, v[58:59]
	v_lshl_add_u64 v[58:59], v[58:59], 0, s[30:31]
	v_lshl_add_u64 v[58:59], v[58:59], 0, v[138:139]
	s_waitcnt lgkmcnt(0)
	global_store_dwordx4 v[58:59], v[50:53], off
	s_nop 1
	v_add_co_u32_e32 v50, vcc, s48, v58
	s_nop 1
	v_addc_co_u32_e32 v51, vcc, 0, v59, vcc
	global_store_dwordx4 v[50:51], v[54:57], off
	v_cvt_pk_bf16_f32 v46, v46, v47
	v_cvt_pk_bf16_f32 v47, v48, v49
	v_cvt_pk_bf16_f32 v42, v42, v43
	v_cvt_pk_bf16_f32 v43, v44, v45
	v_cvt_pk_bf16_f32 v38, v38, v39
	v_cvt_pk_bf16_f32 v39, v40, v41
	v_cvt_pk_bf16_f32 v34, v34, v35
	v_cvt_pk_bf16_f32 v35, v36, v37
	s_nop 0
	v_cndmask_b32_e64 v37, v42, v34, s[2:3]
	v_cndmask_b32_e64 v36, v43, v35, s[2:3]
	v_cndmask_b32_e64 v40, v47, v39, s[2:3]
	v_cndmask_b32_e64 v41, v46, v38, s[2:3]
	v_mov_b32_dpp v37, v37 row_ror:8 row_mask:0xf bank_mask:0xf
	v_mov_b32_dpp v36, v36 row_ror:8 row_mask:0xf bank_mask:0xf
	v_mov_b32_dpp v40, v40 row_ror:8 row_mask:0xf bank_mask:0xf
	v_mov_b32_dpp v41, v41 row_ror:8 row_mask:0xf bank_mask:0xf
	s_waitcnt lgkmcnt(0)
; __device__ __forceinline__ u32x4 pack8(const f32x4& v0, const f32x4& v1) { u32x4 w; w.x = cvt_pk_bf16(v0[0], v0[1]); w.y = cvt_pk_bf16(v0[2], v0[3]); w.z = cvt_pk_bf16(v1[0], v1[1]); w.w = cvt_pk_bf16(v1[2], v1[3]); return w; }
; __device__ __forceinline__ u32x4 xor8_16B(u32x4 v) { u32x4 r; r.x = (unsigned)__shfl_xor((int)v.x, 8); r.y = (unsigned)__shfl_xor((int)v.y, 8); r.z = (unsigned)__shfl_xor((int)v.z, 8); r.w = (unsigned)__shfl_xor((int)v.w, 8); return r; }
; #define PG8_BAR __builtin_amdgcn_s_barrier()
; __device__ __forceinline__ void store_rows_bf16(bf16_t* O, size_t ldc, int r0, int c0, int fr, int fq, u32x4 w0, u32x4 w1) {
;     const bool h = fr & 8; const u32x4 recv = xor8_16B(h ? w0 : w1);
;     const u32x4 d1 = h ? recv : w0, d2 = h ? w1 : recv;
;     const int lane = fr + 16 * fq, src = ((lane >> 3) + 8 * ((lane >> 2) & 1) + 16 * (lane & 3)) * 4;
;     const u32x4 e1 = bperm_16B(src, d1), e2 = bperm_16B(src, d2);
;     bf16_t* p = O + (size_t)(r0 + (lane >> 3)) * ldc + c0 + 8 * (lane & 7);
;     *(u32x4*)p = e1; *(u32x4*)(p + 8 * ldc) = e2;
;     __device__ __forceinline__ void operator()(const f32x4 (&acc)[2][2][4][2], const Unit& u, int wr, int wc, int fr, int fq) const {
; #pragma unroll
;         for (int ai = 0; ai < 2; ++ai)
; #pragma unroll
;             for (int m = 0; m < 4; ++m) store_rows_bf16(O, (size_t)ldc, u.pm * BM + wr * 64 + ai * HALF + m * 16, u.pn * BM + wc * 64, fr, fq, pack8(acc[ai][0][m][0], acc[ai][0][m][1]), pack8(acc[ai][1][m][0], acc[ai][1][m][1]));
;     }
; template <class Epi, class Sched, bool ALIGN_EPI = false, bool SP2 = false>
; __device__ __forceinline__ void gemm_phase(PG8_LAS unsigned char* lds, const Gemm g, const Sched& S, const Epi& E) {
;     ...
;         if (!has_next) break;
; #pragma unroll
;         for (int a = 0; a < 2; ++a)
; #pragma unroll
;             for (int b = 0; b < 2; ++b)
; #pragma unroll
;                 for (int m = 0; m < 4; ++m)
; #pragma unroll
;                     for (int n = 0; n < 2; ++n) acc[a][b][m][n] = (f32x4){0.f, 0.f, 0.f, 0.f};
;         cur = nxt; cA = nA; cB = nB; ++ui;
;         if constexpr (ALIGN_EPI) { if (wr == 1) PG8_BAR; }
	v_cndmask_b32_e64 v42, v37, v42, s[2:3]
	v_cndmask_b32_e64 v43, v36, v43, s[2:3]
	v_cndmask_b32_e64 v44, v40, v47, s[2:3]
	v_cndmask_b32_e64 v45, v41, v46, s[2:3]
	v_cndmask_b32_e64 v46, v35, v36, s[2:3]
	ds_bpermute_b32 v36, v150, v42
	v_add_u32_e32 v42, 0x90, v148
	v_cndmask_b32_e64 v47, v34, v37, s[2:3]
	ds_bpermute_b32 v34, v150, v45
	ds_bpermute_b32 v35, v150, v44
	ds_bpermute_b32 v37, v150, v43
	v_ashrrev_i32_e32 v43, 31, v42
	v_cndmask_b32_e64 v39, v39, v40, s[2:3]
	v_cndmask_b32_e64 v38, v38, v41, s[2:3]
	v_lshlrev_b64 v[42:43], 12, v[42:43]
	ds_bpermute_b32 v38, v150, v38
	ds_bpermute_b32 v39, v150, v39
	ds_bpermute_b32 v40, v150, v47
	ds_bpermute_b32 v41, v150, v46
	v_lshl_add_u64 v[42:43], s[20:21], 0, v[42:43]
	v_lshl_add_u64 v[42:43], v[42:43], 0, s[30:31]
	v_lshl_add_u64 v[42:43], v[42:43], 0, v[138:139]
	s_waitcnt lgkmcnt(0)
	global_store_dwordx4 v[42:43], v[34:37], off
	s_nop 1
	v_add_co_u32_e32 v34, vcc, s48, v42
	s_nop 1
	v_addc_co_u32_e32 v35, vcc, 0, v43, vcc
	global_store_dwordx4 v[34:35], v[38:41], off
	v_cvt_pk_bf16_f32 v30, v30, v31
	v_cvt_pk_bf16_f32 v31, v32, v33
	v_cvt_pk_bf16_f32 v26, v26, v27
	v_cvt_pk_bf16_f32 v27, v28, v29
	v_cvt_pk_bf16_f32 v22, v22, v23
	v_cvt_pk_bf16_f32 v23, v24, v25
	v_cvt_pk_bf16_f32 v18, v18, v19
	v_cvt_pk_bf16_f32 v19, v20, v21
	s_nop 0
	v_cndmask_b32_e64 v21, v26, v18, s[2:3]
	v_cndmask_b32_e64 v20, v27, v19, s[2:3]
	v_cndmask_b32_e64 v24, v31, v23, s[2:3]
	v_cndmask_b32_e64 v25, v30, v22, s[2:3]
	v_mov_b32_dpp v21, v21 row_ror:8 row_mask:0xf bank_mask:0xf
	v_mov_b32_dpp v20, v20 row_ror:8 row_mask:0xf bank_mask:0xf
	v_mov_b32_dpp v24, v24 row_ror:8 row_mask:0xf bank_mask:0xf
	v_mov_b32_dpp v25, v25 row_ror:8 row_mask:0xf bank_mask:0xf
	s_waitcnt lgkmcnt(0)
	v_cndmask_b32_e64 v26, v21, v26, s[2:3]
	v_cndmask_b32_e64 v27, v20, v27, s[2:3]
	v_cndmask_b32_e64 v28, v24, v31, s[2:3]
	v_cndmask_b32_e64 v29, v25, v30, s[2:3]
	v_cndmask_b32_e64 v30, v19, v20, s[2:3]
	ds_bpermute_b32 v20, v150, v26
	v_add_u32_e32 v26, 0xa0, v148
	v_cndmask_b32_e64 v31, v18, v21, s[2:3]
	ds_bpermute_b32 v18, v150, v29
	ds_bpermute_b32 v19, v150, v28
	ds_bpermute_b32 v21, v150, v27
	v_ashrrev_i32_e32 v27, 31, v26
	v_cndmask_b32_e64 v23, v23, v24, s[2:3]
	v_cndmask_b32_e64 v22, v22, v25, s[2:3]
	v_lshlrev_b64 v[26:27], 12, v[26:27]
	ds_bpermute_b32 v22, v150, v22
	ds_bpermute_b32 v23, v150, v23
	ds_bpermute_b32 v24, v150, v31
	ds_bpermute_b32 v25, v150, v30
	v_lshl_add_u64 v[26:27], s[20:21], 0, v[26:27]
	v_lshl_add_u64 v[26:27], v[26:27], 0, s[30:31]
	v_lshl_add_u64 v[26:27], v[26:27], 0, v[138:139]
	s_waitcnt lgkmcnt(0)
	global_store_dwordx4 v[26:27], v[18:21], off
	s_nop 1
	v_add_co_u32_e32 v18, vcc, s48, v26
	s_nop 1
	v_addc_co_u32_e32 v19, vcc, 0, v27, vcc
	global_store_dwordx4 v[18:19], v[22:25], off
	v_cvt_pk_bf16_f32 v14, v14, v15
	v_cvt_pk_bf16_f32 v15, v16, v17
	v_cvt_pk_bf16_f32 v6, v6, v7
	v_cvt_pk_bf16_f32 v7, v8, v9
	v_cvt_pk_bf16_f32 v8, v10, v11
	v_cvt_pk_bf16_f32 v9, v12, v13
	v_cvt_pk_bf16_f32 v2, v2, v3
	v_cvt_pk_bf16_f32 v3, v4, v5
	s_nop 0
	v_cndmask_b32_e64 v4, v7, v3, s[2:3]
	v_cndmask_b32_e64 v5, v6, v2, s[2:3]
	v_cndmask_b32_e64 v10, v15, v9, s[2:3]
	v_cndmask_b32_e64 v11, v14, v8, s[2:3]
	v_mov_b32_dpp v4, v4 row_ror:8 row_mask:0xf bank_mask:0xf
	v_mov_b32_dpp v5, v5 row_ror:8 row_mask:0xf bank_mask:0xf
	v_mov_b32_dpp v10, v10 row_ror:8 row_mask:0xf bank_mask:0xf
	v_mov_b32_dpp v11, v11 row_ror:8 row_mask:0xf bank_mask:0xf
	s_waitcnt lgkmcnt(0)
	v_cndmask_b32_e64 v7, v4, v7, s[2:3]
	v_cndmask_b32_e64 v6, v5, v6, s[2:3]
	v_cndmask_b32_e64 v12, v10, v15, s[2:3]
	v_cndmask_b32_e64 v13, v11, v14, s[2:3]
	v_cndmask_b32_e64 v9, v9, v10, s[2:3]
	v_add_u32_e32 v10, 0xb0, v148
	v_cndmask_b32_e64 v14, v3, v4, s[2:3]
	v_cndmask_b32_e64 v15, v2, v5, s[2:3]
	v_cndmask_b32_e64 v8, v8, v11, s[2:3]
	ds_bpermute_b32 v2, v150, v13
	ds_bpermute_b32 v3, v150, v12
	ds_bpermute_b32 v4, v150, v6
	ds_bpermute_b32 v5, v150, v7
	v_ashrrev_i32_e32 v11, 31, v10
	v_lshlrev_b64 v[10:11], 12, v[10:11]
	v_lshl_add_u64 v[10:11], s[20:21], 0, v[10:11]
	ds_bpermute_b32 v6, v150, v8
	ds_bpermute_b32 v7, v150, v9
	ds_bpermute_b32 v8, v150, v15
	ds_bpermute_b32 v9, v150, v14
	v_lshl_add_u64 v[10:11], v[10:11], 0, s[30:31]
	v_lshl_add_u64 v[10:11], v[10:11], 0, v[138:139]
	s_waitcnt lgkmcnt(0)
	global_store_dwordx4 v[10:11], v[2:5], off
	s_nop 1
	v_add_co_u32_e32 v2, vcc, 0x8000, v10
	s_nop 1
	v_addc_co_u32_e32 v3, vcc, 0, v11, vcc
	s_and_b64 vcc, exec, s[4:5]
	s_mov_b64 s[4:5], -1
	global_store_dwordx4 v[2:3], v[6:9], off
	s_cbranch_vccnz .LBB0_1158
	s_andn2_b64 vcc, exec, s[18:19]
	s_cbranch_vccnz .LBB0_1157
	s_barrier
	s_branch .LBB0_1157

; __device__ __forceinline__ u32x4 pack8(const f32x4& v0, const f32x4& v1) { u32x4 w; w.x = cvt_pk_bf16(v0[0], v0[1]); w.y = cvt_pk_bf16(v0[2], v0[3]); w.z = cvt_pk_bf16(v1[0], v1[1]); w.w = cvt_pk_bf16(v1[2], v1[3]); return w; }
; __device__ __forceinline__ u32x4 xor8_16B(u32x4 v) { u32x4 r; r.x = (unsigned)__shfl_xor((int)v.x, 8); r.y = (unsigned)__shfl_xor((int)v.y, 8); r.z = (unsigned)__shfl_xor((int)v.z, 8); r.w = (unsigned)__shfl_xor((int)v.w, 8); return r; }
; __device__ __forceinline__ u32x4 bperm_16B(int src_byte, u32x4 v) { u32x4 r; r.x = (unsigned)__builtin_amdgcn_ds_bpermute(src_byte, (int)v.x); r.y = (unsigned)__builtin_amdgcn_ds_bpermute(src_byte, (int)v.y); r.z = (unsigned)__builtin_amdgcn_ds_bpermute(src_byte, (int)v.z); r.w = (unsigned)__builtin_amdgcn_ds_bpermute(src_byte, (int)v.w); return r; }
; __device__ __forceinline__ void store_rows_bf16(bf16_t* O, size_t ldc, int r0, int c0, int fr, int fq, u32x4 w0, u32x4 w1) {
;     const bool h = fr & 8; const u32x4 recv = xor8_16B(h ? w0 : w1);
;     const u32x4 d1 = h ? recv : w0, d2 = h ? w1 : recv;
;     const int lane = fr + 16 * fq, src = ((lane >> 3) + 8 * ((lane >> 2) & 1) + 16 * (lane & 3)) * 4;
;     const u32x4 e1 = bperm_16B(src, d1), e2 = bperm_16B(src, d2);
;     bf16_t* p = O + (size_t)(r0 + (lane >> 3)) * ldc + c0 + 8 * (lane & 7);
;     *(u32x4*)p = e1; *(u32x4*)(p + 8 * ldc) = e2;
;     __device__ __forceinline__ void operator()(const f32x4 (&acc)[2][2][4][2], const Unit& u, int wr, int wc, int fr, int fq) const {
; #pragma unroll
;         for (int ai = 0; ai < 2; ++ai)
; #pragma unroll
;             for (int m = 0; m < 4; ++m) store_rows_bf16(O, (size_t)ldc, u.pm * BM + wr * 64 + ai * HALF + m * 16, u.pn * BM + wc * 64, fr, fq, pack8(acc[ai][0][m][0], acc[ai][0][m][1]), pack8(acc[ai][1][m][0], acc[ai][1][m][1]));
;     }
.LBB0_1595:
	v_cvt_pk_bf16_f32 v126, v126, v127
	v_cvt_pk_bf16_f32 v127, v128, v129
	v_cvt_pk_bf16_f32 v122, v122, v123
	v_cvt_pk_bf16_f32 v123, v124, v125
	v_and_b32_e32 v125, 64, v155
	v_xor_b32_e32 v124, 8, v155
	v_add_u32_e32 v125, 64, v125
	v_cmp_lt_i32_e32 vcc, v124, v125
	v_cvt_pk_bf16_f32 v118, v118, v119
	v_cvt_pk_bf16_f32 v119, v120, v121
	v_cvt_pk_bf16_f32 v114, v114, v115
	v_cvt_pk_bf16_f32 v115, v116, v117
	s_lshl_b32 s0, s57, 8
	s_nop 0
	v_cndmask_b32_e32 v124, v155, v124, vcc
	v_cndmask_b32_e64 v116, v123, v115, s[2:3]
	v_cndmask_b32_e64 v117, v122, v114, s[2:3]
	v_cndmask_b32_e64 v120, v127, v119, s[2:3]
	v_cndmask_b32_e64 v121, v126, v118, s[2:3]
	v_lshlrev_b32_e32 v124, 2, v124
	v_mov_b32_dpp v116, v116 row_ror:8 row_mask:0xf bank_mask:0xf
	v_mov_b32_dpp v117, v117 row_ror:8 row_mask:0xf bank_mask:0xf
	v_mov_b32_dpp v120, v120 row_ror:8 row_mask:0xf bank_mask:0xf
	v_mov_b32_dpp v121, v121 row_ror:8 row_mask:0xf bank_mask:0xf
	v_lshl_add_u32 v148, s56, 8, v151
	s_waitcnt lgkmcnt(0)
	v_cndmask_b32_e64 v123, v116, v123, s[2:3]
	v_cndmask_b32_e64 v122, v117, v122, s[2:3]
	v_cndmask_b32_e64 v125, v120, v127, s[2:3]
	v_cndmask_b32_e64 v126, v121, v126, s[2:3]
	s_or_b32 s0, s0, s50
	v_cndmask_b32_e64 v127, v115, v116, s[2:3]
	v_cndmask_b32_e64 v128, v114, v117, s[2:3]
	ds_bpermute_b32 v114, v150, v126
	ds_bpermute_b32 v115, v150, v125
	ds_bpermute_b32 v116, v150, v122
	ds_bpermute_b32 v117, v150, v123
	v_ashrrev_i32_e32 v149, 31, v148
	s_ashr_i32 s1, s0, 31
	v_cndmask_b32_e64 v119, v119, v120, s[2:3]
	v_cndmask_b32_e64 v118, v118, v121, s[2:3]
	v_lshlrev_b64 v[122:123], 11, v[148:149]
	ds_bpermute_b32 v118, v150, v118
	ds_bpermute_b32 v119, v150, v119
	ds_bpermute_b32 v120, v150, v128
	ds_bpermute_b32 v121, v150, v127
	v_lshl_add_u64 v[122:123], s[20:21], 0, v[122:123]
	s_lshl_b64 s[30:31], s[0:1], 1
	v_lshl_add_u64 v[122:123], v[122:123], 0, s[30:31]
	v_lshl_add_u64 v[122:123], v[122:123], 0, v[138:139]
	s_waitcnt lgkmcnt(0)
	global_store_dwordx4 v[122:123], v[114:117], off
	s_nop 1
	v_add_co_u32_e32 v114, vcc, s45, v122
	s_nop 1
	v_addc_co_u32_e32 v115, vcc, 0, v123, vcc
	global_store_dwordx4 v[114:115], v[118:121], off
	v_cvt_pk_bf16_f32 v110, v110, v111
	v_cvt_pk_bf16_f32 v111, v112, v113
	v_cvt_pk_bf16_f32 v106, v106, v107
	v_cvt_pk_bf16_f32 v107, v108, v109
	v_cvt_pk_bf16_f32 v102, v102, v103
	v_cvt_pk_bf16_f32 v103, v104, v105
	v_cvt_pk_bf16_f32 v98, v98, v99
	v_cvt_pk_bf16_f32 v99, v100, v101
	s_nop 0
	v_cndmask_b32_e64 v101, v106, v98, s[2:3]
	v_cndmask_b32_e64 v100, v107, v99, s[2:3]
	v_cndmask_b32_e64 v104, v111, v103, s[2:3]
	v_cndmask_b32_e64 v105, v110, v102, s[2:3]
	v_mov_b32_dpp v101, v101 row_ror:8 row_mask:0xf bank_mask:0xf
	v_mov_b32_dpp v100, v100 row_ror:8 row_mask:0xf bank_mask:0xf
	v_mov_b32_dpp v104, v104 row_ror:8 row_mask:0xf bank_mask:0xf
	v_mov_b32_dpp v105, v105 row_ror:8 row_mask:0xf bank_mask:0xf
	s_waitcnt lgkmcnt(0)
	v_cndmask_b32_e64 v106, v101, v106, s[2:3]
	v_cndmask_b32_e64 v107, v100, v107, s[2:3]
	v_cndmask_b32_e64 v108, v104, v111, s[2:3]
	v_cndmask_b32_e64 v109, v105, v110, s[2:3]
	v_cndmask_b32_e64 v110, v99, v100, s[2:3]
	ds_bpermute_b32 v100, v150, v106
	v_or_b32_e32 v106, 16, v148
	v_cndmask_b32_e64 v111, v98, v101, s[2:3]
	ds_bpermute_b32 v98, v150, v109
	ds_bpermute_b32 v99, v150, v108
	ds_bpermute_b32 v101, v150, v107
	v_ashrrev_i32_e32 v107, 31, v106
	v_cndmask_b32_e64 v103, v103, v104, s[2:3]
	v_cndmask_b32_e64 v102, v102, v105, s[2:3]
	v_lshlrev_b64 v[106:107], 11, v[106:107]
	ds_bpermute_b32 v102, v150, v102
	ds_bpermute_b32 v103, v150, v103
	ds_bpermute_b32 v104, v150, v111
	ds_bpermute_b32 v105, v150, v110
	v_lshl_add_u64 v[106:107], s[20:21], 0, v[106:107]
	v_lshl_add_u64 v[106:107], v[106:107], 0, s[30:31]
	v_lshl_add_u64 v[106:107], v[106:107], 0, v[138:139]
	s_waitcnt lgkmcnt(0)
	global_store_dwordx4 v[106:107], v[98:101], off
	s_nop 1
	v_add_co_u32_e32 v98, vcc, s45, v106
	s_nop 1
	v_addc_co_u32_e32 v99, vcc, 0, v107, vcc
	global_store_dwordx4 v[98:99], v[102:105], off
	v_cvt_pk_bf16_f32 v94, v94, v95
	v_cvt_pk_bf16_f32 v95, v96, v97
	v_cvt_pk_bf16_f32 v90, v90, v91
	v_cvt_pk_bf16_f32 v91, v92, v93
	v_cvt_pk_bf16_f32 v86, v86, v87
	v_cvt_pk_bf16_f32 v87, v88, v89
	v_cvt_pk_bf16_f32 v82, v82, v83
	v_cvt_pk_bf16_f32 v83, v84, v85
	s_nop 0
	v_cndmask_b32_e64 v85, v90, v82, s[2:3]
	v_cndmask_b32_e64 v84, v91, v83, s[2:3]
	v_cndmask_b32_e64 v88, v95, v87, s[2:3]
	v_cndmask_b32_e64 v89, v94, v86, s[2:3]
	v_mov_b32_dpp v85, v85 row_ror:8 row_mask:0xf bank_mask:0xf
	v_mov_b32_dpp v84, v84 row_ror:8 row_mask:0xf bank_mask:0xf
	v_mov_b32_dpp v88, v88 row_ror:8 row_mask:0xf bank_mask:0xf
	v_mov_b32_dpp v89, v89 row_ror:8 row_mask:0xf bank_mask:0xf
	s_waitcnt lgkmcnt(0)
	v_cndmask_b32_e64 v90, v85, v90, s[2:3]
	v_cndmask_b32_e64 v91, v84, v91, s[2:3]
	v_cndmask_b32_e64 v92, v88, v95, s[2:3]
	v_cndmask_b32_e64 v93, v89, v94, s[2:3]
	v_cndmask_b32_e64 v94, v83, v84, s[2:3]
	ds_bpermute_b32 v84, v150, v90
	v_or_b32_e32 v90, 32, v148
	v_cndmask_b32_e64 v95, v82, v85, s[2:3]
	ds_bpermute_b32 v82, v150, v93
	ds_bpermute_b32 v83, v150, v92
	ds_bpermute_b32 v85, v150, v91
	v_ashrrev_i32_e32 v91, 31, v90
	v_cndmask_b32_e64 v87, v87, v88, s[2:3]
	v_cndmask_b32_e64 v86, v86, v89, s[2:3]
	v_lshlrev_b64 v[90:91], 11, v[90:91]
	ds_bpermute_b32 v86, v150, v86
	ds_bpermute_b32 v87, v150, v87
	ds_bpermute_b32 v88, v150, v95
	ds_bpermute_b32 v89, v150, v94
	v_lshl_add_u64 v[90:91], s[20:21], 0, v[90:91]
	v_lshl_add_u64 v[90:91], v[90:91], 0, s[30:31]
	v_lshl_add_u64 v[90:91], v[90:91], 0, v[138:139]
	s_waitcnt lgkmcnt(0)
; __device__ __forceinline__ u32x4 pack8(const f32x4& v0, const f32x4& v1) { u32x4 w; w.x = cvt_pk_bf16(v0[0], v0[1]); w.y = cvt_pk_bf16(v0[2], v0[3]); w.z = cvt_pk_bf16(v1[0], v1[1]); w.w = cvt_pk_bf16(v1[2], v1[3]); return w; }
; __device__ __forceinline__ u32x4 xor8_16B(u32x4 v) { u32x4 r; r.x = (unsigned)__shfl_xor((int)v.x, 8); r.y = (unsigned)__shfl_xor((int)v.y, 8); r.z = (unsigned)__shfl_xor((int)v.z, 8); r.w = (unsigned)__shfl_xor((int)v.w, 8); return r; }
; __device__ __forceinline__ u32x4 bperm_16B(int src_byte, u32x4 v) { u32x4 r; r.x = (unsigned)__builtin_amdgcn_ds_bpermute(src_byte, (int)v.x); r.y = (unsigned)__builtin_amdgcn_ds_bpermute(src_byte, (int)v.y); r.z = (unsigned)__builtin_amdgcn_ds_bpermute(src_byte, (int)v.z); r.w = (unsigned)__builtin_amdgcn_ds_bpermute(src_byte, (int)v.w); return r; }
; __device__ __forceinline__ void store_rows_bf16(bf16_t* O, size_t ldc, int r0, int c0, int fr, int fq, u32x4 w0, u32x4 w1) {
;     const bool h = fr & 8; const u32x4 recv = xor8_16B(h ? w0 : w1);
;     const u32x4 d1 = h ? recv : w0, d2 = h ? w1 : recv;
;     const int lane = fr + 16 * fq, src = ((lane >> 3) + 8 * ((lane >> 2) & 1) + 16 * (lane & 3)) * 4;
;     const u32x4 e1 = bperm_16B(src, d1), e2 = bperm_16B(src, d2);
;     bf16_t* p = O + (size_t)(r0 + (lane >> 3)) * ldc + c0 + 8 * (lane & 7);
;     *(u32x4*)p = e1; *(u32x4*)(p + 8 * ldc) = e2;
;     __device__ __forceinline__ void operator()(const f32x4 (&acc)[2][2][4][2], const Unit& u, int wr, int wc, int fr, int fq) const {
; #pragma unroll
;         for (int ai = 0; ai < 2; ++ai)
; #pragma unroll
;             for (int m = 0; m < 4; ++m) store_rows_bf16(O, (size_t)ldc, u.pm * BM + wr * 64 + ai * HALF + m * 16, u.pn * BM + wc * 64, fr, fq, pack8(acc[ai][0][m][0], acc[ai][0][m][1]), pack8(acc[ai][1][m][0], acc[ai][1][m][1]));
;     }
	global_store_dwordx4 v[90:91], v[82:85], off
	s_nop 1
	v_add_co_u32_e32 v82, vcc, s45, v90
	s_nop 1
	v_addc_co_u32_e32 v83, vcc, 0, v91, vcc
	global_store_dwordx4 v[82:83], v[86:89], off
	v_cvt_pk_bf16_f32 v78, v78, v79
	v_cvt_pk_bf16_f32 v79, v80, v81
	v_cvt_pk_bf16_f32 v74, v74, v75
	v_cvt_pk_bf16_f32 v75, v76, v77
	v_cvt_pk_bf16_f32 v70, v70, v71
	v_cvt_pk_bf16_f32 v71, v72, v73
	v_cvt_pk_bf16_f32 v66, v66, v67
	v_cvt_pk_bf16_f32 v67, v68, v69
	s_nop 0
	v_cndmask_b32_e64 v69, v74, v66, s[2:3]
	v_cndmask_b32_e64 v68, v75, v67, s[2:3]
	v_cndmask_b32_e64 v72, v79, v71, s[2:3]
	v_cndmask_b32_e64 v73, v78, v70, s[2:3]
	v_mov_b32_dpp v69, v69 row_ror:8 row_mask:0xf bank_mask:0xf
	v_mov_b32_dpp v68, v68 row_ror:8 row_mask:0xf bank_mask:0xf
	v_mov_b32_dpp v72, v72 row_ror:8 row_mask:0xf bank_mask:0xf
	v_mov_b32_dpp v73, v73 row_ror:8 row_mask:0xf bank_mask:0xf
	s_waitcnt lgkmcnt(0)
	v_cndmask_b32_e64 v74, v69, v74, s[2:3]
	v_cndmask_b32_e64 v75, v68, v75, s[2:3]
	v_cndmask_b32_e64 v76, v72, v79, s[2:3]
	v_cndmask_b32_e64 v77, v73, v78, s[2:3]
	v_cndmask_b32_e64 v78, v67, v68, s[2:3]
	ds_bpermute_b32 v68, v150, v74
	v_or_b32_e32 v74, 48, v148
	v_cndmask_b32_e64 v79, v66, v69, s[2:3]
	ds_bpermute_b32 v66, v150, v77
	ds_bpermute_b32 v67, v150, v76
	ds_bpermute_b32 v69, v150, v75
	v_ashrrev_i32_e32 v75, 31, v74
	v_cndmask_b32_e64 v71, v71, v72, s[2:3]
	v_cndmask_b32_e64 v70, v70, v73, s[2:3]
	v_lshlrev_b64 v[74:75], 11, v[74:75]
	ds_bpermute_b32 v70, v150, v70
	ds_bpermute_b32 v71, v150, v71
	ds_bpermute_b32 v72, v150, v79
	ds_bpermute_b32 v73, v150, v78
	v_lshl_add_u64 v[74:75], s[20:21], 0, v[74:75]
	v_lshl_add_u64 v[74:75], v[74:75], 0, s[30:31]
	v_lshl_add_u64 v[74:75], v[74:75], 0, v[138:139]
	s_waitcnt lgkmcnt(0)
	global_store_dwordx4 v[74:75], v[66:69], off
	s_nop 1
	v_add_co_u32_e32 v66, vcc, s45, v74
	s_nop 1
	v_addc_co_u32_e32 v67, vcc, 0, v75, vcc
	global_store_dwordx4 v[66:67], v[70:73], off
	v_cvt_pk_bf16_f32 v62, v62, v63
	v_cvt_pk_bf16_f32 v63, v64, v65
	v_cvt_pk_bf16_f32 v59, v58, v59
	v_cvt_pk_bf16_f32 v60, v60, v61
	v_cvt_pk_bf16_f32 v54, v54, v55
	v_cvt_pk_bf16_f32 v55, v56, v57
	v_cvt_pk_bf16_f32 v50, v50, v51
	v_cvt_pk_bf16_f32 v51, v52, v53
	v_add_u32_e32 v58, 0x80, v148
	v_cndmask_b32_e64 v52, v60, v51, s[2:3]
	v_cndmask_b32_e64 v53, v59, v50, s[2:3]
	v_cndmask_b32_e64 v56, v63, v55, s[2:3]
	v_cndmask_b32_e64 v57, v62, v54, s[2:3]
	v_mov_b32_dpp v52, v52 row_ror:8 row_mask:0xf bank_mask:0xf
	v_mov_b32_dpp v53, v53 row_ror:8 row_mask:0xf bank_mask:0xf
	v_mov_b32_dpp v56, v56 row_ror:8 row_mask:0xf bank_mask:0xf
	v_mov_b32_dpp v57, v57 row_ror:8 row_mask:0xf bank_mask:0xf
	s_waitcnt lgkmcnt(0)
	v_cndmask_b32_e64 v60, v52, v60, s[2:3]
	v_cndmask_b32_e64 v59, v53, v59, s[2:3]
	v_cndmask_b32_e64 v61, v56, v63, s[2:3]
	v_cndmask_b32_e64 v62, v57, v62, s[2:3]
	v_cndmask_b32_e64 v63, v51, v52, s[2:3]
	v_cndmask_b32_e64 v64, v50, v53, s[2:3]
	ds_bpermute_b32 v50, v150, v62
	ds_bpermute_b32 v51, v150, v61
	ds_bpermute_b32 v52, v150, v59
	ds_bpermute_b32 v53, v150, v60
	v_ashrrev_i32_e32 v59, 31, v58
	v_cndmask_b32_e64 v55, v55, v56, s[2:3]
	v_cndmask_b32_e64 v54, v54, v57, s[2:3]
	v_lshlrev_b64 v[58:59], 11, v[58:59]
	ds_bpermute_b32 v54, v150, v54
	ds_bpermute_b32 v55, v150, v55
	ds_bpermute_b32 v56, v150, v64
	ds_bpermute_b32 v57, v150, v63
	v_lshl_add_u64 v[58:59], s[20:21], 0, v[58:59]
	v_lshl_add_u64 v[58:59], v[58:59], 0, s[30:31]
	v_lshl_add_u64 v[58:59], v[58:59], 0, v[138:139]
	s_waitcnt lgkmcnt(0)
	global_store_dwordx4 v[58:59], v[50:53], off
	s_nop 1
	v_add_co_u32_e32 v50, vcc, s45, v58
	s_nop 1
	v_addc_co_u32_e32 v51, vcc, 0, v59, vcc
	global_store_dwordx4 v[50:51], v[54:57], off
	v_cvt_pk_bf16_f32 v46, v46, v47
	v_cvt_pk_bf16_f32 v47, v48, v49
	v_cvt_pk_bf16_f32 v42, v42, v43
	v_cvt_pk_bf16_f32 v43, v44, v45
	v_cvt_pk_bf16_f32 v38, v38, v39
	v_cvt_pk_bf16_f32 v39, v40, v41
	v_cvt_pk_bf16_f32 v34, v34, v35
	v_cvt_pk_bf16_f32 v35, v36, v37
	s_nop 0
	v_cndmask_b32_e64 v37, v42, v34, s[2:3]
	v_cndmask_b32_e64 v36, v43, v35, s[2:3]
	v_cndmask_b32_e64 v40, v47, v39, s[2:3]
	v_cndmask_b32_e64 v41, v46, v38, s[2:3]
	v_mov_b32_dpp v37, v37 row_ror:8 row_mask:0xf bank_mask:0xf
	v_mov_b32_dpp v36, v36 row_ror:8 row_mask:0xf bank_mask:0xf
	v_mov_b32_dpp v40, v40 row_ror:8 row_mask:0xf bank_mask:0xf
	v_mov_b32_dpp v41, v41 row_ror:8 row_mask:0xf bank_mask:0xf
	s_waitcnt lgkmcnt(0)
; __device__ __forceinline__ u32x4 pack8(const f32x4& v0, const f32x4& v1) { u32x4 w; w.x = cvt_pk_bf16(v0[0], v0[1]); w.y = cvt_pk_bf16(v0[2], v0[3]); w.z = cvt_pk_bf16(v1[0], v1[1]); w.w = cvt_pk_bf16(v1[2], v1[3]); return w; }
; __device__ __forceinline__ u32x4 xor8_16B(u32x4 v) { u32x4 r; r.x = (unsigned)__shfl_xor((int)v.x, 8); r.y = (unsigned)__shfl_xor((int)v.y, 8); r.z = (unsigned)__shfl_xor((int)v.z, 8); r.w = (unsigned)__shfl_xor((int)v.w, 8); return r; }
; #define PG8_BAR __builtin_amdgcn_s_barrier()
; __device__ __forceinline__ void store_rows_bf16(bf16_t* O, size_t ldc, int r0, int c0, int fr, int fq, u32x4 w0, u32x4 w1) {
;     const bool h = fr & 8; const u32x4 recv = xor8_16B(h ? w0 : w1);
;     const u32x4 d1 = h ? recv : w0, d2 = h ? w1 : recv;
;     const int lane = fr + 16 * fq, src = ((lane >> 3) + 8 * ((lane >> 2) & 1) + 16 * (lane & 3)) * 4;
;     const u32x4 e1 = bperm_16B(src, d1), e2 = bperm_16B(src, d2);
;     bf16_t* p = O + (size_t)(r0 + (lane >> 3)) * ldc + c0 + 8 * (lane & 7);
;     *(u32x4*)p = e1; *(u32x4*)(p + 8 * ldc) = e2;
;     __device__ __forceinline__ void operator()(const f32x4 (&acc)[2][2][4][2], const Unit& u, int wr, int wc, int fr, int fq) const {
; #pragma unroll
;         for (int ai = 0; ai < 2; ++ai)
; #pragma unroll
;             for (int m = 0; m < 4; ++m) store_rows_bf16(O, (size_t)ldc, u.pm * BM + wr * 64 + ai * HALF + m * 16, u.pn * BM + wc * 64, fr, fq, pack8(acc[ai][0][m][0], acc[ai][0][m][1]), pack8(acc[ai][1][m][0], acc[ai][1][m][1]));
;     }
; template <class Epi, class Sched, bool ALIGN_EPI = false, bool SP2 = false>
; __device__ __forceinline__ void gemm_phase(PG8_LAS unsigned char* lds, const Gemm g, const Sched& S, const Epi& E) {
;     ...
;         if (!has_next) break;
; #pragma unroll
;         for (int a = 0; a < 2; ++a)
; #pragma unroll
;             for (int b = 0; b < 2; ++b)
; #pragma unroll
;                 for (int m = 0; m < 4; ++m)
; #pragma unroll
;                     for (int n = 0; n < 2; ++n) acc[a][b][m][n] = (f32x4){0.f, 0.f, 0.f, 0.f};
;         cur = nxt; cA = nA; cB = nB; ++ui;
;         if constexpr (ALIGN_EPI) { if (wr == 1) PG8_BAR; }
	v_cndmask_b32_e64 v42, v37, v42, s[2:3]
	v_cndmask_b32_e64 v43, v36, v43, s[2:3]
	v_cndmask_b32_e64 v44, v40, v47, s[2:3]
	v_cndmask_b32_e64 v45, v41, v46, s[2:3]
	v_cndmask_b32_e64 v46, v35, v36, s[2:3]
	ds_bpermute_b32 v36, v150, v42
	v_add_u32_e32 v42, 0x90, v148
	v_cndmask_b32_e64 v47, v34, v37, s[2:3]
	ds_bpermute_b32 v34, v150, v45
	ds_bpermute_b32 v35, v150, v44
	ds_bpermute_b32 v37, v150, v43
	v_ashrrev_i32_e32 v43, 31, v42
	v_cndmask_b32_e64 v39, v39, v40, s[2:3]
	v_cndmask_b32_e64 v38, v38, v41, s[2:3]
	v_lshlrev_b64 v[42:43], 11, v[42:43]
	ds_bpermute_b32 v38, v150, v38
	ds_bpermute_b32 v39, v150, v39
	ds_bpermute_b32 v40, v150, v47
	ds_bpermute_b32 v41, v150, v46
	v_lshl_add_u64 v[42:43], s[20:21], 0, v[42:43]
	v_lshl_add_u64 v[42:43], v[42:43], 0, s[30:31]
	v_lshl_add_u64 v[42:43], v[42:43], 0, v[138:139]
	s_waitcnt lgkmcnt(0)
	global_store_dwordx4 v[42:43], v[34:37], off
	s_nop 1
	v_add_co_u32_e32 v34, vcc, s45, v42
	s_nop 1
	v_addc_co_u32_e32 v35, vcc, 0, v43, vcc
	global_store_dwordx4 v[34:35], v[38:41], off
	v_cvt_pk_bf16_f32 v30, v30, v31
	v_cvt_pk_bf16_f32 v31, v32, v33
	v_cvt_pk_bf16_f32 v26, v26, v27
	v_cvt_pk_bf16_f32 v27, v28, v29
	v_cvt_pk_bf16_f32 v22, v22, v23
	v_cvt_pk_bf16_f32 v23, v24, v25
	v_cvt_pk_bf16_f32 v18, v18, v19
	v_cvt_pk_bf16_f32 v19, v20, v21
	s_nop 0
	v_cndmask_b32_e64 v21, v26, v18, s[2:3]
	v_cndmask_b32_e64 v20, v27, v19, s[2:3]
	v_cndmask_b32_e64 v24, v31, v23, s[2:3]
	v_cndmask_b32_e64 v25, v30, v22, s[2:3]
	v_mov_b32_dpp v21, v21 row_ror:8 row_mask:0xf bank_mask:0xf
	v_mov_b32_dpp v20, v20 row_ror:8 row_mask:0xf bank_mask:0xf
	v_mov_b32_dpp v24, v24 row_ror:8 row_mask:0xf bank_mask:0xf
	v_mov_b32_dpp v25, v25 row_ror:8 row_mask:0xf bank_mask:0xf
	s_waitcnt lgkmcnt(0)
	v_cndmask_b32_e64 v26, v21, v26, s[2:3]
	v_cndmask_b32_e64 v27, v20, v27, s[2:3]
	v_cndmask_b32_e64 v28, v24, v31, s[2:3]
	v_cndmask_b32_e64 v29, v25, v30, s[2:3]
	v_cndmask_b32_e64 v30, v19, v20, s[2:3]
	ds_bpermute_b32 v20, v150, v26
	v_add_u32_e32 v26, 0xa0, v148
	v_cndmask_b32_e64 v31, v18, v21, s[2:3]
	ds_bpermute_b32 v18, v150, v29
	ds_bpermute_b32 v19, v150, v28
	ds_bpermute_b32 v21, v150, v27
	v_ashrrev_i32_e32 v27, 31, v26
	v_cndmask_b32_e64 v23, v23, v24, s[2:3]
	v_cndmask_b32_e64 v22, v22, v25, s[2:3]
	v_lshlrev_b64 v[26:27], 11, v[26:27]
	ds_bpermute_b32 v22, v150, v22
	ds_bpermute_b32 v23, v150, v23
	ds_bpermute_b32 v24, v150, v31
	ds_bpermute_b32 v25, v150, v30
	v_lshl_add_u64 v[26:27], s[20:21], 0, v[26:27]
	v_lshl_add_u64 v[26:27], v[26:27], 0, s[30:31]
	v_lshl_add_u64 v[26:27], v[26:27], 0, v[138:139]
	s_waitcnt lgkmcnt(0)
	global_store_dwordx4 v[26:27], v[18:21], off
	s_nop 1
	v_add_co_u32_e32 v18, vcc, s45, v26
	s_nop 1
	v_addc_co_u32_e32 v19, vcc, 0, v27, vcc
	global_store_dwordx4 v[18:19], v[22:25], off
	v_cvt_pk_bf16_f32 v14, v14, v15
	v_cvt_pk_bf16_f32 v15, v16, v17
	v_cvt_pk_bf16_f32 v6, v6, v7
	v_cvt_pk_bf16_f32 v7, v8, v9
	v_cvt_pk_bf16_f32 v8, v10, v11
	v_cvt_pk_bf16_f32 v9, v12, v13
	v_cvt_pk_bf16_f32 v2, v2, v3
	v_cvt_pk_bf16_f32 v3, v4, v5
	s_nop 0
	v_cndmask_b32_e64 v4, v7, v3, s[2:3]
	v_cndmask_b32_e64 v5, v6, v2, s[2:3]
	v_cndmask_b32_e64 v10, v15, v9, s[2:3]
	v_cndmask_b32_e64 v11, v14, v8, s[2:3]
	v_mov_b32_dpp v4, v4 row_ror:8 row_mask:0xf bank_mask:0xf
	v_mov_b32_dpp v5, v5 row_ror:8 row_mask:0xf bank_mask:0xf
	v_mov_b32_dpp v10, v10 row_ror:8 row_mask:0xf bank_mask:0xf
	v_mov_b32_dpp v11, v11 row_ror:8 row_mask:0xf bank_mask:0xf
	s_waitcnt lgkmcnt(0)
	v_cndmask_b32_e64 v7, v4, v7, s[2:3]
	v_cndmask_b32_e64 v6, v5, v6, s[2:3]
	v_cndmask_b32_e64 v12, v10, v15, s[2:3]
	v_cndmask_b32_e64 v13, v11, v14, s[2:3]
	v_cndmask_b32_e64 v9, v9, v10, s[2:3]
	v_add_u32_e32 v10, 0xb0, v148
	v_cndmask_b32_e64 v14, v3, v4, s[2:3]
	v_cndmask_b32_e64 v15, v2, v5, s[2:3]
	v_cndmask_b32_e64 v8, v8, v11, s[2:3]
	ds_bpermute_b32 v2, v150, v13
	ds_bpermute_b32 v3, v150, v12
	ds_bpermute_b32 v4, v150, v6
	ds_bpermute_b32 v5, v150, v7
	v_ashrrev_i32_e32 v11, 31, v10
	v_lshlrev_b64 v[10:11], 11, v[10:11]
	v_lshl_add_u64 v[10:11], s[20:21], 0, v[10:11]
	ds_bpermute_b32 v6, v150, v8
	ds_bpermute_b32 v7, v150, v9
	ds_bpermute_b32 v8, v150, v15
	ds_bpermute_b32 v9, v150, v14
	v_lshl_add_u64 v[10:11], v[10:11], 0, s[30:31]
	v_lshl_add_u64 v[10:11], v[10:11], 0, v[138:139]
	s_waitcnt lgkmcnt(0)
	global_store_dwordx4 v[10:11], v[2:5], off
	s_nop 1
	v_add_co_u32_e32 v2, vcc, 0x4000, v10
	s_nop 1
	v_addc_co_u32_e32 v3, vcc, 0, v11, vcc
	s_and_b64 vcc, exec, s[4:5]
	s_mov_b64 s[4:5], -1
	global_store_dwordx4 v[2:3], v[6:9], off
	s_cbranch_vccnz .LBB0_1579
	s_andn2_b64 vcc, exec, s[18:19]
	s_cbranch_vccnz .LBB0_1578
	s_barrier
	s_branch .LBB0_1578

; __device__ __forceinline__ float sigm(float x) { return __builtin_amdgcn_rcpf(1.0f + __builtin_amdgcn_exp2f(-1.4426950408889634f * x)); }
; __device__ __forceinline__ u32x4 pack8(const f32x4& v0, const f32x4& v1) { u32x4 w; w.x = cvt_pk_bf16(v0[0], v0[1]); w.y = cvt_pk_bf16(v0[2], v0[3]); w.z = cvt_pk_bf16(v1[0], v1[1]); w.w = cvt_pk_bf16(v1[2], v1[3]); return w; }
; __device__ __forceinline__ void unpack8(const u32x4& w, f32x4& v0, f32x4& v1) { v0[0] = bf_lo(w.x); v0[1] = bf_hi(w.x); v0[2] = bf_lo(w.y); v0[3] = bf_hi(w.y); v1[0] = bf_lo(w.z); v1[1] = bf_hi(w.z); v1[2] = bf_lo(w.w); v1[3] = bf_hi(w.w); }
; __device__ __forceinline__ void store_rows_bf16(bf16_t* O, size_t ldc, int r0, int c0, int fr, int fq, u32x4 w0, u32x4 w1) {
;     const bool h = fr & 8; const u32x4 recv = xor8_16B(h ? w0 : w1);
;     const u32x4 d1 = h ? recv : w0, d2 = h ? w1 : recv;
;     const int lane = fr + 16 * fq, src = ((lane >> 3) + 8 * ((lane >> 2) & 1) + 16 * (lane & 3)) * 4;
;     const u32x4 e1 = bperm_16B(src, d1), e2 = bperm_16B(src, d2);
;     __device__ __forceinline__ void operator()(const f32x4 (&acc)[2][2][4][2], const Unit& u, int wr, int wc, int fr, int fq) const {
;         const int row0 = u.pm * BM + wr * 64 + fr;
;         float sq_next = ssq[row0];
; #pragma unroll
;         for (int ai = 0; ai < 2; ++ai)
; #pragma unroll
;             for (int m = 0; m < 4; ++m) { const int row = row0 + ai * HALF + m * 16; const float sq = sq_next; u32x4 wx[2];
;                 if (!(ai == 1 && m == 3)) sq_next = ssq[row0 + (m == 3 ? HALF : ai * HALF + (m + 1) * 16)];
;                 const float rstd = rsqrtf(sq * (1.0f / 1024.0f) + 1e-6f);
; #pragma unroll
;                 for (int bj = 0; bj < 2; ++bj) { const int ct = wc * 64 + bj * 32 + 8 * fq; f32x4 v0 = acc[ai][bj][m][0] * rstd, v1 = acc[ai][bj][m][1] * rstd;
;                     const size_t o = (size_t)row * 1024 + u.pn * BM + ct; f32x4 e0, e1, r0, r1; unpack8(*(const u32x4*)(e + o), e0, e1); unpack8(*(const u32x4*)(x2 + o), r0, r1);
; #pragma unroll
;                     for (int i = 0; i < 4; ++i) { v0[i] = r0[i] + sigm(v0[i]) * e0[i]; v1[i] = r1[i] + sigm(v1[i]) * e1[i]; }
;                     wx[bj] = pack8(v0, v1); }
;                 store_rows_bf16(x3, 1024, u.pm * BM + wr * 64 + ai * HALF + m * 16, u.pn * BM + wc * 64, fr, fq, wx[0], wx[1]); }
.LBB0_1628:
	s_lshl_b32 s47, s78, 8
	s_add_i32 s47, s47, s59
	v_or_b32_e32 v8, s47, v1
	v_ashrrev_i32_e32 v9, 31, v8
	v_lshl_add_u64 v[6:7], v[8:9], 2, s[26:27]
	global_load_dword v22, v[6:7], off
	s_lshl_b32 s48, s79, 8
	s_ashr_i32 s49, s48, 31
	v_lshlrev_b64 v[2:3], 10, v[8:9]
	v_lshl_add_u64 v[4:5], v[2:3], 0, s[48:49]
	v_or_b32_e32 v2, v4, v172
	v_mov_b32_e32 v3, v5
	v_lshlrev_b64 v[2:3], 1, v[2:3]
	v_lshl_add_u64 v[10:11], s[24:25], 0, v[2:3]
	global_load_dwordx4 v[12:15], v[10:11], off
	v_lshl_add_u64 v[2:3], s[16:17], 0, v[2:3]
	global_load_dwordx4 v[16:19], v[2:3], off
	v_or_b32_e32 v10, 16, v8
	v_ashrrev_i32_e32 v11, 31, v10
	v_lshl_add_u64 v[2:3], v[10:11], 2, s[26:27]
	global_load_dword v9, v[2:3], off
	v_or_b32_e32 v2, v4, v174
	v_mov_b32_e32 v3, v5
	v_lshlrev_b64 v[2:3], 1, v[2:3]
	v_lshl_add_u64 v[20:21], s[24:25], 0, v[2:3]
	v_lshl_add_u64 v[2:3], s[16:17], 0, v[2:3]
	s_or_b32 s46, s48, s67
	v_lshlrev_b64 v[10:11], 10, v[10:11]
	s_waitcnt vmcnt(0)
	v_fmamk_f32 v22, v22, 0x3a800000, v202
	v_mul_f32_e32 v23, 0x4b800000, v22
	v_cmp_gt_f32_e32 vcc, s75, v22
	v_and_b32_e32 v24, 0xffff0000, v12
	s_nop 0
	v_cndmask_b32_e32 v22, v22, v23, vcc
	v_rsq_f32_e32 v22, v22
	v_lshlrev_b32_e32 v23, 16, v12
	v_lshlrev_b32_e32 v27, 16, v14
	v_and_b32_e32 v28, 0xffff0000, v14
	v_mul_f32_e32 v12, 0x45800000, v22
	v_cndmask_b32_e32 v22, v22, v12, vcc
	v_lshlrev_b32_e32 v29, 16, v15
	v_and_b32_e32 v30, 0xffff0000, v15
	v_pk_mul_f32 v[14:15], v[158:159], v[22:23] op_sel_hi:[1,0]
	v_lshlrev_b32_e32 v25, 16, v13
	v_and_b32_e32 v26, 0xffff0000, v13
	v_lshlrev_b32_e32 v31, 16, v16
	v_and_b32_e32 v32, 0xffff0000, v16
	v_lshlrev_b32_e32 v33, 16, v17
	v_and_b32_e32 v184, 0xffff0000, v17
	v_lshlrev_b32_e32 v185, 16, v18
	v_and_b32_e32 v186, 0xffff0000, v18
	v_lshlrev_b32_e32 v187, 16, v19
	v_and_b32_e32 v188, 0xffff0000, v19
	v_pk_mul_f32 v[12:13], v[160:161], v[22:23] op_sel_hi:[1,0]
	v_pk_mul_f32 v[16:17], v[156:157], v[22:23] op_sel_hi:[1,0]
	v_pk_mul_f32 v[18:19], v[154:155], v[22:23] op_sel_hi:[1,0]
	v_mul_f32_e32 v14, 0xbfb8aa3b, v14
	v_mul_f32_e32 v15, 0xbfb8aa3b, v15
	v_mul_f32_e32 v18, 0xbfb8aa3b, v18
	v_mul_f32_e32 v19, 0xbfb8aa3b, v19
	v_mul_f32_e32 v12, 0xbfb8aa3b, v12
	v_mul_f32_e32 v16, 0xbfb8aa3b, v16
	v_mul_f32_e32 v13, 0xbfb8aa3b, v13
	v_mul_f32_e32 v17, 0xbfb8aa3b, v17
	v_exp_f32_e32 v14, v14
	v_exp_f32_e32 v15, v15
	v_exp_f32_e32 v18, v18
	v_exp_f32_e32 v19, v19
	v_exp_f32_e32 v12, v12
	v_exp_f32_e32 v16, v16
	v_exp_f32_e32 v13, v13
	v_exp_f32_e32 v17, v17
	v_add_f32_e32 v14, 1.0, v14
	v_add_f32_e32 v15, 1.0, v15
	v_add_f32_e32 v18, 1.0, v18
	v_add_f32_e32 v19, 1.0, v19
	v_add_f32_e32 v12, 1.0, v12
	v_add_f32_e32 v16, 1.0, v16
	v_add_f32_e32 v13, 1.0, v13
	v_add_f32_e32 v17, 1.0, v17
	v_rcp_f32_e32 v14, v14
	v_rcp_f32_e32 v15, v15
	v_rcp_f32_e32 v18, v18
	v_rcp_f32_e32 v19, v19
	v_rcp_f32_e32 v12, v12
	v_rcp_f32_e32 v16, v16
	v_rcp_f32_e32 v13, v13
	v_rcp_f32_e32 v17, v17
	v_fmac_f32_e32 v31, v14, v23
	v_fmac_f32_e32 v32, v15, v24
	v_fmac_f32_e32 v185, v18, v27
	v_fmac_f32_e32 v186, v19, v28
	v_fmac_f32_e32 v33, v12, v25
	v_fmac_f32_e32 v187, v16, v29
	v_fmac_f32_e32 v184, v13, v26
	v_fmac_f32_e32 v188, v17, v30
	v_cvt_pk_bf16_f32 v13, v31, v32
	v_cvt_pk_bf16_f32 v30, v33, v184
	v_cvt_pk_bf16_f32 v31, v185, v186
	v_cvt_pk_bf16_f32 v32, v187, v188
	global_load_dwordx4 v[14:17], v[20:21], off
	v_pk_mul_f32 v[24:25], v[152:153], v[22:23] op_sel_hi:[1,0]
	global_load_dwordx4 v[18:21], v[2:3], off
	v_and_b32_e32 v2, 64, v203
	v_xor_b32_e32 v3, 8, v203
	v_add_u32_e32 v12, 64, v2
	v_cmp_lt_i32_e32 vcc, v3, v12
	v_pk_mul_f32 v[26:27], v[150:151], v[22:23] op_sel_hi:[1,0]
	v_pk_mul_f32 v[28:29], v[148:149], v[22:23] op_sel_hi:[1,0]
	v_cndmask_b32_e32 v3, v203, v3, vcc
	v_pk_mul_f32 v[22:23], v[146:147], v[22:23] op_sel_hi:[1,0]
	v_lshlrev_b32_e32 v12, 2, v3
	v_mul_f32_e32 v3, 0xbfb8aa3b, v26
	v_mul_f32_e32 v26, 0xbfb8aa3b, v27
	v_mul_f32_e32 v23, 0xbfb8aa3b, v23
	v_mul_f32_e32 v25, 0xbfb8aa3b, v25
	v_mul_f32_e32 v22, 0xbfb8aa3b, v22
	v_mul_f32_e32 v24, 0xbfb8aa3b, v24
	v_mul_f32_e32 v27, 0xbfb8aa3b, v28
	v_mul_f32_e32 v28, 0xbfb8aa3b, v29
	v_exp_f32_e32 v26, v26
	v_exp_f32_e32 v23, v23
	v_exp_f32_e32 v25, v25
	v_exp_f32_e32 v3, v3
	v_exp_f32_e32 v22, v22
	v_exp_f32_e32 v24, v24
	v_exp_f32_e32 v27, v27
	v_exp_f32_e32 v28, v28
	v_add_f32_e32 v26, 1.0, v26
	v_add_f32_e32 v23, 1.0, v23
	v_add_f32_e32 v25, 1.0, v25
	v_add_f32_e32 v3, 1.0, v3
	v_add_f32_e32 v22, 1.0, v22
	v_add_f32_e32 v24, 1.0, v24
	v_add_f32_e32 v27, 1.0, v27
	v_add_f32_e32 v28, 1.0, v28
	v_rcp_f32_e32 v26, v26
	v_rcp_f32_e32 v23, v23
	v_rcp_f32_e32 v25, v25
	v_rcp_f32_e32 v3, v3
	v_rcp_f32_e32 v22, v22
	v_rcp_f32_e32 v24, v24
	v_rcp_f32_e32 v27, v27
	v_rcp_f32_e32 v28, v28
	v_or_b32_e32 v2, s47, v175
	s_ashr_i32 s47, s46, 31
	s_lshl_b64 s[46:47], s[46:47], 1
	s_waitcnt vmcnt(0)
	v_lshlrev_b32_e32 v29, 16, v14
	v_and_b32_e32 v14, 0xffff0000, v14
	v_lshlrev_b32_e32 v33, 16, v15
	v_and_b32_e32 v15, 0xffff0000, v15
	v_lshlrev_b32_e32 v146, 16, v16
	v_and_b32_e32 v16, 0xffff0000, v16
	v_lshlrev_b32_e32 v148, 16, v18
	v_and_b32_e32 v18, 0xffff0000, v18
	v_lshlrev_b32_e32 v149, 16, v19
	v_and_b32_e32 v19, 0xffff0000, v19
	v_lshlrev_b32_e32 v150, 16, v20
	v_and_b32_e32 v20, 0xffff0000, v20
	v_lshlrev_b32_e32 v147, 16, v17
	v_and_b32_e32 v17, 0xffff0000, v17
	v_lshlrev_b32_e32 v151, 16, v21
	v_and_b32_e32 v21, 0xffff0000, v21
	v_fmac_f32_e32 v18, v26, v14
	v_fmac_f32_e32 v20, v23, v16
	v_fmac_f32_e32 v19, v25, v15
	v_fmac_f32_e32 v148, v3, v29
	v_fmac_f32_e32 v150, v22, v146
	v_fmac_f32_e32 v149, v24, v33
	v_fmac_f32_e32 v151, v27, v147
	v_fmac_f32_e32 v21, v28, v17
	v_cvt_pk_bf16_f32 v14, v148, v18
	v_cvt_pk_bf16_f32 v15, v149, v19
	v_cvt_pk_bf16_f32 v16, v150, v20
	v_cvt_pk_bf16_f32 v17, v151, v21
	s_nop 0
	v_cndmask_b32_e64 v3, v32, v17, s[4:5]
	v_cndmask_b32_e64 v18, v31, v16, s[4:5]
	v_cndmask_b32_e64 v19, v30, v15, s[4:5]
	v_cndmask_b32_e64 v20, v13, v14, s[4:5]
	v_mov_b32_dpp v21, v3 row_ror:8 row_mask:0xf bank_mask:0xf
	v_mov_b32_dpp v18, v18 row_ror:8 row_mask:0xf bank_mask:0xf
	v_mov_b32_dpp v19, v19 row_ror:8 row_mask:0xf bank_mask:0xf
	v_mov_b32_dpp v20, v20 row_ror:8 row_mask:0xf bank_mask:0xf
	v_ashrrev_i32_e32 v3, 31, v2
	s_waitcnt lgkmcnt(0)
; __device__ __forceinline__ float sigm(float x) { return __builtin_amdgcn_rcpf(1.0f + __builtin_amdgcn_exp2f(-1.4426950408889634f * x)); }
; __device__ __forceinline__ u32x4 pack8(const f32x4& v0, const f32x4& v1) { u32x4 w; w.x = cvt_pk_bf16(v0[0], v0[1]); w.y = cvt_pk_bf16(v0[2], v0[3]); w.z = cvt_pk_bf16(v1[0], v1[1]); w.w = cvt_pk_bf16(v1[2], v1[3]); return w; }
; __device__ __forceinline__ void unpack8(const u32x4& w, f32x4& v0, f32x4& v1) { v0[0] = bf_lo(w.x); v0[1] = bf_hi(w.x); v0[2] = bf_lo(w.y); v0[3] = bf_hi(w.y); v1[0] = bf_lo(w.z); v1[1] = bf_hi(w.z); v1[2] = bf_lo(w.w); v1[3] = bf_hi(w.w); }
; __device__ __forceinline__ void store_rows_bf16(bf16_t* O, size_t ldc, int r0, int c0, int fr, int fq, u32x4 w0, u32x4 w1) {
;     const bool h = fr & 8; const u32x4 recv = xor8_16B(h ? w0 : w1);
;     const u32x4 d1 = h ? recv : w0, d2 = h ? w1 : recv;
;     const int lane = fr + 16 * fq, src = ((lane >> 3) + 8 * ((lane >> 2) & 1) + 16 * (lane & 3)) * 4;
;     const u32x4 e1 = bperm_16B(src, d1), e2 = bperm_16B(src, d2);
;     bf16_t* p = O + (size_t)(r0 + (lane >> 3)) * ldc + c0 + 8 * (lane & 7);
;     *(u32x4*)p = e1; *(u32x4*)(p + 8 * ldc) = e2;
;     __device__ __forceinline__ void operator()(const f32x4 (&acc)[2][2][4][2], const Unit& u, int wr, int wc, int fr, int fq) const {
;     ...
;             for (int m = 0; m < 4; ++m) { const int row = row0 + ai * HALF + m * 16; const float sq = sq_next; u32x4 wx[2];
;                 if (!(ai == 1 && m == 3)) sq_next = ssq[row0 + (m == 3 ? HALF : ai * HALF + (m + 1) * 16)];
;                 const float rstd = rsqrtf(sq * (1.0f / 1024.0f) + 1e-6f);
; #pragma unroll
;                 for (int bj = 0; bj < 2; ++bj) { const int ct = wc * 64 + bj * 32 + 8 * fq; f32x4 v0 = acc[ai][bj][m][0] * rstd, v1 = acc[ai][bj][m][1] * rstd;
;                     const size_t o = (size_t)row * 1024 + u.pn * BM + ct; f32x4 e0, e1, r0, r1; unpack8(*(const u32x4*)(e + o), e0, e1); unpack8(*(const u32x4*)(x2 + o), r0, r1);
; #pragma unroll
;                     for (int i = 0; i < 4; ++i) { v0[i] = r0[i] + sigm(v0[i]) * e0[i]; v1[i] = r1[i] + sigm(v1[i]) * e1[i]; }
;                     wx[bj] = pack8(v0, v1); }
;                 store_rows_bf16(x3, 1024, u.pm * BM + wr * 64 + ai * HALF + m * 16, u.pn * BM + wc * 64, fr, fq, wx[0], wx[1]); }
	v_cndmask_b32_e64 v22, v21, v32, s[4:5]
	v_cndmask_b32_e64 v23, v18, v31, s[4:5]
	v_cndmask_b32_e64 v24, v19, v30, s[4:5]
	v_cndmask_b32_e64 v13, v20, v13, s[4:5]
	v_cndmask_b32_e64 v21, v17, v21, s[4:5]
	v_cndmask_b32_e64 v25, v16, v18, s[4:5]
	v_cndmask_b32_e64 v19, v15, v19, s[4:5]
	v_cndmask_b32_e64 v18, v14, v20, s[4:5]
	ds_bpermute_b32 v14, v196, v13
	ds_bpermute_b32 v15, v196, v24
	ds_bpermute_b32 v16, v196, v23
	ds_bpermute_b32 v17, v196, v22
	v_lshlrev_b64 v[22:23], 11, v[2:3]
	v_lshl_add_u64 v[22:23], s[22:23], 0, v[22:23]
	v_lshl_add_u64 v[22:23], v[22:23], 0, s[46:47]
	ds_bpermute_b32 v18, v196, v18
	ds_bpermute_b32 v19, v196, v19
	ds_bpermute_b32 v20, v196, v25
	ds_bpermute_b32 v21, v196, v21
	v_lshl_add_u64 v[22:23], v[22:23], 0, v[170:171]
	s_waitcnt lgkmcnt(4)
	global_store_dwordx4 v[22:23], v[14:17], off
	v_fmamk_f32 v3, v9, 0x3a800000, v202
	v_mul_f32_e32 v9, 0x4b800000, v3
	v_add_co_u32_e32 v14, vcc, s55, v22
	s_nop 1
	v_addc_co_u32_e32 v15, vcc, 0, v23, vcc
	v_lshl_add_u64 v[22:23], v[10:11], 0, s[48:49]
	v_or_b32_e32 v10, v22, v172
	v_mov_b32_e32 v11, v23
	v_lshlrev_b64 v[10:11], 1, v[10:11]
	s_waitcnt lgkmcnt(0)
	global_store_dwordx4 v[14:15], v[18:21], off
	v_lshl_add_u64 v[14:15], s[24:25], 0, v[10:11]
	v_lshl_add_u64 v[10:11], s[16:17], 0, v[10:11]
	global_load_dwordx4 v[14:17], v[14:15], off
	v_cmp_gt_f32_e32 vcc, s75, v3
	global_load_dwordx4 v[18:21], v[10:11], off
	v_or_b32_e32 v10, 32, v8
	v_cndmask_b32_e32 v3, v3, v9, vcc
	v_rsq_f32_e32 v3, v3
	v_ashrrev_i32_e32 v11, 31, v10
	v_lshl_add_u64 v[24:25], v[10:11], 2, s[26:27]
	global_load_dword v9, v[24:25], off
	v_mul_f32_e32 v13, 0x45800000, v3
	v_cndmask_b32_e32 v24, v3, v13, vcc
	v_pk_mul_f32 v[26:27], v[144:145], v[24:25] op_sel_hi:[1,0]
	v_pk_mul_f32 v[28:29], v[142:143], v[24:25] op_sel_hi:[1,0]
	v_pk_mul_f32 v[30:31], v[140:141], v[24:25] op_sel_hi:[1,0]
	v_pk_mul_f32 v[32:33], v[138:139], v[24:25] op_sel_hi:[1,0]
	v_mul_f32_e32 v25, 0xbfb8aa3b, v29
	v_mul_f32_e32 v27, 0xbfb8aa3b, v27
	v_mul_f32_e32 v3, 0xbfb8aa3b, v28
	v_mul_f32_e32 v13, 0xbfb8aa3b, v32
	v_mul_f32_e32 v26, 0xbfb8aa3b, v26
	v_exp_f32_e32 v25, v25
	v_exp_f32_e32 v27, v27
	v_mul_f32_e32 v28, 0xbfb8aa3b, v33
	v_mul_f32_e32 v29, 0xbfb8aa3b, v30
	v_mul_f32_e32 v30, 0xbfb8aa3b, v31
	v_exp_f32_e32 v3, v3
	v_exp_f32_e32 v13, v13
	v_exp_f32_e32 v26, v26
	v_exp_f32_e32 v28, v28
	v_exp_f32_e32 v30, v30
	v_exp_f32_e32 v29, v29
	v_add_f32_e32 v25, 1.0, v25
	v_add_f32_e32 v27, 1.0, v27
	v_add_f32_e32 v3, 1.0, v3
	v_add_f32_e32 v13, 1.0, v13
	v_add_f32_e32 v26, 1.0, v26
	v_rcp_f32_e32 v25, v25
	v_rcp_f32_e32 v27, v27
	v_add_f32_e32 v28, 1.0, v28
	v_add_f32_e32 v30, 1.0, v30
	v_rcp_f32_e32 v3, v3
	v_rcp_f32_e32 v13, v13
	v_rcp_f32_e32 v26, v26
	v_add_f32_e32 v29, 1.0, v29
	v_rcp_f32_e32 v28, v28
	v_rcp_f32_e32 v30, v30
	v_rcp_f32_e32 v29, v29
	v_or_b32_e32 v22, v22, v174
	v_lshlrev_b64 v[10:11], 10, v[10:11]
	v_lshl_add_u64 v[10:11], v[10:11], 0, s[48:49]
	v_or_b32_e32 v8, 48, v8
	s_waitcnt vmcnt(2)
	v_lshlrev_b32_e32 v31, 16, v14
	v_and_b32_e32 v14, 0xffff0000, v14
	v_lshlrev_b32_e32 v32, 16, v15
	v_and_b32_e32 v15, 0xffff0000, v15
	s_waitcnt vmcnt(1)
	v_lshlrev_b32_e32 v139, 16, v18
	v_and_b32_e32 v18, 0xffff0000, v18
	v_lshlrev_b32_e32 v140, 16, v19
	v_and_b32_e32 v19, 0xffff0000, v19
	v_lshlrev_b32_e32 v33, 16, v16
	v_lshlrev_b32_e32 v141, 16, v20
	v_fmac_f32_e32 v18, v25, v14
	v_fmac_f32_e32 v19, v27, v15
	v_and_b32_e32 v16, 0xffff0000, v16
	v_lshlrev_b32_e32 v138, 16, v17
	v_and_b32_e32 v17, 0xffff0000, v17
	v_and_b32_e32 v20, 0xffff0000, v20
	v_lshlrev_b32_e32 v142, 16, v21
	v_and_b32_e32 v21, 0xffff0000, v21
	v_fmac_f32_e32 v139, v3, v31
	v_fmac_f32_e32 v141, v13, v33
	v_fmac_f32_e32 v140, v26, v32
	v_cvt_pk_bf16_f32 v3, v139, v18
	v_cvt_pk_bf16_f32 v13, v140, v19
	v_lshlrev_b64 v[18:19], 1, v[22:23]
	v_fmac_f32_e32 v20, v28, v16
	v_fmac_f32_e32 v21, v30, v17
	v_lshl_add_u64 v[14:15], s[24:25], 0, v[18:19]
	v_lshl_add_u64 v[18:19], s[16:17], 0, v[18:19]
	v_fmac_f32_e32 v142, v29, v138
	v_cvt_pk_bf16_f32 v30, v141, v20
	v_cvt_pk_bf16_f32 v31, v142, v21
	global_load_dwordx4 v[14:17], v[14:15], off
	v_pk_mul_f32 v[26:27], v[134:135], v[24:25] op_sel_hi:[1,0]
	global_load_dwordx4 v[18:21], v[18:19], off
	v_pk_mul_f32 v[22:23], v[136:137], v[24:25] op_sel_hi:[1,0]
	v_pk_mul_f32 v[28:29], v[132:133], v[24:25] op_sel_hi:[1,0]
	v_pk_mul_f32 v[24:25], v[130:131], v[24:25] op_sel_hi:[1,0]
	v_mul_f32_e32 v27, 0xbfb8aa3b, v27
	v_mul_f32_e32 v26, 0xbfb8aa3b, v26
	v_mul_f32_e32 v24, 0xbfb8aa3b, v24
	v_mul_f32_e32 v25, 0xbfb8aa3b, v25
	v_mul_f32_e32 v22, 0xbfb8aa3b, v22
	v_mul_f32_e32 v28, 0xbfb8aa3b, v28
	v_mul_f32_e32 v23, 0xbfb8aa3b, v23
	v_mul_f32_e32 v29, 0xbfb8aa3b, v29
	v_exp_f32_e32 v27, v27
	v_exp_f32_e32 v26, v26
	v_exp_f32_e32 v24, v24
	v_exp_f32_e32 v25, v25
	v_exp_f32_e32 v22, v22
	v_exp_f32_e32 v28, v28
	v_exp_f32_e32 v23, v23
	v_exp_f32_e32 v29, v29
	v_add_f32_e32 v27, 1.0, v27
	v_add_f32_e32 v26, 1.0, v26
	v_add_f32_e32 v24, 1.0, v24
	v_add_f32_e32 v25, 1.0, v25
	v_add_f32_e32 v22, 1.0, v22
	v_add_f32_e32 v28, 1.0, v28
	v_add_f32_e32 v23, 1.0, v23
	v_add_f32_e32 v29, 1.0, v29
	v_rcp_f32_e32 v27, v27
	v_rcp_f32_e32 v26, v26
	v_rcp_f32_e32 v24, v24
	v_rcp_f32_e32 v25, v25
	v_rcp_f32_e32 v22, v22
	v_rcp_f32_e32 v28, v28
	v_rcp_f32_e32 v23, v23
	v_rcp_f32_e32 v29, v29
	s_waitcnt vmcnt(1)
	v_lshlrev_b32_e32 v32, 16, v14
	v_and_b32_e32 v14, 0xffff0000, v14
	s_waitcnt vmcnt(0)
; __device__ __forceinline__ float sigm(float x) { return __builtin_amdgcn_rcpf(1.0f + __builtin_amdgcn_exp2f(-1.4426950408889634f * x)); }
; __device__ __forceinline__ u32x4 pack8(const f32x4& v0, const f32x4& v1) { u32x4 w; w.x = cvt_pk_bf16(v0[0], v0[1]); w.y = cvt_pk_bf16(v0[2], v0[3]); w.z = cvt_pk_bf16(v1[0], v1[1]); w.w = cvt_pk_bf16(v1[2], v1[3]); return w; }
; __device__ __forceinline__ void unpack8(const u32x4& w, f32x4& v0, f32x4& v1) { v0[0] = bf_lo(w.x); v0[1] = bf_hi(w.x); v0[2] = bf_lo(w.y); v0[3] = bf_hi(w.y); v1[0] = bf_lo(w.z); v1[1] = bf_hi(w.z); v1[2] = bf_lo(w.w); v1[3] = bf_hi(w.w); }
; __device__ __forceinline__ void store_rows_bf16(bf16_t* O, size_t ldc, int r0, int c0, int fr, int fq, u32x4 w0, u32x4 w1) {
;     const bool h = fr & 8; const u32x4 recv = xor8_16B(h ? w0 : w1);
;     const u32x4 d1 = h ? recv : w0, d2 = h ? w1 : recv;
;     const int lane = fr + 16 * fq, src = ((lane >> 3) + 8 * ((lane >> 2) & 1) + 16 * (lane & 3)) * 4;
;     const u32x4 e1 = bperm_16B(src, d1), e2 = bperm_16B(src, d2);
;     bf16_t* p = O + (size_t)(r0 + (lane >> 3)) * ldc + c0 + 8 * (lane & 7);
;     *(u32x4*)p = e1; *(u32x4*)(p + 8 * ldc) = e2;
;     __device__ __forceinline__ void operator()(const f32x4 (&acc)[2][2][4][2], const Unit& u, int wr, int wc, int fr, int fq) const {
;     ...
;             for (int m = 0; m < 4; ++m) { const int row = row0 + ai * HALF + m * 16; const float sq = sq_next; u32x4 wx[2];
;                 if (!(ai == 1 && m == 3)) sq_next = ssq[row0 + (m == 3 ? HALF : ai * HALF + (m + 1) * 16)];
;                 const float rstd = rsqrtf(sq * (1.0f / 1024.0f) + 1e-6f);
; #pragma unroll
;                 for (int bj = 0; bj < 2; ++bj) { const int ct = wc * 64 + bj * 32 + 8 * fq; f32x4 v0 = acc[ai][bj][m][0] * rstd, v1 = acc[ai][bj][m][1] * rstd;
;                     const size_t o = (size_t)row * 1024 + u.pn * BM + ct; f32x4 e0, e1, r0, r1; unpack8(*(const u32x4*)(e + o), e0, e1); unpack8(*(const u32x4*)(x2 + o), r0, r1);
; #pragma unroll
;                     for (int i = 0; i < 4; ++i) { v0[i] = r0[i] + sigm(v0[i]) * e0[i]; v1[i] = r1[i] + sigm(v1[i]) * e1[i]; }
;                     wx[bj] = pack8(v0, v1); }
;                 store_rows_bf16(x3, 1024, u.pm * BM + wr * 64 + ai * HALF + m * 16, u.pn * BM + wc * 64, fr, fq, wx[0], wx[1]); }
	v_lshlrev_b32_e32 v132, 16, v18
	v_and_b32_e32 v18, 0xffff0000, v18
	v_lshlrev_b32_e32 v33, 16, v15
	v_and_b32_e32 v15, 0xffff0000, v15
	v_lshlrev_b32_e32 v130, 16, v16
	v_and_b32_e32 v16, 0xffff0000, v16
	v_lshlrev_b32_e32 v131, 16, v17
	v_and_b32_e32 v17, 0xffff0000, v17
	v_lshlrev_b32_e32 v133, 16, v19
	v_and_b32_e32 v19, 0xffff0000, v19
	v_lshlrev_b32_e32 v134, 16, v20
	v_and_b32_e32 v20, 0xffff0000, v20
	v_lshlrev_b32_e32 v135, 16, v21
	v_and_b32_e32 v21, 0xffff0000, v21
	v_fmac_f32_e32 v18, v27, v14
	v_fmac_f32_e32 v132, v26, v32
	v_fmac_f32_e32 v134, v24, v130
	v_fmac_f32_e32 v20, v25, v16
	v_fmac_f32_e32 v133, v22, v33
	v_fmac_f32_e32 v135, v28, v131
	v_fmac_f32_e32 v19, v23, v15
	v_fmac_f32_e32 v21, v29, v17
	v_cvt_pk_bf16_f32 v14, v132, v18
	v_cvt_pk_bf16_f32 v15, v133, v19
	v_cvt_pk_bf16_f32 v16, v134, v20
	v_cvt_pk_bf16_f32 v17, v135, v21
	s_nop 0
	v_cndmask_b32_e64 v18, v31, v17, s[4:5]
	v_cndmask_b32_e64 v19, v30, v16, s[4:5]
	v_cndmask_b32_e64 v20, v13, v15, s[4:5]
	v_cndmask_b32_e64 v21, v3, v14, s[4:5]
	v_mov_b32_dpp v18, v18 row_ror:8 row_mask:0xf bank_mask:0xf
	v_mov_b32_dpp v19, v19 row_ror:8 row_mask:0xf bank_mask:0xf
	v_mov_b32_dpp v20, v20 row_ror:8 row_mask:0xf bank_mask:0xf
	v_mov_b32_dpp v21, v21 row_ror:8 row_mask:0xf bank_mask:0xf
	s_waitcnt lgkmcnt(0)
	v_cndmask_b32_e64 v22, v18, v31, s[4:5]
	s_waitcnt lgkmcnt(0)
	v_cndmask_b32_e64 v23, v19, v30, s[4:5]
	s_waitcnt lgkmcnt(0)
	v_cndmask_b32_e64 v13, v20, v13, s[4:5]
	s_waitcnt lgkmcnt(0)
	v_cndmask_b32_e64 v3, v21, v3, s[4:5]
	v_cndmask_b32_e64 v24, v17, v18, s[4:5]
	ds_bpermute_b32 v17, v196, v22
	v_or_b32_e32 v22, 16, v2
	v_cndmask_b32_e64 v25, v16, v19, s[4:5]
	v_cndmask_b32_e64 v19, v15, v20, s[4:5]
	v_cndmask_b32_e64 v18, v14, v21, s[4:5]
	ds_bpermute_b32 v14, v196, v3
	ds_bpermute_b32 v15, v196, v13
	ds_bpermute_b32 v16, v196, v23
	v_ashrrev_i32_e32 v23, 31, v22
	v_lshlrev_b64 v[22:23], 11, v[22:23]
	ds_bpermute_b32 v18, v196, v18
	ds_bpermute_b32 v19, v196, v19
	ds_bpermute_b32 v20, v196, v25
	ds_bpermute_b32 v21, v196, v24
	v_lshl_add_u64 v[22:23], s[22:23], 0, v[22:23]
	v_lshl_add_u64 v[22:23], v[22:23], 0, s[46:47]
	v_lshl_add_u64 v[22:23], v[22:23], 0, v[170:171]
	s_waitcnt lgkmcnt(4)
	global_store_dwordx4 v[22:23], v[14:17], off
	v_fmamk_f32 v3, v9, 0x3a800000, v202
	v_mul_f32_e32 v9, 0x4b800000, v3
	v_add_co_u32_e32 v14, vcc, s55, v22
	s_nop 1
	v_addc_co_u32_e32 v15, vcc, 0, v23, vcc
	s_waitcnt lgkmcnt(0)
	global_store_dwordx4 v[14:15], v[18:21], off
	v_or_b32_e32 v14, v10, v172
	v_mov_b32_e32 v15, v11
	v_lshlrev_b64 v[18:19], 1, v[14:15]
	v_lshl_add_u64 v[14:15], s[24:25], 0, v[18:19]
	v_lshl_add_u64 v[18:19], s[16:17], 0, v[18:19]
	global_load_dwordx4 v[14:17], v[14:15], off
	v_cmp_gt_f32_e32 vcc, s75, v3
	global_load_dwordx4 v[18:21], v[18:19], off
	v_or_b32_e32 v10, v10, v174
	v_cndmask_b32_e32 v3, v3, v9, vcc
	v_rsq_f32_e32 v3, v3
	v_ashrrev_i32_e32 v9, 31, v8
	v_lshl_add_u64 v[22:23], v[8:9], 2, s[26:27]
	global_load_dword v13, v[22:23], off
	v_mul_f32_e32 v22, 0x45800000, v3
	v_cndmask_b32_e32 v22, v3, v22, vcc
	v_pk_mul_f32 v[26:27], v[126:127], v[22:23] op_sel_hi:[1,0]
	v_pk_mul_f32 v[30:31], v[122:123], v[22:23] op_sel_hi:[1,0]
	v_pk_mul_f32 v[24:25], v[128:129], v[22:23] op_sel_hi:[1,0]
	v_pk_mul_f32 v[28:29], v[124:125], v[22:23] op_sel_hi:[1,0]
	v_mul_f32_e32 v3, 0xbfb8aa3b, v26
	v_mul_f32_e32 v23, 0xbfb8aa3b, v30
	v_mul_f32_e32 v26, 0xbfb8aa3b, v27
	v_mul_f32_e32 v27, 0xbfb8aa3b, v31
	v_exp_f32_e32 v23, v23
	v_exp_f32_e32 v27, v27
	v_exp_f32_e32 v26, v26
	v_exp_f32_e32 v3, v3
	v_add_f32_e32 v23, 1.0, v23
	v_add_f32_e32 v27, 1.0, v27
	v_rcp_f32_e32 v23, v23
	v_rcp_f32_e32 v27, v27
	v_mul_f32_e32 v28, 0xbfb8aa3b, v28
	v_add_f32_e32 v26, 1.0, v26
	v_mul_f32_e32 v24, 0xbfb8aa3b, v24
	v_exp_f32_e32 v28, v28
	v_add_f32_e32 v3, 1.0, v3
	v_rcp_f32_e32 v26, v26
	v_exp_f32_e32 v24, v24
	v_rcp_f32_e32 v3, v3
	v_lshlrev_b64 v[10:11], 1, v[10:11]
	v_lshlrev_b64 v[8:9], 10, v[8:9]
	s_waitcnt vmcnt(2)
	v_lshlrev_b32_e32 v32, 16, v16
	v_and_b32_e32 v16, 0xffff0000, v16
	s_waitcnt vmcnt(1)
	v_lshlrev_b32_e32 v124, 16, v20
	v_and_b32_e32 v20, 0xffff0000, v20
	v_fmac_f32_e32 v124, v23, v32
	v_fmac_f32_e32 v20, v27, v16
	v_mul_f32_e32 v16, 0xbfb8aa3b, v25
	v_mul_f32_e32 v23, 0xbfb8aa3b, v29
	v_exp_f32_e32 v16, v16
	v_exp_f32_e32 v23, v23
	v_lshlrev_b32_e32 v30, 16, v14
	v_and_b32_e32 v14, 0xffff0000, v14
	v_lshlrev_b32_e32 v122, 16, v18
	v_and_b32_e32 v18, 0xffff0000, v18
	v_fmac_f32_e32 v18, v26, v14
	v_add_f32_e32 v14, 1.0, v28
	v_add_f32_e32 v16, 1.0, v16
	v_add_f32_e32 v23, 1.0, v23
	v_fmac_f32_e32 v122, v3, v30
	v_add_f32_e32 v3, 1.0, v24
	v_rcp_f32_e32 v14, v14
	v_rcp_f32_e32 v16, v16
	v_rcp_f32_e32 v23, v23
	v_rcp_f32_e32 v3, v3
	v_lshlrev_b32_e32 v31, 16, v15
	v_and_b32_e32 v15, 0xffff0000, v15
	v_lshlrev_b32_e32 v33, 16, v17
	v_and_b32_e32 v17, 0xffff0000, v17
	v_lshlrev_b32_e32 v123, 16, v19
	v_and_b32_e32 v19, 0xffff0000, v19
	v_lshlrev_b32_e32 v125, 16, v21
	v_and_b32_e32 v21, 0xffff0000, v21
	v_fmac_f32_e32 v125, v14, v33
	v_fmac_f32_e32 v19, v16, v15
	v_fmac_f32_e32 v21, v23, v17
	v_lshl_add_u64 v[14:15], s[24:25], 0, v[10:11]
	v_lshl_add_u64 v[10:11], s[16:17], 0, v[10:11]
	v_fmac_f32_e32 v123, v3, v31
	v_cvt_pk_bf16_f32 v3, v122, v18
	v_cvt_pk_bf16_f32 v28, v123, v19
	v_cvt_pk_bf16_f32 v29, v124, v20
	v_cvt_pk_bf16_f32 v30, v125, v21
	global_load_dwordx4 v[14:17], v[14:15], off
	v_pk_mul_f32 v[24:25], v[118:119], v[22:23] op_sel_hi:[1,0]
	global_load_dwordx4 v[18:21], v[10:11], off
	v_pk_mul_f32 v[10:11], v[120:121], v[22:23] op_sel_hi:[1,0]
	v_pk_mul_f32 v[26:27], v[116:117], v[22:23] op_sel_hi:[1,0]
	v_mul_f32_e32 v11, 0xbfb8aa3b, v11
	v_pk_mul_f32 v[22:23], v[114:115], v[22:23] op_sel_hi:[1,0]
	v_mul_f32_e32 v24, 0xbfb8aa3b, v24
	v_mul_f32_e32 v25, 0xbfb8aa3b, v25
	v_mul_f32_e32 v10, 0xbfb8aa3b, v10
	v_exp_f32_e32 v11, v11
	v_mul_f32_e32 v22, 0xbfb8aa3b, v22
	v_mul_f32_e32 v23, 0xbfb8aa3b, v23
	v_mul_f32_e32 v26, 0xbfb8aa3b, v26
	v_mul_f32_e32 v27, 0xbfb8aa3b, v27
	v_exp_f32_e32 v24, v24
	v_exp_f32_e32 v25, v25
	v_exp_f32_e32 v10, v10
	v_exp_f32_e32 v22, v22
	v_exp_f32_e32 v23, v23
	v_exp_f32_e32 v26, v26
	v_exp_f32_e32 v27, v27
	v_add_f32_e32 v11, 1.0, v11
	v_add_f32_e32 v24, 1.0, v24
	v_add_f32_e32 v25, 1.0, v25
	v_add_f32_e32 v10, 1.0, v10
	v_rcp_f32_e32 v11, v11
	v_add_f32_e32 v22, 1.0, v22
	v_add_f32_e32 v23, 1.0, v23
	v_add_f32_e32 v26, 1.0, v26
	v_add_f32_e32 v27, 1.0, v27
	v_rcp_f32_e32 v24, v24
	v_rcp_f32_e32 v25, v25
	v_rcp_f32_e32 v10, v10
	v_rcp_f32_e32 v22, v22
	v_rcp_f32_e32 v23, v23
	v_rcp_f32_e32 v26, v26
	v_rcp_f32_e32 v27, v27
	s_waitcnt vmcnt(1)
; __device__ __forceinline__ float sigm(float x) { return __builtin_amdgcn_rcpf(1.0f + __builtin_amdgcn_exp2f(-1.4426950408889634f * x)); }
; __device__ __forceinline__ u32x4 pack8(const f32x4& v0, const f32x4& v1) { u32x4 w; w.x = cvt_pk_bf16(v0[0], v0[1]); w.y = cvt_pk_bf16(v0[2], v0[3]); w.z = cvt_pk_bf16(v1[0], v1[1]); w.w = cvt_pk_bf16(v1[2], v1[3]); return w; }
; __device__ __forceinline__ void unpack8(const u32x4& w, f32x4& v0, f32x4& v1) { v0[0] = bf_lo(w.x); v0[1] = bf_hi(w.x); v0[2] = bf_lo(w.y); v0[3] = bf_hi(w.y); v1[0] = bf_lo(w.z); v1[1] = bf_hi(w.z); v1[2] = bf_lo(w.w); v1[3] = bf_hi(w.w); }
; __device__ __forceinline__ void store_rows_bf16(bf16_t* O, size_t ldc, int r0, int c0, int fr, int fq, u32x4 w0, u32x4 w1) {
;     const bool h = fr & 8; const u32x4 recv = xor8_16B(h ? w0 : w1);
;     const u32x4 d1 = h ? recv : w0, d2 = h ? w1 : recv;
;     const int lane = fr + 16 * fq, src = ((lane >> 3) + 8 * ((lane >> 2) & 1) + 16 * (lane & 3)) * 4;
;     const u32x4 e1 = bperm_16B(src, d1), e2 = bperm_16B(src, d2);
;     bf16_t* p = O + (size_t)(r0 + (lane >> 3)) * ldc + c0 + 8 * (lane & 7);
;     *(u32x4*)p = e1; *(u32x4*)(p + 8 * ldc) = e2;
;     __device__ __forceinline__ void operator()(const f32x4 (&acc)[2][2][4][2], const Unit& u, int wr, int wc, int fr, int fq) const {
;     ...
;             for (int m = 0; m < 4; ++m) { const int row = row0 + ai * HALF + m * 16; const float sq = sq_next; u32x4 wx[2];
;                 if (!(ai == 1 && m == 3)) sq_next = ssq[row0 + (m == 3 ? HALF : ai * HALF + (m + 1) * 16)];
;                 const float rstd = rsqrtf(sq * (1.0f / 1024.0f) + 1e-6f);
; #pragma unroll
;                 for (int bj = 0; bj < 2; ++bj) { const int ct = wc * 64 + bj * 32 + 8 * fq; f32x4 v0 = acc[ai][bj][m][0] * rstd, v1 = acc[ai][bj][m][1] * rstd;
;                     const size_t o = (size_t)row * 1024 + u.pn * BM + ct; f32x4 e0, e1, r0, r1; unpack8(*(const u32x4*)(e + o), e0, e1); unpack8(*(const u32x4*)(x2 + o), r0, r1);
; #pragma unroll
;                     for (int i = 0; i < 4; ++i) { v0[i] = r0[i] + sigm(v0[i]) * e0[i]; v1[i] = r1[i] + sigm(v1[i]) * e1[i]; }
;                     wx[bj] = pack8(v0, v1); }
;                 store_rows_bf16(x3, 1024, u.pm * BM + wr * 64 + ai * HALF + m * 16, u.pn * BM + wc * 64, fr, fq, wx[0], wx[1]); }
	v_lshlrev_b32_e32 v32, 16, v15
	v_and_b32_e32 v15, 0xffff0000, v15
	s_waitcnt vmcnt(0)
	v_lshlrev_b32_e32 v116, 16, v19
	v_and_b32_e32 v19, 0xffff0000, v19
	v_lshlrev_b32_e32 v31, 16, v14
	v_and_b32_e32 v14, 0xffff0000, v14
	v_lshlrev_b32_e32 v115, 16, v18
	v_and_b32_e32 v18, 0xffff0000, v18
	v_fmac_f32_e32 v19, v11, v15
	v_lshlrev_b32_e32 v33, 16, v16
	v_and_b32_e32 v16, 0xffff0000, v16
	v_lshlrev_b32_e32 v114, 16, v17
	v_and_b32_e32 v17, 0xffff0000, v17
	v_lshlrev_b32_e32 v117, 16, v20
	v_and_b32_e32 v20, 0xffff0000, v20
	v_lshlrev_b32_e32 v118, 16, v21
	v_and_b32_e32 v21, 0xffff0000, v21
	v_fmac_f32_e32 v115, v24, v31
	v_fmac_f32_e32 v18, v25, v14
	v_fmac_f32_e32 v116, v10, v32
	v_cvt_pk_bf16_f32 v10, v115, v18
	v_cvt_pk_bf16_f32 v11, v116, v19
	v_fmac_f32_e32 v117, v22, v33
	v_cndmask_b32_e64 v19, v3, v10, s[4:5]
	v_fmac_f32_e32 v20, v23, v16
	v_fmac_f32_e32 v118, v26, v114
	v_fmac_f32_e32 v21, v27, v17
	v_cvt_pk_bf16_f32 v14, v117, v20
	v_cvt_pk_bf16_f32 v15, v118, v21
	v_cndmask_b32_e64 v18, v28, v11, s[4:5]
	v_cndmask_b32_e64 v16, v30, v15, s[4:5]
	v_cndmask_b32_e64 v17, v29, v14, s[4:5]
	v_mov_b32_dpp v19, v19 row_ror:8 row_mask:0xf bank_mask:0xf
	v_mov_b32_dpp v16, v16 row_ror:8 row_mask:0xf bank_mask:0xf
	v_mov_b32_dpp v17, v17 row_ror:8 row_mask:0xf bank_mask:0xf
	v_mov_b32_dpp v18, v18 row_ror:8 row_mask:0xf bank_mask:0xf
	s_waitcnt lgkmcnt(0)
	v_cndmask_b32_e64 v10, v10, v19, s[4:5]
	s_waitcnt lgkmcnt(0)
	v_cndmask_b32_e64 v20, v16, v30, s[4:5]
	s_waitcnt lgkmcnt(0)
	v_cndmask_b32_e64 v21, v17, v29, s[4:5]
	s_waitcnt lgkmcnt(0)
	v_cndmask_b32_e64 v22, v18, v28, s[4:5]
	v_cndmask_b32_e64 v3, v19, v3, s[4:5]
	v_cndmask_b32_e64 v11, v11, v18, s[4:5]
	ds_bpermute_b32 v18, v196, v10
	v_or_b32_e32 v10, 32, v2
	v_cndmask_b32_e64 v23, v15, v16, s[4:5]
	v_cndmask_b32_e64 v24, v14, v17, s[4:5]
	ds_bpermute_b32 v14, v196, v3
	ds_bpermute_b32 v15, v196, v22
	ds_bpermute_b32 v16, v196, v21
	ds_bpermute_b32 v17, v196, v20
	ds_bpermute_b32 v19, v196, v11
	v_ashrrev_i32_e32 v11, 31, v10
	v_lshlrev_b64 v[10:11], 11, v[10:11]
	ds_bpermute_b32 v20, v196, v24
	ds_bpermute_b32 v21, v196, v23
	v_lshl_add_u64 v[10:11], s[22:23], 0, v[10:11]
	v_lshl_add_u64 v[10:11], v[10:11], 0, s[46:47]
	v_lshl_add_u64 v[10:11], v[10:11], 0, v[170:171]
	s_waitcnt lgkmcnt(3)
	global_store_dwordx4 v[10:11], v[14:17], off
	v_add_co_u32_e32 v10, vcc, s55, v10
	v_fmamk_f32 v3, v13, 0x3a800000, v202
	s_nop 0
	v_addc_co_u32_e32 v11, vcc, 0, v11, vcc
	s_waitcnt lgkmcnt(0)
	global_store_dwordx4 v[10:11], v[18:21], off
	v_mul_f32_e32 v13, 0x4b800000, v3
	v_cmp_gt_f32_e32 vcc, s75, v3
	v_lshl_add_u64 v[18:19], v[8:9], 0, s[48:49]
	v_or_b32_e32 v8, v18, v172
	v_mov_b32_e32 v9, v19
	v_lshlrev_b64 v[14:15], 1, v[8:9]
	v_lshl_add_u64 v[8:9], s[24:25], 0, v[14:15]
	v_lshl_add_u64 v[14:15], s[16:17], 0, v[14:15]
	global_load_dwordx4 v[8:11], v[8:9], off
	v_cndmask_b32_e32 v3, v3, v13, vcc
	global_load_dwordx4 v[14:17], v[14:15], off
	v_rsq_f32_e32 v3, v3
	global_load_dword v13, v[6:7], off offset:512
	v_or_b32_e32 v18, v18, v174
	v_mul_f32_e32 v20, 0x45800000, v3
	v_cndmask_b32_e32 v20, v3, v20, vcc
	v_pk_mul_f32 v[24:25], v[110:111], v[20:21] op_sel_hi:[1,0]
	v_pk_mul_f32 v[28:29], v[106:107], v[20:21] op_sel_hi:[1,0]
	v_mul_f32_e32 v3, 0xbfb8aa3b, v24
	v_exp_f32_e32 v3, v3
	v_pk_mul_f32 v[22:23], v[112:113], v[20:21] op_sel_hi:[1,0]
	v_pk_mul_f32 v[26:27], v[108:109], v[20:21] op_sel_hi:[1,0]
	v_mul_f32_e32 v21, 0xbfb8aa3b, v28
	v_mul_f32_e32 v24, 0xbfb8aa3b, v25
	v_exp_f32_e32 v21, v21
	v_exp_f32_e32 v24, v24
	v_mul_f32_e32 v25, 0xbfb8aa3b, v29
	v_add_f32_e32 v3, 1.0, v3
	v_exp_f32_e32 v25, v25
	v_rcp_f32_e32 v3, v3
	v_add_f32_e32 v21, 1.0, v21
	v_add_f32_e32 v24, 1.0, v24
	v_rcp_f32_e32 v21, v21
	v_rcp_f32_e32 v24, v24
	s_waitcnt vmcnt(2)
	v_lshlrev_b32_e32 v28, 16, v8
	v_and_b32_e32 v8, 0xffff0000, v8
	s_waitcnt vmcnt(1)
	v_lshlrev_b32_e32 v32, 16, v14
	v_fmac_f32_e32 v32, v3, v28
	v_add_f32_e32 v3, 1.0, v25
	v_lshlrev_b32_e32 v30, 16, v10
	v_and_b32_e32 v14, 0xffff0000, v14
	v_lshlrev_b32_e32 v106, 16, v16
	v_rcp_f32_e32 v3, v3
	v_fmac_f32_e32 v106, v21, v30
	v_fmac_f32_e32 v14, v24, v8
	v_mul_f32_e32 v8, 0xbfb8aa3b, v22
	v_mul_f32_e32 v21, 0xbfb8aa3b, v26
	v_exp_f32_e32 v8, v8
	v_exp_f32_e32 v21, v21
	v_and_b32_e32 v10, 0xffff0000, v10
	v_and_b32_e32 v16, 0xffff0000, v16
	v_fmac_f32_e32 v16, v3, v10
	v_mul_f32_e32 v10, 0xbfb8aa3b, v23
	v_exp_f32_e32 v10, v10
	v_add_f32_e32 v3, 1.0, v8
	v_add_f32_e32 v8, 1.0, v21
	v_mul_f32_e32 v21, 0xbfb8aa3b, v27
	v_exp_f32_e32 v21, v21
	v_add_f32_e32 v10, 1.0, v10
	v_rcp_f32_e32 v10, v10
	v_rcp_f32_e32 v3, v3
	v_add_f32_e32 v21, 1.0, v21
	v_rcp_f32_e32 v8, v8
	v_rcp_f32_e32 v21, v21
	v_lshlrev_b32_e32 v29, 16, v9
	v_and_b32_e32 v9, 0xffff0000, v9
	v_lshlrev_b32_e32 v33, 16, v15
	v_and_b32_e32 v15, 0xffff0000, v15
	v_fmac_f32_e32 v15, v10, v9
	v_lshlrev_b32_e32 v31, 16, v11
	v_and_b32_e32 v11, 0xffff0000, v11
	v_lshlrev_b32_e32 v107, 16, v17
	v_and_b32_e32 v17, 0xffff0000, v17
	v_fmac_f32_e32 v33, v3, v29
	v_cvt_pk_bf16_f32 v3, v32, v14
	v_cvt_pk_bf16_f32 v26, v33, v15
	v_lshlrev_b64 v[14:15], 1, v[18:19]
	v_fmac_f32_e32 v107, v8, v31
	v_fmac_f32_e32 v17, v21, v11
	v_lshl_add_u64 v[8:9], s[24:25], 0, v[14:15]
	v_lshl_add_u64 v[14:15], s[16:17], 0, v[14:15]
	v_cvt_pk_bf16_f32 v27, v106, v16
	v_cvt_pk_bf16_f32 v28, v107, v17
	global_load_dwordx4 v[8:11], v[8:9], off
	v_pk_mul_f32 v[18:19], v[104:105], v[20:21] op_sel_hi:[1,0]
	global_load_dwordx4 v[14:17], v[14:15], off
	v_pk_mul_f32 v[22:23], v[102:103], v[20:21] op_sel_hi:[1,0]
	v_pk_mul_f32 v[24:25], v[100:101], v[20:21] op_sel_hi:[1,0]
	v_pk_mul_f32 v[20:21], v[98:99], v[20:21] op_sel_hi:[1,0]
	v_mul_f32_e32 v23, 0xbfb8aa3b, v23
	v_mul_f32_e32 v21, 0xbfb8aa3b, v21
	v_exp_f32_e32 v23, v23
	v_exp_f32_e32 v21, v21
	v_mul_f32_e32 v22, 0xbfb8aa3b, v22
	v_mul_f32_e32 v20, 0xbfb8aa3b, v20
	v_add_f32_e32 v23, 1.0, v23
	v_add_f32_e32 v21, 1.0, v21
	v_rcp_f32_e32 v23, v23
	v_rcp_f32_e32 v21, v21
	v_mul_f32_e32 v18, 0xbfb8aa3b, v18
	v_mul_f32_e32 v24, 0xbfb8aa3b, v24
	v_exp_f32_e32 v22, v22
	v_exp_f32_e32 v20, v20
	v_exp_f32_e32 v18, v18
	v_exp_f32_e32 v24, v24
	v_add_f32_e32 v22, 1.0, v22
	v_add_f32_e32 v20, 1.0, v20
	v_add_f32_e32 v18, 1.0, v18
	v_add_f32_e32 v24, 1.0, v24
	v_rcp_f32_e32 v22, v22
	v_rcp_f32_e32 v20, v20
	v_rcp_f32_e32 v18, v18
	s_waitcnt vmcnt(1)
; __device__ __forceinline__ float sigm(float x) { return __builtin_amdgcn_rcpf(1.0f + __builtin_amdgcn_exp2f(-1.4426950408889634f * x)); }
; __device__ __forceinline__ u32x4 pack8(const f32x4& v0, const f32x4& v1) { u32x4 w; w.x = cvt_pk_bf16(v0[0], v0[1]); w.y = cvt_pk_bf16(v0[2], v0[3]); w.z = cvt_pk_bf16(v1[0], v1[1]); w.w = cvt_pk_bf16(v1[2], v1[3]); return w; }
; __device__ __forceinline__ void unpack8(const u32x4& w, f32x4& v0, f32x4& v1) { v0[0] = bf_lo(w.x); v0[1] = bf_hi(w.x); v0[2] = bf_lo(w.y); v0[3] = bf_hi(w.y); v1[0] = bf_lo(w.z); v1[1] = bf_hi(w.z); v1[2] = bf_lo(w.w); v1[3] = bf_hi(w.w); }
; __device__ __forceinline__ void store_rows_bf16(bf16_t* O, size_t ldc, int r0, int c0, int fr, int fq, u32x4 w0, u32x4 w1) {
;     const bool h = fr & 8; const u32x4 recv = xor8_16B(h ? w0 : w1);
;     const u32x4 d1 = h ? recv : w0, d2 = h ? w1 : recv;
;     const int lane = fr + 16 * fq, src = ((lane >> 3) + 8 * ((lane >> 2) & 1) + 16 * (lane & 3)) * 4;
;     const u32x4 e1 = bperm_16B(src, d1), e2 = bperm_16B(src, d2);
;     bf16_t* p = O + (size_t)(r0 + (lane >> 3)) * ldc + c0 + 8 * (lane & 7);
;     *(u32x4*)p = e1; *(u32x4*)(p + 8 * ldc) = e2;
;     __device__ __forceinline__ void operator()(const f32x4 (&acc)[2][2][4][2], const Unit& u, int wr, int wc, int fr, int fq) const {
;     ...
;             for (int m = 0; m < 4; ++m) { const int row = row0 + ai * HALF + m * 16; const float sq = sq_next; u32x4 wx[2];
;                 if (!(ai == 1 && m == 3)) sq_next = ssq[row0 + (m == 3 ? HALF : ai * HALF + (m + 1) * 16)];
;                 const float rstd = rsqrtf(sq * (1.0f / 1024.0f) + 1e-6f);
; #pragma unroll
;                 for (int bj = 0; bj < 2; ++bj) { const int ct = wc * 64 + bj * 32 + 8 * fq; f32x4 v0 = acc[ai][bj][m][0] * rstd, v1 = acc[ai][bj][m][1] * rstd;
;                     const size_t o = (size_t)row * 1024 + u.pn * BM + ct; f32x4 e0, e1, r0, r1; unpack8(*(const u32x4*)(e + o), e0, e1); unpack8(*(const u32x4*)(x2 + o), r0, r1);
; #pragma unroll
;                     for (int i = 0; i < 4; ++i) { v0[i] = r0[i] + sigm(v0[i]) * e0[i]; v1[i] = r1[i] + sigm(v1[i]) * e1[i]; }
;                     wx[bj] = pack8(v0, v1); }
;                 store_rows_bf16(x3, 1024, u.pm * BM + wr * 64 + ai * HALF + m * 16, u.pn * BM + wc * 64, fr, fq, wx[0], wx[1]); }
	v_lshlrev_b32_e32 v29, 16, v8
	v_and_b32_e32 v8, 0xffff0000, v8
	v_lshlrev_b32_e32 v31, 16, v10
	v_and_b32_e32 v10, 0xffff0000, v10
	s_waitcnt vmcnt(0)
	v_lshlrev_b32_e32 v33, 16, v14
	v_and_b32_e32 v14, 0xffff0000, v14
	v_lshlrev_b32_e32 v99, 16, v16
	v_and_b32_e32 v16, 0xffff0000, v16
	v_fmac_f32_e32 v14, v23, v8
	v_fmac_f32_e32 v16, v21, v10
	v_mul_f32_e32 v8, 0xbfb8aa3b, v19
	v_mul_f32_e32 v10, 0xbfb8aa3b, v25
	v_exp_f32_e32 v8, v8
	v_exp_f32_e32 v10, v10
	v_rcp_f32_e32 v19, v24
	v_lshlrev_b32_e32 v30, 16, v9
	v_add_f32_e32 v8, 1.0, v8
	v_add_f32_e32 v10, 1.0, v10
	v_rcp_f32_e32 v8, v8
	v_rcp_f32_e32 v10, v10
	v_and_b32_e32 v9, 0xffff0000, v9
	v_lshlrev_b32_e32 v32, 16, v11
	v_and_b32_e32 v11, 0xffff0000, v11
	v_lshlrev_b32_e32 v98, 16, v15
	v_and_b32_e32 v15, 0xffff0000, v15
	v_lshlrev_b32_e32 v100, 16, v17
	v_and_b32_e32 v17, 0xffff0000, v17
	v_fmac_f32_e32 v33, v22, v29
	v_fmac_f32_e32 v99, v20, v31
	v_fmac_f32_e32 v98, v18, v30
	v_fmac_f32_e32 v100, v19, v32
	v_fmac_f32_e32 v15, v8, v9
	v_fmac_f32_e32 v17, v10, v11
	v_cvt_pk_bf16_f32 v8, v33, v14
	v_cvt_pk_bf16_f32 v9, v98, v15
	v_cvt_pk_bf16_f32 v10, v99, v16
	v_cvt_pk_bf16_f32 v11, v100, v17
	s_nop 0
	v_cndmask_b32_e64 v14, v28, v11, s[4:5]
	v_cndmask_b32_e64 v15, v27, v10, s[4:5]
	v_cndmask_b32_e64 v16, v26, v9, s[4:5]
	v_cndmask_b32_e64 v17, v3, v8, s[4:5]
	v_mov_b32_dpp v14, v14 row_ror:8 row_mask:0xf bank_mask:0xf
	v_mov_b32_dpp v15, v15 row_ror:8 row_mask:0xf bank_mask:0xf
	v_mov_b32_dpp v16, v16 row_ror:8 row_mask:0xf bank_mask:0xf
	v_mov_b32_dpp v17, v17 row_ror:8 row_mask:0xf bank_mask:0xf
	s_waitcnt lgkmcnt(0)
	v_cndmask_b32_e64 v18, v14, v28, s[4:5]
	s_waitcnt lgkmcnt(0)
	v_cndmask_b32_e64 v19, v15, v27, s[4:5]
	s_waitcnt lgkmcnt(0)
	v_cndmask_b32_e64 v20, v16, v26, s[4:5]
	s_waitcnt lgkmcnt(0)
	v_cndmask_b32_e64 v3, v17, v3, s[4:5]
	v_cndmask_b32_e64 v21, v11, v14, s[4:5]
	ds_bpermute_b32 v11, v196, v18
	v_or_b32_e32 v18, 48, v2
	v_cndmask_b32_e64 v22, v10, v15, s[4:5]
	v_cndmask_b32_e64 v15, v9, v16, s[4:5]
	v_cndmask_b32_e64 v14, v8, v17, s[4:5]
	ds_bpermute_b32 v8, v196, v3
	ds_bpermute_b32 v9, v196, v20
	ds_bpermute_b32 v10, v196, v19
	v_ashrrev_i32_e32 v19, 31, v18
	v_lshlrev_b64 v[18:19], 11, v[18:19]
	ds_bpermute_b32 v14, v196, v14
	ds_bpermute_b32 v15, v196, v15
	ds_bpermute_b32 v16, v196, v22
	ds_bpermute_b32 v17, v196, v21
	v_lshl_add_u64 v[18:19], s[22:23], 0, v[18:19]
	v_lshl_add_u64 v[18:19], v[18:19], 0, s[46:47]
	v_lshl_add_u64 v[18:19], v[18:19], 0, v[170:171]
	s_waitcnt lgkmcnt(4)
	global_store_dwordx4 v[18:19], v[8:11], off
	v_fmamk_f32 v3, v13, 0x3a800000, v202
	v_mul_f32_e32 v13, 0x4b800000, v3
	v_add_co_u32_e32 v8, vcc, s55, v18
	s_nop 1
	v_addc_co_u32_e32 v9, vcc, 0, v19, vcc
	v_lshl_add_u64 v[18:19], v[4:5], 0, s[36:37]
	s_waitcnt lgkmcnt(0)
	global_store_dwordx4 v[8:9], v[14:17], off
	v_or_b32_e32 v8, v18, v172
	v_mov_b32_e32 v9, v19
	v_lshlrev_b64 v[14:15], 1, v[8:9]
	v_lshl_add_u64 v[8:9], s[24:25], 0, v[14:15]
	v_lshl_add_u64 v[14:15], s[16:17], 0, v[14:15]
	global_load_dwordx4 v[8:11], v[8:9], off
	v_cmp_gt_f32_e32 vcc, s75, v3
	global_load_dwordx4 v[14:17], v[14:15], off
	v_or_b32_e32 v18, v18, v174
	v_cndmask_b32_e32 v3, v3, v13, vcc
	v_rsq_f32_e32 v3, v3
	global_load_dword v13, v[6:7], off offset:576
	v_mul_f32_e32 v20, 0x45800000, v3
	v_cndmask_b32_e32 v20, v3, v20, vcc
	v_pk_mul_f32 v[24:25], v[94:95], v[20:21] op_sel_hi:[1,0]
	v_pk_mul_f32 v[28:29], v[90:91], v[20:21] op_sel_hi:[1,0]
	v_mul_f32_e32 v3, 0xbfb8aa3b, v24
	v_exp_f32_e32 v3, v3
	v_pk_mul_f32 v[22:23], v[96:97], v[20:21] op_sel_hi:[1,0]
	v_pk_mul_f32 v[26:27], v[92:93], v[20:21] op_sel_hi:[1,0]
	v_mul_f32_e32 v21, 0xbfb8aa3b, v28
	v_mul_f32_e32 v24, 0xbfb8aa3b, v25
	v_exp_f32_e32 v21, v21
	v_exp_f32_e32 v24, v24
	v_add_f32_e32 v3, 1.0, v3
	v_mul_f32_e32 v29, 0xbfb8aa3b, v29
	v_rcp_f32_e32 v3, v3
	v_exp_f32_e32 v29, v29
	v_add_f32_e32 v21, 1.0, v21
	v_add_f32_e32 v24, 1.0, v24
	v_rcp_f32_e32 v21, v21
	v_rcp_f32_e32 v24, v24
	s_waitcnt vmcnt(2)
	v_lshlrev_b32_e32 v25, 16, v8
	v_and_b32_e32 v8, 0xffff0000, v8
	s_waitcnt vmcnt(1)
	v_lshlrev_b32_e32 v32, 16, v14
	v_fmac_f32_e32 v32, v3, v25
	v_add_f32_e32 v3, 1.0, v29
	v_lshlrev_b32_e32 v30, 16, v10
	v_and_b32_e32 v14, 0xffff0000, v14
	v_lshlrev_b32_e32 v90, 16, v16
	v_rcp_f32_e32 v3, v3
	v_fmac_f32_e32 v90, v21, v30
	v_fmac_f32_e32 v14, v24, v8
	v_mul_f32_e32 v8, 0xbfb8aa3b, v22
	v_mul_f32_e32 v21, 0xbfb8aa3b, v26
	v_exp_f32_e32 v8, v8
	v_exp_f32_e32 v21, v21
	v_and_b32_e32 v10, 0xffff0000, v10
	v_and_b32_e32 v16, 0xffff0000, v16
	v_fmac_f32_e32 v16, v3, v10
	v_mul_f32_e32 v10, 0xbfb8aa3b, v23
	v_exp_f32_e32 v10, v10
	v_add_f32_e32 v3, 1.0, v8
	v_add_f32_e32 v8, 1.0, v21
	v_mul_f32_e32 v21, 0xbfb8aa3b, v27
	v_exp_f32_e32 v21, v21
	v_add_f32_e32 v10, 1.0, v10
	v_rcp_f32_e32 v10, v10
	v_rcp_f32_e32 v3, v3
	v_add_f32_e32 v21, 1.0, v21
	v_rcp_f32_e32 v8, v8
	v_rcp_f32_e32 v21, v21
	v_lshlrev_b32_e32 v28, 16, v9
	v_and_b32_e32 v9, 0xffff0000, v9
	v_lshlrev_b32_e32 v33, 16, v15
	v_and_b32_e32 v15, 0xffff0000, v15
	v_fmac_f32_e32 v15, v10, v9
	v_lshlrev_b32_e32 v31, 16, v11
	v_and_b32_e32 v11, 0xffff0000, v11
	v_lshlrev_b32_e32 v91, 16, v17
	v_and_b32_e32 v17, 0xffff0000, v17
	v_fmac_f32_e32 v33, v3, v28
	v_cvt_pk_bf16_f32 v3, v32, v14
	v_cvt_pk_bf16_f32 v26, v33, v15
	v_lshlrev_b64 v[14:15], 1, v[18:19]
	v_fmac_f32_e32 v91, v8, v31
	v_fmac_f32_e32 v17, v21, v11
	v_lshl_add_u64 v[8:9], s[24:25], 0, v[14:15]
	v_lshl_add_u64 v[14:15], s[16:17], 0, v[14:15]
	v_cvt_pk_bf16_f32 v27, v90, v16
	v_cvt_pk_bf16_f32 v28, v91, v17
	global_load_dwordx4 v[8:11], v[8:9], off
	v_pk_mul_f32 v[22:23], v[86:87], v[20:21] op_sel_hi:[1,0]
	global_load_dwordx4 v[14:17], v[14:15], off
	v_mul_f32_e32 v23, 0xbfb8aa3b, v23
	v_exp_f32_e32 v23, v23
	v_pk_mul_f32 v[18:19], v[88:89], v[20:21] op_sel_hi:[1,0]
	v_pk_mul_f32 v[24:25], v[84:85], v[20:21] op_sel_hi:[1,0]
	v_pk_mul_f32 v[20:21], v[82:83], v[20:21] op_sel_hi:[1,0]
	v_add_f32_e32 v23, 1.0, v23
	v_mul_f32_e32 v21, 0xbfb8aa3b, v21
	v_exp_f32_e32 v21, v21
	v_rcp_f32_e32 v23, v23
	v_mul_f32_e32 v22, 0xbfb8aa3b, v22
	v_mul_f32_e32 v20, 0xbfb8aa3b, v20
	v_add_f32_e32 v21, 1.0, v21
	v_rcp_f32_e32 v21, v21
	v_exp_f32_e32 v22, v22
	v_exp_f32_e32 v20, v20
	v_add_f32_e32 v22, 1.0, v22
	v_add_f32_e32 v20, 1.0, v20
	v_rcp_f32_e32 v22, v22
	v_rcp_f32_e32 v20, v20
	s_waitcnt vmcnt(1)
; __device__ __forceinline__ float sigm(float x) { return __builtin_amdgcn_rcpf(1.0f + __builtin_amdgcn_exp2f(-1.4426950408889634f * x)); }
; __device__ __forceinline__ u32x4 pack8(const f32x4& v0, const f32x4& v1) { u32x4 w; w.x = cvt_pk_bf16(v0[0], v0[1]); w.y = cvt_pk_bf16(v0[2], v0[3]); w.z = cvt_pk_bf16(v1[0], v1[1]); w.w = cvt_pk_bf16(v1[2], v1[3]); return w; }
; __device__ __forceinline__ void unpack8(const u32x4& w, f32x4& v0, f32x4& v1) { v0[0] = bf_lo(w.x); v0[1] = bf_hi(w.x); v0[2] = bf_lo(w.y); v0[3] = bf_hi(w.y); v1[0] = bf_lo(w.z); v1[1] = bf_hi(w.z); v1[2] = bf_lo(w.w); v1[3] = bf_hi(w.w); }
; __device__ __forceinline__ void store_rows_bf16(bf16_t* O, size_t ldc, int r0, int c0, int fr, int fq, u32x4 w0, u32x4 w1) {
;     const bool h = fr & 8; const u32x4 recv = xor8_16B(h ? w0 : w1);
;     const u32x4 d1 = h ? recv : w0, d2 = h ? w1 : recv;
;     const int lane = fr + 16 * fq, src = ((lane >> 3) + 8 * ((lane >> 2) & 1) + 16 * (lane & 3)) * 4;
;     const u32x4 e1 = bperm_16B(src, d1), e2 = bperm_16B(src, d2);
;     bf16_t* p = O + (size_t)(r0 + (lane >> 3)) * ldc + c0 + 8 * (lane & 7);
;     *(u32x4*)p = e1; *(u32x4*)(p + 8 * ldc) = e2;
;     __device__ __forceinline__ void operator()(const f32x4 (&acc)[2][2][4][2], const Unit& u, int wr, int wc, int fr, int fq) const {
;     ...
;             for (int m = 0; m < 4; ++m) { const int row = row0 + ai * HALF + m * 16; const float sq = sq_next; u32x4 wx[2];
;                 if (!(ai == 1 && m == 3)) sq_next = ssq[row0 + (m == 3 ? HALF : ai * HALF + (m + 1) * 16)];
;                 const float rstd = rsqrtf(sq * (1.0f / 1024.0f) + 1e-6f);
; #pragma unroll
;                 for (int bj = 0; bj < 2; ++bj) { const int ct = wc * 64 + bj * 32 + 8 * fq; f32x4 v0 = acc[ai][bj][m][0] * rstd, v1 = acc[ai][bj][m][1] * rstd;
;                     const size_t o = (size_t)row * 1024 + u.pn * BM + ct; f32x4 e0, e1, r0, r1; unpack8(*(const u32x4*)(e + o), e0, e1); unpack8(*(const u32x4*)(x2 + o), r0, r1);
; #pragma unroll
;                     for (int i = 0; i < 4; ++i) { v0[i] = r0[i] + sigm(v0[i]) * e0[i]; v1[i] = r1[i] + sigm(v1[i]) * e1[i]; }
;                     wx[bj] = pack8(v0, v1); }
;                 store_rows_bf16(x3, 1024, u.pm * BM + wr * 64 + ai * HALF + m * 16, u.pn * BM + wc * 64, fr, fq, wx[0], wx[1]); }
	v_lshlrev_b32_e32 v29, 16, v8
	v_and_b32_e32 v8, 0xffff0000, v8
	s_waitcnt vmcnt(0)
	v_lshlrev_b32_e32 v33, 16, v14
	v_and_b32_e32 v14, 0xffff0000, v14
	v_fmac_f32_e32 v14, v23, v8
	v_mul_f32_e32 v8, 0xbfb8aa3b, v18
	v_mul_f32_e32 v18, 0xbfb8aa3b, v24
	v_exp_f32_e32 v18, v18
	v_lshlrev_b32_e32 v31, 16, v10
	v_and_b32_e32 v10, 0xffff0000, v10
	v_lshlrev_b32_e32 v83, 16, v16
	v_and_b32_e32 v16, 0xffff0000, v16
	v_fmac_f32_e32 v16, v21, v10
	v_add_f32_e32 v10, 1.0, v18
	v_mul_f32_e32 v18, 0xbfb8aa3b, v19
	v_mul_f32_e32 v19, 0xbfb8aa3b, v25
	v_exp_f32_e32 v18, v18
	v_exp_f32_e32 v19, v19
	v_exp_f32_e32 v8, v8
	v_rcp_f32_e32 v10, v10
	v_add_f32_e32 v18, 1.0, v18
	v_add_f32_e32 v19, 1.0, v19
	v_add_f32_e32 v8, 1.0, v8
	v_rcp_f32_e32 v18, v18
	v_rcp_f32_e32 v19, v19
	v_rcp_f32_e32 v8, v8
	v_lshlrev_b32_e32 v30, 16, v9
	v_and_b32_e32 v9, 0xffff0000, v9
	v_lshlrev_b32_e32 v32, 16, v11
	v_and_b32_e32 v11, 0xffff0000, v11
	v_lshlrev_b32_e32 v82, 16, v15
	v_and_b32_e32 v15, 0xffff0000, v15
	v_lshlrev_b32_e32 v84, 16, v17
	v_and_b32_e32 v17, 0xffff0000, v17
	v_fmac_f32_e32 v15, v18, v9
	v_fmac_f32_e32 v17, v19, v11
	v_fmac_f32_e32 v33, v22, v29
	v_fmac_f32_e32 v83, v20, v31
	v_fmac_f32_e32 v82, v8, v30
	v_fmac_f32_e32 v84, v10, v32
	v_cvt_pk_bf16_f32 v8, v33, v14
	v_cvt_pk_bf16_f32 v9, v82, v15
	v_cvt_pk_bf16_f32 v10, v83, v16
	v_cvt_pk_bf16_f32 v11, v84, v17
	v_add_u32_e32 v18, 0x80, v2
	v_cndmask_b32_e64 v14, v28, v11, s[4:5]
	v_cndmask_b32_e64 v15, v27, v10, s[4:5]
	v_cndmask_b32_e64 v16, v26, v9, s[4:5]
	v_cndmask_b32_e64 v17, v3, v8, s[4:5]
	v_mov_b32_dpp v14, v14 row_ror:8 row_mask:0xf bank_mask:0xf
	v_mov_b32_dpp v15, v15 row_ror:8 row_mask:0xf bank_mask:0xf
	v_mov_b32_dpp v16, v16 row_ror:8 row_mask:0xf bank_mask:0xf
	v_mov_b32_dpp v17, v17 row_ror:8 row_mask:0xf bank_mask:0xf
	s_waitcnt lgkmcnt(0)
	v_cndmask_b32_e64 v19, v14, v28, s[4:5]
	s_waitcnt lgkmcnt(0)
	v_cndmask_b32_e64 v20, v15, v27, s[4:5]
	s_waitcnt lgkmcnt(0)
	v_cndmask_b32_e64 v21, v16, v26, s[4:5]
	s_waitcnt lgkmcnt(0)
	v_cndmask_b32_e64 v3, v17, v3, s[4:5]
	v_cndmask_b32_e64 v22, v11, v14, s[4:5]
	v_cndmask_b32_e64 v23, v10, v15, s[4:5]
	v_cndmask_b32_e64 v15, v9, v16, s[4:5]
	v_cndmask_b32_e64 v14, v8, v17, s[4:5]
	ds_bpermute_b32 v8, v196, v3
	ds_bpermute_b32 v9, v196, v21
	ds_bpermute_b32 v10, v196, v20
	ds_bpermute_b32 v11, v196, v19
	v_ashrrev_i32_e32 v19, 31, v18
	v_lshlrev_b64 v[18:19], 11, v[18:19]
	ds_bpermute_b32 v14, v196, v14
	ds_bpermute_b32 v15, v196, v15
	ds_bpermute_b32 v16, v196, v23
	ds_bpermute_b32 v17, v196, v22
	v_lshl_add_u64 v[18:19], s[22:23], 0, v[18:19]
	v_lshl_add_u64 v[18:19], v[18:19], 0, s[46:47]
	v_lshl_add_u64 v[18:19], v[18:19], 0, v[170:171]
	s_waitcnt lgkmcnt(4)
	global_store_dwordx4 v[18:19], v[8:11], off
	v_fmamk_f32 v3, v13, 0x3a800000, v202
	v_mul_f32_e32 v13, 0x4b800000, v3
	v_add_co_u32_e32 v8, vcc, s55, v18
	s_nop 1
	v_addc_co_u32_e32 v9, vcc, 0, v19, vcc
	v_lshl_add_u64 v[18:19], v[4:5], 0, s[38:39]
	s_waitcnt lgkmcnt(0)
	global_store_dwordx4 v[8:9], v[14:17], off
	v_or_b32_e32 v8, v18, v172
	v_mov_b32_e32 v9, v19
	v_lshlrev_b64 v[14:15], 1, v[8:9]
	v_lshl_add_u64 v[8:9], s[24:25], 0, v[14:15]
	v_lshl_add_u64 v[14:15], s[16:17], 0, v[14:15]
	global_load_dwordx4 v[8:11], v[8:9], off
	v_cmp_gt_f32_e32 vcc, s75, v3
	global_load_dwordx4 v[14:17], v[14:15], off
	v_or_b32_e32 v18, v18, v174
	v_cndmask_b32_e32 v3, v3, v13, vcc
	v_rsq_f32_e32 v3, v3
	global_load_dword v13, v[6:7], off offset:640
	v_mul_f32_e32 v20, 0x45800000, v3
	v_cndmask_b32_e32 v20, v3, v20, vcc
	v_pk_mul_f32 v[24:25], v[78:79], v[20:21] op_sel_hi:[1,0]
	v_pk_mul_f32 v[28:29], v[74:75], v[20:21] op_sel_hi:[1,0]
	v_mul_f32_e32 v3, 0xbfb8aa3b, v24
	v_exp_f32_e32 v3, v3
	v_mul_f32_e32 v25, 0xbfb8aa3b, v25
	v_exp_f32_e32 v25, v25
	v_mul_f32_e32 v29, 0xbfb8aa3b, v29
	v_add_f32_e32 v3, 1.0, v3
	v_rcp_f32_e32 v3, v3
	v_exp_f32_e32 v29, v29
	v_add_f32_e32 v25, 1.0, v25
	v_rcp_f32_e32 v25, v25
	v_pk_mul_f32 v[22:23], v[80:81], v[20:21] op_sel_hi:[1,0]
	v_pk_mul_f32 v[26:27], v[76:77], v[20:21] op_sel_hi:[1,0]
	v_mul_f32_e32 v28, 0xbfb8aa3b, v28
	v_exp_f32_e32 v28, v28
	s_waitcnt vmcnt(2)
	v_lshlrev_b32_e32 v21, 16, v8
	v_and_b32_e32 v8, 0xffff0000, v8
	s_waitcnt vmcnt(1)
	v_lshlrev_b32_e32 v32, 16, v14
	v_fmac_f32_e32 v32, v3, v21
	v_add_f32_e32 v3, 1.0, v29
	v_and_b32_e32 v14, 0xffff0000, v14
	v_rcp_f32_e32 v3, v3
	v_fmac_f32_e32 v14, v25, v8
	v_mul_f32_e32 v8, 0xbfb8aa3b, v22
	v_mul_f32_e32 v21, 0xbfb8aa3b, v26
	v_exp_f32_e32 v8, v8
	v_exp_f32_e32 v21, v21
	v_lshlrev_b32_e32 v30, 16, v10
	v_and_b32_e32 v10, 0xffff0000, v10
	v_lshlrev_b32_e32 v74, 16, v16
	v_and_b32_e32 v16, 0xffff0000, v16
	v_fmac_f32_e32 v16, v3, v10
	v_mul_f32_e32 v10, 0xbfb8aa3b, v23
	v_exp_f32_e32 v10, v10
	v_add_f32_e32 v3, 1.0, v8
	v_add_f32_e32 v8, 1.0, v21
	v_mul_f32_e32 v21, 0xbfb8aa3b, v27
	v_exp_f32_e32 v21, v21
	v_add_f32_e32 v10, 1.0, v10
	v_rcp_f32_e32 v10, v10
	v_rcp_f32_e32 v3, v3
	v_add_f32_e32 v21, 1.0, v21
	v_add_f32_e32 v28, 1.0, v28
	v_rcp_f32_e32 v8, v8
	v_rcp_f32_e32 v21, v21
	v_lshlrev_b32_e32 v24, 16, v9
	v_and_b32_e32 v9, 0xffff0000, v9
	v_lshlrev_b32_e32 v33, 16, v15
	v_and_b32_e32 v15, 0xffff0000, v15
	v_rcp_f32_e32 v28, v28
	v_fmac_f32_e32 v15, v10, v9
	v_lshlrev_b32_e32 v31, 16, v11
	v_and_b32_e32 v11, 0xffff0000, v11
	v_lshlrev_b32_e32 v75, 16, v17
	v_and_b32_e32 v17, 0xffff0000, v17
	v_fmac_f32_e32 v33, v3, v24
	v_cvt_pk_bf16_f32 v3, v32, v14
	v_cvt_pk_bf16_f32 v26, v33, v15
	v_lshlrev_b64 v[14:15], 1, v[18:19]
	v_fmac_f32_e32 v75, v8, v31
	v_fmac_f32_e32 v17, v21, v11
	v_lshl_add_u64 v[8:9], s[24:25], 0, v[14:15]
	v_lshl_add_u64 v[14:15], s[16:17], 0, v[14:15]
	v_fmac_f32_e32 v74, v28, v30
	v_cvt_pk_bf16_f32 v27, v74, v16
	v_cvt_pk_bf16_f32 v28, v75, v17
	global_load_dwordx4 v[8:11], v[8:9], off
	v_pk_mul_f32 v[22:23], v[70:71], v[20:21] op_sel_hi:[1,0]
	global_load_dwordx4 v[14:17], v[14:15], off
	v_mul_f32_e32 v23, 0xbfb8aa3b, v23
	v_exp_f32_e32 v23, v23
	v_pk_mul_f32 v[18:19], v[72:73], v[20:21] op_sel_hi:[1,0]
	v_pk_mul_f32 v[24:25], v[68:69], v[20:21] op_sel_hi:[1,0]
	v_pk_mul_f32 v[20:21], v[66:67], v[20:21] op_sel_hi:[1,0]
	v_add_f32_e32 v23, 1.0, v23
	v_mul_f32_e32 v20, 0xbfb8aa3b, v20
	v_mul_f32_e32 v21, 0xbfb8aa3b, v21
	v_exp_f32_e32 v20, v20
	v_rcp_f32_e32 v23, v23
	v_exp_f32_e32 v21, v21
	v_mul_f32_e32 v18, 0xbfb8aa3b, v18
	v_add_f32_e32 v20, 1.0, v20
	v_rcp_f32_e32 v20, v20
	v_exp_f32_e32 v18, v18
	v_mul_f32_e32 v22, 0xbfb8aa3b, v22
	v_exp_f32_e32 v22, v22
	s_waitcnt vmcnt(1)
; __device__ __forceinline__ float sigm(float x) { return __builtin_amdgcn_rcpf(1.0f + __builtin_amdgcn_exp2f(-1.4426950408889634f * x)); }
; __device__ __forceinline__ u32x4 pack8(const f32x4& v0, const f32x4& v1) { u32x4 w; w.x = cvt_pk_bf16(v0[0], v0[1]); w.y = cvt_pk_bf16(v0[2], v0[3]); w.z = cvt_pk_bf16(v1[0], v1[1]); w.w = cvt_pk_bf16(v1[2], v1[3]); return w; }
; __device__ __forceinline__ void unpack8(const u32x4& w, f32x4& v0, f32x4& v1) { v0[0] = bf_lo(w.x); v0[1] = bf_hi(w.x); v0[2] = bf_lo(w.y); v0[3] = bf_hi(w.y); v1[0] = bf_lo(w.z); v1[1] = bf_hi(w.z); v1[2] = bf_lo(w.w); v1[3] = bf_hi(w.w); }
; __device__ __forceinline__ void store_rows_bf16(bf16_t* O, size_t ldc, int r0, int c0, int fr, int fq, u32x4 w0, u32x4 w1) {
;     const bool h = fr & 8; const u32x4 recv = xor8_16B(h ? w0 : w1);
;     const u32x4 d1 = h ? recv : w0, d2 = h ? w1 : recv;
;     const int lane = fr + 16 * fq, src = ((lane >> 3) + 8 * ((lane >> 2) & 1) + 16 * (lane & 3)) * 4;
;     const u32x4 e1 = bperm_16B(src, d1), e2 = bperm_16B(src, d2);
;     bf16_t* p = O + (size_t)(r0 + (lane >> 3)) * ldc + c0 + 8 * (lane & 7);
;     *(u32x4*)p = e1; *(u32x4*)(p + 8 * ldc) = e2;
;     __device__ __forceinline__ void operator()(const f32x4 (&acc)[2][2][4][2], const Unit& u, int wr, int wc, int fr, int fq) const {
;     ...
;             for (int m = 0; m < 4; ++m) { const int row = row0 + ai * HALF + m * 16; const float sq = sq_next; u32x4 wx[2];
;                 if (!(ai == 1 && m == 3)) sq_next = ssq[row0 + (m == 3 ? HALF : ai * HALF + (m + 1) * 16)];
;                 const float rstd = rsqrtf(sq * (1.0f / 1024.0f) + 1e-6f);
; #pragma unroll
;                 for (int bj = 0; bj < 2; ++bj) { const int ct = wc * 64 + bj * 32 + 8 * fq; f32x4 v0 = acc[ai][bj][m][0] * rstd, v1 = acc[ai][bj][m][1] * rstd;
;                     const size_t o = (size_t)row * 1024 + u.pn * BM + ct; f32x4 e0, e1, r0, r1; unpack8(*(const u32x4*)(e + o), e0, e1); unpack8(*(const u32x4*)(x2 + o), r0, r1);
; #pragma unroll
;                     for (int i = 0; i < 4; ++i) { v0[i] = r0[i] + sigm(v0[i]) * e0[i]; v1[i] = r1[i] + sigm(v1[i]) * e1[i]; }
;                     wx[bj] = pack8(v0, v1); }
;                 store_rows_bf16(x3, 1024, u.pm * BM + wr * 64 + ai * HALF + m * 16, u.pn * BM + wc * 64, fr, fq, wx[0], wx[1]); }
	v_lshlrev_b32_e32 v29, 16, v8
	v_and_b32_e32 v8, 0xffff0000, v8
	s_waitcnt vmcnt(0)
	v_lshlrev_b32_e32 v33, 16, v14
	v_and_b32_e32 v14, 0xffff0000, v14
	v_fmac_f32_e32 v14, v23, v8
	v_add_f32_e32 v8, 1.0, v21
	v_rcp_f32_e32 v8, v8
	v_lshlrev_b32_e32 v31, 16, v10
	v_and_b32_e32 v10, 0xffff0000, v10
	v_lshlrev_b32_e32 v67, 16, v16
	v_and_b32_e32 v16, 0xffff0000, v16
	v_fmac_f32_e32 v67, v20, v31
	v_mul_f32_e32 v20, 0xbfb8aa3b, v24
	v_fmac_f32_e32 v16, v8, v10
	v_add_f32_e32 v8, 1.0, v18
	v_mul_f32_e32 v18, 0xbfb8aa3b, v19
	v_mul_f32_e32 v19, 0xbfb8aa3b, v25
	v_exp_f32_e32 v20, v20
	v_exp_f32_e32 v18, v18
	v_exp_f32_e32 v19, v19
	v_add_f32_e32 v22, 1.0, v22
	v_add_f32_e32 v10, 1.0, v20
	v_add_f32_e32 v18, 1.0, v18
	v_add_f32_e32 v19, 1.0, v19
	v_rcp_f32_e32 v22, v22
	v_rcp_f32_e32 v8, v8
	v_rcp_f32_e32 v10, v10
	v_rcp_f32_e32 v18, v18
	v_rcp_f32_e32 v19, v19
	v_lshlrev_b32_e32 v30, 16, v9
	v_and_b32_e32 v9, 0xffff0000, v9
	v_lshlrev_b32_e32 v32, 16, v11
	v_and_b32_e32 v11, 0xffff0000, v11
	v_lshlrev_b32_e32 v66, 16, v15
	v_and_b32_e32 v15, 0xffff0000, v15
	v_lshlrev_b32_e32 v68, 16, v17
	v_and_b32_e32 v17, 0xffff0000, v17
	v_fmac_f32_e32 v33, v22, v29
	v_fmac_f32_e32 v66, v8, v30
	v_fmac_f32_e32 v68, v10, v32
	v_fmac_f32_e32 v15, v18, v9
	v_fmac_f32_e32 v17, v19, v11
	v_cvt_pk_bf16_f32 v8, v33, v14
	v_cvt_pk_bf16_f32 v9, v66, v15
	v_cvt_pk_bf16_f32 v10, v67, v16
	v_cvt_pk_bf16_f32 v11, v68, v17
	s_nop 0
	v_cndmask_b32_e64 v14, v28, v11, s[4:5]
	v_cndmask_b32_e64 v15, v27, v10, s[4:5]
	v_cndmask_b32_e64 v16, v26, v9, s[4:5]
	v_cndmask_b32_e64 v17, v3, v8, s[4:5]
	v_mov_b32_dpp v14, v14 row_ror:8 row_mask:0xf bank_mask:0xf
	v_mov_b32_dpp v15, v15 row_ror:8 row_mask:0xf bank_mask:0xf
	v_mov_b32_dpp v16, v16 row_ror:8 row_mask:0xf bank_mask:0xf
	v_mov_b32_dpp v17, v17 row_ror:8 row_mask:0xf bank_mask:0xf
	s_waitcnt lgkmcnt(0)
	v_cndmask_b32_e64 v18, v14, v28, s[4:5]
	s_waitcnt lgkmcnt(0)
	v_cndmask_b32_e64 v19, v15, v27, s[4:5]
	s_waitcnt lgkmcnt(0)
	v_cndmask_b32_e64 v20, v16, v26, s[4:5]
	s_waitcnt lgkmcnt(0)
	v_cndmask_b32_e64 v3, v17, v3, s[4:5]
	v_cndmask_b32_e64 v21, v11, v14, s[4:5]
	ds_bpermute_b32 v11, v196, v18
	v_add_u32_e32 v18, 0x90, v2
	v_cndmask_b32_e64 v22, v10, v15, s[4:5]
	v_cndmask_b32_e64 v15, v9, v16, s[4:5]
	v_cndmask_b32_e64 v14, v8, v17, s[4:5]
	ds_bpermute_b32 v8, v196, v3
	ds_bpermute_b32 v9, v196, v20
	ds_bpermute_b32 v10, v196, v19
	v_ashrrev_i32_e32 v19, 31, v18
	v_lshlrev_b64 v[18:19], 11, v[18:19]
	ds_bpermute_b32 v14, v196, v14
	ds_bpermute_b32 v15, v196, v15
	ds_bpermute_b32 v16, v196, v22
	ds_bpermute_b32 v17, v196, v21
	v_lshl_add_u64 v[18:19], s[22:23], 0, v[18:19]
	v_lshl_add_u64 v[18:19], v[18:19], 0, s[46:47]
	v_lshl_add_u64 v[18:19], v[18:19], 0, v[170:171]
	s_waitcnt lgkmcnt(4)
	global_store_dwordx4 v[18:19], v[8:11], off
	v_fmamk_f32 v3, v13, 0x3a800000, v202
	v_mul_f32_e32 v13, 0x4b800000, v3
	v_add_co_u32_e32 v8, vcc, s55, v18
	s_nop 1
	v_addc_co_u32_e32 v9, vcc, 0, v19, vcc
	v_lshl_add_u64 v[18:19], v[4:5], 0, s[40:41]
	s_waitcnt lgkmcnt(0)
	global_store_dwordx4 v[8:9], v[14:17], off
	v_or_b32_e32 v8, v18, v172
	v_mov_b32_e32 v9, v19
	v_lshlrev_b64 v[14:15], 1, v[8:9]
	v_lshl_add_u64 v[8:9], s[24:25], 0, v[14:15]
	v_lshl_add_u64 v[14:15], s[16:17], 0, v[14:15]
	global_load_dwordx4 v[8:11], v[8:9], off
	v_cmp_gt_f32_e32 vcc, s75, v3
	global_load_dwordx4 v[14:17], v[14:15], off
	v_or_b32_e32 v18, v18, v174
	v_cndmask_b32_e32 v3, v3, v13, vcc
	v_rsq_f32_e32 v3, v3
	global_load_dword v13, v[6:7], off offset:704
	v_mul_f32_e32 v6, 0x45800000, v3
	v_cndmask_b32_e32 v20, v3, v6, vcc
	v_pk_mul_f32 v[22:23], v[62:63], v[20:21] op_sel_hi:[1,0]
	v_pk_mul_f32 v[26:27], v[58:59], v[20:21] op_sel_hi:[1,0]
	v_mul_f32_e32 v22, 0xbfb8aa3b, v22
	v_mul_f32_e32 v23, 0xbfb8aa3b, v23
	v_exp_f32_e32 v22, v22
	v_exp_f32_e32 v23, v23
	v_mul_f32_e32 v27, 0xbfb8aa3b, v27
	v_exp_f32_e32 v27, v27
	v_add_f32_e32 v22, 1.0, v22
	v_add_f32_e32 v23, 1.0, v23
	v_rcp_f32_e32 v22, v22
	v_rcp_f32_e32 v23, v23
	v_pk_mul_f32 v[6:7], v[64:65], v[20:21] op_sel_hi:[1,0]
	v_pk_mul_f32 v[24:25], v[60:61], v[20:21] op_sel_hi:[1,0]
	v_mul_f32_e32 v6, 0xbfb8aa3b, v6
	v_exp_f32_e32 v6, v6
	v_mul_f32_e32 v7, 0xbfb8aa3b, v7
	v_mul_f32_e32 v26, 0xbfb8aa3b, v26
	v_exp_f32_e32 v7, v7
	v_exp_f32_e32 v26, v26
	v_add_f32_e32 v7, 1.0, v7
	v_add_f32_e32 v26, 1.0, v26
	v_rcp_f32_e32 v7, v7
	v_rcp_f32_e32 v26, v26
	s_waitcnt vmcnt(2)
	v_lshlrev_b32_e32 v3, 16, v8
	v_and_b32_e32 v8, 0xffff0000, v8
	s_waitcnt vmcnt(1)
	v_lshlrev_b32_e32 v30, 16, v14
	v_and_b32_e32 v14, 0xffff0000, v14
	v_fmac_f32_e32 v30, v22, v3
	v_fmac_f32_e32 v14, v23, v8
	v_add_f32_e32 v3, 1.0, v27
	v_mul_f32_e32 v8, 0xbfb8aa3b, v24
	v_rcp_f32_e32 v3, v3
	v_exp_f32_e32 v8, v8
	v_lshlrev_b32_e32 v28, 16, v10
	v_and_b32_e32 v10, 0xffff0000, v10
	v_lshlrev_b32_e32 v32, 16, v16
	v_and_b32_e32 v16, 0xffff0000, v16
	v_fmac_f32_e32 v16, v3, v10
	v_add_f32_e32 v3, 1.0, v6
	v_add_f32_e32 v6, 1.0, v8
	v_mul_f32_e32 v8, 0xbfb8aa3b, v25
	v_exp_f32_e32 v8, v8
	v_rcp_f32_e32 v6, v6
	v_rcp_f32_e32 v3, v3
	v_lshlrev_b32_e32 v29, 16, v11
	v_add_f32_e32 v8, 1.0, v8
	v_rcp_f32_e32 v8, v8
	v_and_b32_e32 v11, 0xffff0000, v11
	v_lshlrev_b32_e32 v33, 16, v17
	v_and_b32_e32 v17, 0xffff0000, v17
	v_lshlrev_b32_e32 v21, 16, v9
	v_and_b32_e32 v9, 0xffff0000, v9
	v_lshlrev_b32_e32 v31, 16, v15
	v_and_b32_e32 v15, 0xffff0000, v15
	v_fmac_f32_e32 v17, v8, v11
	v_lshlrev_b64 v[10:11], 1, v[18:19]
	v_fmac_f32_e32 v33, v6, v29
	v_fmac_f32_e32 v15, v7, v9
	v_lshl_add_u64 v[6:7], s[24:25], 0, v[10:11]
	v_lshl_add_u64 v[10:11], s[16:17], 0, v[10:11]
	v_fmac_f32_e32 v32, v26, v28
	v_fmac_f32_e32 v31, v3, v21
	v_cvt_pk_bf16_f32 v3, v30, v14
	v_cvt_pk_bf16_f32 v24, v31, v15
	v_cvt_pk_bf16_f32 v25, v32, v16
	v_cvt_pk_bf16_f32 v26, v33, v17
	global_load_dwordx4 v[6:9], v[6:7], off
	v_pk_mul_f32 v[18:19], v[54:55], v[20:21] op_sel_hi:[1,0]
	global_load_dwordx4 v[14:17], v[10:11], off
	v_mul_f32_e32 v19, 0xbfb8aa3b, v19
	v_exp_f32_e32 v19, v19
	v_pk_mul_f32 v[10:11], v[56:57], v[20:21] op_sel_hi:[1,0]
	v_pk_mul_f32 v[22:23], v[52:53], v[20:21] op_sel_hi:[1,0]
	v_pk_mul_f32 v[20:21], v[50:51], v[20:21] op_sel_hi:[1,0]
	v_mul_f32_e32 v18, 0xbfb8aa3b, v18
	v_add_f32_e32 v19, 1.0, v19
	v_mul_f32_e32 v21, 0xbfb8aa3b, v21
	v_exp_f32_e32 v18, v18
	v_rcp_f32_e32 v19, v19
	v_exp_f32_e32 v21, v21
	v_mul_f32_e32 v10, 0xbfb8aa3b, v10
	v_add_f32_e32 v18, 1.0, v18
	v_rcp_f32_e32 v18, v18
	v_exp_f32_e32 v10, v10
	v_mul_f32_e32 v20, 0xbfb8aa3b, v20
	v_exp_f32_e32 v20, v20
	s_waitcnt vmcnt(1)
; __device__ __forceinline__ float sigm(float x) { return __builtin_amdgcn_rcpf(1.0f + __builtin_amdgcn_exp2f(-1.4426950408889634f * x)); }
; __device__ __forceinline__ u32x4 pack8(const f32x4& v0, const f32x4& v1) { u32x4 w; w.x = cvt_pk_bf16(v0[0], v0[1]); w.y = cvt_pk_bf16(v0[2], v0[3]); w.z = cvt_pk_bf16(v1[0], v1[1]); w.w = cvt_pk_bf16(v1[2], v1[3]); return w; }
; __device__ __forceinline__ void unpack8(const u32x4& w, f32x4& v0, f32x4& v1) { v0[0] = bf_lo(w.x); v0[1] = bf_hi(w.x); v0[2] = bf_lo(w.y); v0[3] = bf_hi(w.y); v1[0] = bf_lo(w.z); v1[1] = bf_hi(w.z); v1[2] = bf_lo(w.w); v1[3] = bf_hi(w.w); }
; __device__ __forceinline__ void store_rows_bf16(bf16_t* O, size_t ldc, int r0, int c0, int fr, int fq, u32x4 w0, u32x4 w1) {
;     const bool h = fr & 8; const u32x4 recv = xor8_16B(h ? w0 : w1);
;     const u32x4 d1 = h ? recv : w0, d2 = h ? w1 : recv;
;     const int lane = fr + 16 * fq, src = ((lane >> 3) + 8 * ((lane >> 2) & 1) + 16 * (lane & 3)) * 4;
;     const u32x4 e1 = bperm_16B(src, d1), e2 = bperm_16B(src, d2);
;     bf16_t* p = O + (size_t)(r0 + (lane >> 3)) * ldc + c0 + 8 * (lane & 7);
;     *(u32x4*)p = e1; *(u32x4*)(p + 8 * ldc) = e2;
;     __device__ __forceinline__ void operator()(const f32x4 (&acc)[2][2][4][2], const Unit& u, int wr, int wc, int fr, int fq) const {
;     ...
;             for (int m = 0; m < 4; ++m) { const int row = row0 + ai * HALF + m * 16; const float sq = sq_next; u32x4 wx[2];
;                 if (!(ai == 1 && m == 3)) sq_next = ssq[row0 + (m == 3 ? HALF : ai * HALF + (m + 1) * 16)];
;                 const float rstd = rsqrtf(sq * (1.0f / 1024.0f) + 1e-6f);
; #pragma unroll
;                 for (int bj = 0; bj < 2; ++bj) { const int ct = wc * 64 + bj * 32 + 8 * fq; f32x4 v0 = acc[ai][bj][m][0] * rstd, v1 = acc[ai][bj][m][1] * rstd;
;                     const size_t o = (size_t)row * 1024 + u.pn * BM + ct; f32x4 e0, e1, r0, r1; unpack8(*(const u32x4*)(e + o), e0, e1); unpack8(*(const u32x4*)(x2 + o), r0, r1);
; #pragma unroll
;                     for (int i = 0; i < 4; ++i) { v0[i] = r0[i] + sigm(v0[i]) * e0[i]; v1[i] = r1[i] + sigm(v1[i]) * e1[i]; }
;                     wx[bj] = pack8(v0, v1); }
;                 store_rows_bf16(x3, 1024, u.pm * BM + wr * 64 + ai * HALF + m * 16, u.pn * BM + wc * 64, fr, fq, wx[0], wx[1]); }
	v_lshlrev_b32_e32 v27, 16, v6
	v_and_b32_e32 v6, 0xffff0000, v6
	s_waitcnt vmcnt(0)
	v_lshlrev_b32_e32 v31, 16, v14
	v_and_b32_e32 v14, 0xffff0000, v14
	v_fmac_f32_e32 v14, v19, v6
	v_add_f32_e32 v6, 1.0, v21
	v_rcp_f32_e32 v6, v6
	v_lshlrev_b32_e32 v29, 16, v8
	v_and_b32_e32 v8, 0xffff0000, v8
	v_lshlrev_b32_e32 v33, 16, v16
	v_and_b32_e32 v16, 0xffff0000, v16
	v_fmac_f32_e32 v31, v18, v27
	v_mul_f32_e32 v18, 0xbfb8aa3b, v22
	v_fmac_f32_e32 v16, v6, v8
	v_add_f32_e32 v6, 1.0, v10
	v_mul_f32_e32 v10, 0xbfb8aa3b, v11
	v_mul_f32_e32 v11, 0xbfb8aa3b, v23
	v_exp_f32_e32 v18, v18
	v_exp_f32_e32 v10, v10
	v_exp_f32_e32 v11, v11
	v_add_f32_e32 v20, 1.0, v20
	v_add_f32_e32 v8, 1.0, v18
	v_add_f32_e32 v10, 1.0, v10
	v_add_f32_e32 v11, 1.0, v11
	v_rcp_f32_e32 v20, v20
	v_rcp_f32_e32 v6, v6
	v_rcp_f32_e32 v8, v8
	v_rcp_f32_e32 v10, v10
	v_rcp_f32_e32 v11, v11
	v_lshlrev_b32_e32 v28, 16, v7
	v_and_b32_e32 v7, 0xffff0000, v7
	v_lshlrev_b32_e32 v30, 16, v9
	v_and_b32_e32 v9, 0xffff0000, v9
	v_lshlrev_b32_e32 v32, 16, v15
	v_and_b32_e32 v15, 0xffff0000, v15
	v_lshlrev_b32_e32 v50, 16, v17
	v_and_b32_e32 v17, 0xffff0000, v17
	v_fmac_f32_e32 v33, v20, v29
	v_fmac_f32_e32 v32, v6, v28
	v_fmac_f32_e32 v50, v8, v30
	v_fmac_f32_e32 v15, v10, v7
	v_fmac_f32_e32 v17, v11, v9
	v_cvt_pk_bf16_f32 v6, v31, v14
	v_cvt_pk_bf16_f32 v7, v32, v15
	v_cvt_pk_bf16_f32 v8, v33, v16
	v_cvt_pk_bf16_f32 v9, v50, v17
	s_nop 0
	v_cndmask_b32_e64 v10, v26, v9, s[4:5]
	v_cndmask_b32_e64 v11, v25, v8, s[4:5]
	v_cndmask_b32_e64 v14, v24, v7, s[4:5]
	v_cndmask_b32_e64 v15, v3, v6, s[4:5]
	v_mov_b32_dpp v10, v10 row_ror:8 row_mask:0xf bank_mask:0xf
	v_mov_b32_dpp v11, v11 row_ror:8 row_mask:0xf bank_mask:0xf
	v_mov_b32_dpp v14, v14 row_ror:8 row_mask:0xf bank_mask:0xf
	v_mov_b32_dpp v15, v15 row_ror:8 row_mask:0xf bank_mask:0xf
	s_waitcnt lgkmcnt(0)
	v_cndmask_b32_e64 v16, v10, v26, s[4:5]
	s_waitcnt lgkmcnt(0)
	v_cndmask_b32_e64 v17, v11, v25, s[4:5]
	v_cndmask_b32_e64 v10, v9, v10, s[4:5]
	s_waitcnt lgkmcnt(0)
	v_cndmask_b32_e64 v18, v14, v24, s[4:5]
	s_waitcnt lgkmcnt(0)
	v_cndmask_b32_e64 v3, v15, v3, s[4:5]
	v_cndmask_b32_e64 v11, v8, v11, s[4:5]
	ds_bpermute_b32 v8, v196, v17
	ds_bpermute_b32 v17, v196, v10
	v_add_u32_e32 v10, 0xa0, v2
	v_cndmask_b32_e64 v19, v7, v14, s[4:5]
	v_cndmask_b32_e64 v14, v6, v15, s[4:5]
	ds_bpermute_b32 v6, v196, v3
	ds_bpermute_b32 v7, v196, v18
	ds_bpermute_b32 v9, v196, v16
	ds_bpermute_b32 v16, v196, v11
	v_ashrrev_i32_e32 v11, 31, v10
	v_lshlrev_b64 v[10:11], 11, v[10:11]
	ds_bpermute_b32 v14, v196, v14
	ds_bpermute_b32 v15, v196, v19
	v_lshl_add_u64 v[10:11], s[22:23], 0, v[10:11]
	v_lshl_add_u64 v[10:11], v[10:11], 0, s[46:47]
	v_lshl_add_u64 v[10:11], v[10:11], 0, v[170:171]
	s_waitcnt lgkmcnt(3)
	global_store_dwordx4 v[10:11], v[6:9], off
	v_fmamk_f32 v3, v13, 0x3a800000, v202
	v_mul_f32_e32 v13, 0x4b800000, v3
	v_add_co_u32_e32 v6, vcc, s55, v10
	v_add_u32_e32 v2, 0xb0, v2
	s_nop 0
	v_addc_co_u32_e32 v7, vcc, 0, v11, vcc
	s_waitcnt lgkmcnt(0)
	global_store_dwordx4 v[6:7], v[14:17], off
	v_cmp_gt_f32_e32 vcc, s75, v3
	s_nop 0
	v_lshl_add_u64 v[14:15], v[4:5], 0, s[42:43]
	v_or_b32_e32 v4, v14, v172
	v_mov_b32_e32 v5, v15
	v_lshlrev_b64 v[8:9], 1, v[4:5]
	v_lshl_add_u64 v[4:5], s[24:25], 0, v[8:9]
	v_lshl_add_u64 v[8:9], s[16:17], 0, v[8:9]
	global_load_dwordx4 v[4:7], v[4:5], off
	v_cndmask_b32_e32 v3, v3, v13, vcc
	global_load_dwordx4 v[8:11], v[8:9], off
	v_rsq_f32_e32 v3, v3
	v_or_b32_e32 v14, v14, v174
	v_mul_f32_e32 v13, 0x45800000, v3
	v_cndmask_b32_e32 v16, v3, v13, vcc
	v_pk_mul_f32 v[20:21], v[46:47], v[16:17] op_sel_hi:[1,0]
	v_pk_mul_f32 v[24:25], v[42:43], v[16:17] op_sel_hi:[1,0]
	v_mul_f32_e32 v20, 0xbfb8aa3b, v20
	v_exp_f32_e32 v20, v20
	v_mul_f32_e32 v24, 0xbfb8aa3b, v24
	v_mul_f32_e32 v21, 0xbfb8aa3b, v21
	v_exp_f32_e32 v24, v24
	v_exp_f32_e32 v21, v21
	v_add_f32_e32 v20, 1.0, v20
	v_mul_f32_e32 v25, 0xbfb8aa3b, v25
	v_rcp_f32_e32 v20, v20
	v_exp_f32_e32 v25, v25
	v_add_f32_e32 v24, 1.0, v24
	v_add_f32_e32 v21, 1.0, v21
	v_rcp_f32_e32 v24, v24
	v_rcp_f32_e32 v21, v21
	v_pk_mul_f32 v[18:19], v[48:49], v[16:17] op_sel_hi:[1,0]
	v_pk_mul_f32 v[22:23], v[44:45], v[16:17] op_sel_hi:[1,0]
	s_waitcnt vmcnt(1)
	v_lshlrev_b32_e32 v3, 16, v4
	v_and_b32_e32 v4, 0xffff0000, v4
	s_waitcnt vmcnt(0)
; __device__ __forceinline__ float sigm(float x) { return __builtin_amdgcn_rcpf(1.0f + __builtin_amdgcn_exp2f(-1.4426950408889634f * x)); }
; __device__ __forceinline__ u32x4 pack8(const f32x4& v0, const f32x4& v1) { u32x4 w; w.x = cvt_pk_bf16(v0[0], v0[1]); w.y = cvt_pk_bf16(v0[2], v0[3]); w.z = cvt_pk_bf16(v1[0], v1[1]); w.w = cvt_pk_bf16(v1[2], v1[3]); return w; }
; __device__ __forceinline__ void unpack8(const u32x4& w, f32x4& v0, f32x4& v1) { v0[0] = bf_lo(w.x); v0[1] = bf_hi(w.x); v0[2] = bf_lo(w.y); v0[3] = bf_hi(w.y); v1[0] = bf_lo(w.z); v1[1] = bf_hi(w.z); v1[2] = bf_lo(w.w); v1[3] = bf_hi(w.w); }
; __device__ __forceinline__ void store_rows_bf16(bf16_t* O, size_t ldc, int r0, int c0, int fr, int fq, u32x4 w0, u32x4 w1) {
;     const bool h = fr & 8; const u32x4 recv = xor8_16B(h ? w0 : w1);
;     const u32x4 d1 = h ? recv : w0, d2 = h ? w1 : recv;
;     const int lane = fr + 16 * fq, src = ((lane >> 3) + 8 * ((lane >> 2) & 1) + 16 * (lane & 3)) * 4;
;     const u32x4 e1 = bperm_16B(src, d1), e2 = bperm_16B(src, d2);
;     bf16_t* p = O + (size_t)(r0 + (lane >> 3)) * ldc + c0 + 8 * (lane & 7);
;     *(u32x4*)p = e1; *(u32x4*)(p + 8 * ldc) = e2;
;     __device__ __forceinline__ void operator()(const f32x4 (&acc)[2][2][4][2], const Unit& u, int wr, int wc, int fr, int fq) const {
;     ...
;             for (int m = 0; m < 4; ++m) { const int row = row0 + ai * HALF + m * 16; const float sq = sq_next; u32x4 wx[2];
;                 if (!(ai == 1 && m == 3)) sq_next = ssq[row0 + (m == 3 ? HALF : ai * HALF + (m + 1) * 16)];
;                 const float rstd = rsqrtf(sq * (1.0f / 1024.0f) + 1e-6f);
; #pragma unroll
;                 for (int bj = 0; bj < 2; ++bj) { const int ct = wc * 64 + bj * 32 + 8 * fq; f32x4 v0 = acc[ai][bj][m][0] * rstd, v1 = acc[ai][bj][m][1] * rstd;
;                     const size_t o = (size_t)row * 1024 + u.pn * BM + ct; f32x4 e0, e1, r0, r1; unpack8(*(const u32x4*)(e + o), e0, e1); unpack8(*(const u32x4*)(x2 + o), r0, r1);
; #pragma unroll
;                     for (int i = 0; i < 4; ++i) { v0[i] = r0[i] + sigm(v0[i]) * e0[i]; v1[i] = r1[i] + sigm(v1[i]) * e1[i]; }
;                     wx[bj] = pack8(v0, v1); }
;                 store_rows_bf16(x3, 1024, u.pm * BM + wr * 64 + ai * HALF + m * 16, u.pn * BM + wc * 64, fr, fq, wx[0], wx[1]); }
	v_lshlrev_b32_e32 v27, 16, v8
	v_fmac_f32_e32 v27, v20, v3
	v_add_f32_e32 v3, 1.0, v25
	v_lshlrev_b32_e32 v17, 16, v6
	v_and_b32_e32 v8, 0xffff0000, v8
	v_lshlrev_b32_e32 v29, 16, v10
	v_rcp_f32_e32 v3, v3
	v_fmac_f32_e32 v29, v24, v17
	v_fmac_f32_e32 v8, v21, v4
	v_mul_f32_e32 v4, 0xbfb8aa3b, v18
	v_mul_f32_e32 v17, 0xbfb8aa3b, v22
	v_exp_f32_e32 v4, v4
	v_exp_f32_e32 v17, v17
	v_and_b32_e32 v6, 0xffff0000, v6
	v_and_b32_e32 v10, 0xffff0000, v10
	v_fmac_f32_e32 v10, v3, v6
	v_mul_f32_e32 v6, 0xbfb8aa3b, v19
	v_exp_f32_e32 v6, v6
	v_add_f32_e32 v3, 1.0, v4
	v_add_f32_e32 v4, 1.0, v17
	v_mul_f32_e32 v17, 0xbfb8aa3b, v23
	v_exp_f32_e32 v17, v17
	v_add_f32_e32 v6, 1.0, v6
	v_rcp_f32_e32 v6, v6
	v_rcp_f32_e32 v3, v3
	v_add_f32_e32 v17, 1.0, v17
	v_rcp_f32_e32 v4, v4
	v_rcp_f32_e32 v17, v17
	v_lshlrev_b32_e32 v13, 16, v5
	v_and_b32_e32 v5, 0xffff0000, v5
	v_lshlrev_b32_e32 v28, 16, v9
	v_and_b32_e32 v9, 0xffff0000, v9
	v_fmac_f32_e32 v9, v6, v5
	v_lshlrev_b32_e32 v26, 16, v7
	v_and_b32_e32 v7, 0xffff0000, v7
	v_lshlrev_b32_e32 v30, 16, v11
	v_and_b32_e32 v11, 0xffff0000, v11
	v_fmac_f32_e32 v28, v3, v13
	v_cvt_pk_bf16_f32 v3, v27, v8
	v_cvt_pk_bf16_f32 v13, v28, v9
	v_lshlrev_b64 v[8:9], 1, v[14:15]
	v_fmac_f32_e32 v30, v4, v26
	v_fmac_f32_e32 v11, v17, v7
	v_lshl_add_u64 v[4:5], s[24:25], 0, v[8:9]
	v_lshl_add_u64 v[8:9], s[16:17], 0, v[8:9]
	v_cvt_pk_bf16_f32 v22, v29, v10
	v_cvt_pk_bf16_f32 v23, v30, v11
	global_load_dwordx4 v[4:7], v[4:5], off
	v_pk_mul_f32 v[18:19], v[38:39], v[16:17] op_sel_hi:[1,0]
	global_load_dwordx4 v[8:11], v[8:9], off
	v_mul_f32_e32 v19, 0xbfb8aa3b, v19
	v_exp_f32_e32 v19, v19
	v_pk_mul_f32 v[14:15], v[40:41], v[16:17] op_sel_hi:[1,0]
	v_pk_mul_f32 v[20:21], v[36:37], v[16:17] op_sel_hi:[1,0]
	v_pk_mul_f32 v[16:17], v[34:35], v[16:17] op_sel_hi:[1,0]
	v_add_f32_e32 v19, 1.0, v19
	v_mul_f32_e32 v17, 0xbfb8aa3b, v17
	v_mul_f32_e32 v16, 0xbfb8aa3b, v16
	v_rcp_f32_e32 v19, v19
	v_exp_f32_e32 v17, v17
	v_exp_f32_e32 v16, v16
	v_mul_f32_e32 v14, 0xbfb8aa3b, v14
	v_exp_f32_e32 v14, v14
	v_mul_f32_e32 v18, 0xbfb8aa3b, v18
	v_add_f32_e32 v16, 1.0, v16
	v_rcp_f32_e32 v16, v16
	v_exp_f32_e32 v18, v18
	s_waitcnt vmcnt(1)
	v_lshlrev_b32_e32 v24, 16, v4
	v_and_b32_e32 v4, 0xffff0000, v4
	s_waitcnt vmcnt(0)
	v_lshlrev_b32_e32 v28, 16, v8
	v_and_b32_e32 v8, 0xffff0000, v8
	v_fmac_f32_e32 v8, v19, v4
	v_add_f32_e32 v4, 1.0, v17
	v_rcp_f32_e32 v4, v4
	v_lshlrev_b32_e32 v26, 16, v6
	v_and_b32_e32 v6, 0xffff0000, v6
	v_lshlrev_b32_e32 v30, 16, v10
	v_and_b32_e32 v10, 0xffff0000, v10
	v_fmac_f32_e32 v10, v4, v6
	v_add_f32_e32 v4, 1.0, v14
	v_mul_f32_e32 v14, 0xbfb8aa3b, v15
	v_mul_f32_e32 v15, 0xbfb8aa3b, v21
	v_fmac_f32_e32 v30, v16, v26
	v_mul_f32_e32 v16, 0xbfb8aa3b, v20
	v_exp_f32_e32 v14, v14
	v_exp_f32_e32 v15, v15
	v_exp_f32_e32 v16, v16
	v_add_f32_e32 v18, 1.0, v18
	v_add_f32_e32 v14, 1.0, v14
	v_add_f32_e32 v15, 1.0, v15
	v_add_f32_e32 v6, 1.0, v16
	v_rcp_f32_e32 v14, v14
	v_rcp_f32_e32 v15, v15
	v_rcp_f32_e32 v18, v18
	v_rcp_f32_e32 v4, v4
	v_rcp_f32_e32 v6, v6
	v_lshlrev_b32_e32 v25, 16, v5
	v_and_b32_e32 v5, 0xffff0000, v5
	v_lshlrev_b32_e32 v27, 16, v7
	v_and_b32_e32 v7, 0xffff0000, v7
	v_lshlrev_b32_e32 v29, 16, v9
	v_and_b32_e32 v9, 0xffff0000, v9
	v_lshlrev_b32_e32 v31, 16, v11
	v_and_b32_e32 v11, 0xffff0000, v11
	v_fmac_f32_e32 v9, v14, v5
	v_fmac_f32_e32 v11, v15, v7
	v_fmac_f32_e32 v28, v18, v24
	v_fmac_f32_e32 v29, v4, v25
	v_fmac_f32_e32 v31, v6, v27
	v_cvt_pk_bf16_f32 v4, v28, v8
	v_cvt_pk_bf16_f32 v5, v29, v9
	v_cvt_pk_bf16_f32 v6, v30, v10
	v_cvt_pk_bf16_f32 v7, v31, v11
	s_nop 0
	v_cndmask_b32_e64 v8, v23, v7, s[4:5]
	v_cndmask_b32_e64 v9, v22, v6, s[4:5]
	v_cndmask_b32_e64 v10, v13, v5, s[4:5]
	v_cndmask_b32_e64 v11, v3, v4, s[4:5]
	v_mov_b32_dpp v8, v8 row_ror:8 row_mask:0xf bank_mask:0xf
	v_mov_b32_dpp v9, v9 row_ror:8 row_mask:0xf bank_mask:0xf
	v_mov_b32_dpp v10, v10 row_ror:8 row_mask:0xf bank_mask:0xf
	v_mov_b32_dpp v11, v11 row_ror:8 row_mask:0xf bank_mask:0xf
	s_waitcnt lgkmcnt(0)
	v_cndmask_b32_e64 v12, v8, v23, s[4:5]
	s_waitcnt lgkmcnt(0)
	v_cndmask_b32_e64 v14, v9, v22, s[4:5]
	s_waitcnt lgkmcnt(0)
	v_cndmask_b32_e64 v13, v10, v13, s[4:5]
	s_waitcnt lgkmcnt(0)
	v_cndmask_b32_e64 v3, v11, v3, s[4:5]
	v_cndmask_b32_e64 v15, v7, v8, s[4:5]
	v_cndmask_b32_e64 v16, v6, v9, s[4:5]
	v_cndmask_b32_e64 v9, v5, v10, s[4:5]
	v_cndmask_b32_e64 v8, v4, v11, s[4:5]
	ds_bpermute_b32 v4, v196, v3
	ds_bpermute_b32 v5, v196, v13
	ds_bpermute_b32 v6, v196, v14
	ds_bpermute_b32 v7, v196, v12
	v_ashrrev_i32_e32 v3, 31, v2
	v_lshlrev_b64 v[2:3], 11, v[2:3]
	v_lshl_add_u64 v[2:3], s[22:23], 0, v[2:3]
	ds_bpermute_b32 v8, v196, v8
	ds_bpermute_b32 v9, v196, v9
	ds_bpermute_b32 v10, v196, v16
	ds_bpermute_b32 v11, v196, v15
	v_lshl_add_u64 v[2:3], v[2:3], 0, s[46:47]
	v_lshl_add_u64 v[2:3], v[2:3], 0, v[170:171]
	s_waitcnt lgkmcnt(4)
	global_store_dwordx4 v[2:3], v[4:7], off
	v_add_co_u32_e32 v2, vcc, 0x4000, v2
	s_nop 1
	v_addc_co_u32_e32 v3, vcc, 0, v3, vcc
	s_and_b64 vcc, exec, s[6:7]
	s_mov_b64 s[6:7], -1
	s_waitcnt lgkmcnt(0)
	global_store_dwordx4 v[2:3], v[8:11], off
	s_cbranch_vccnz .LBB0_1612
	s_andn2_b64 vcc, exec, s[20:21]
	s_cbranch_vccnz .LBB0_1611
	s_barrier
	s_branch .LBB0_1611
